# speedup vs baseline: 1.0192x; 1.0125x over previous
.LBB7_11:
	s_mov_b64 s[26:27], 0x80
	s_and_b32 s22, s20, 3
	s_add_i32 m0, s43, 0x18000
	v_lshl_add_u64 v[8:9], v[8:9], 0, s[26:27]
	s_lshl_b32 s48, s21, 6
	s_lshl_b32 s21, s21, 13
	s_lshl_b32 s23, s22, 12
	s_waitcnt vmcnt(4)
	s_barrier
	global_load_lds_dwordx4 v[8:9], off
	v_lshl_add_u64 v[6:7], v[6:7], 0, s[26:27]
	s_add_i32 m0, s43, 0x1a000
	s_add_i32 s49, s43, 0x8000
	s_add_i32 s50, s43, 0xa000
	global_load_lds_dwordx4 v[6:7], off
	v_lshl_add_u64 v[4:5], v[4:5], 0, s[26:27]
	s_mov_b32 m0, s49
	s_add_u32 s0, s30, 0xc080
	global_load_lds_dwordx4 v[4:5], off
	v_lshl_add_u64 v[2:3], v[2:3], 0, s[26:27]
	s_mov_b32 m0, s50
	s_addc_u32 s1, s31, 0
	global_load_lds_dwordx4 v[2:3], off
	s_add_i32 m0, s43, 0x1c000
	v_lshl_add_u64 v[2:3], s[0:1], 0, v[146:147]
	global_load_lds_dwordx4 v[2:3], off
	v_lshl_add_u64 v[2:3], s[0:1], 0, v[150:151]
	s_add_i32 m0, s43, 0x1e000
	s_lshl_b32 s53, s33, 2
	global_load_lds_dwordx4 v[2:3], off
	s_abs_i32 s54, s53
	v_cvt_f32_u32_e32 v6, s54
	v_and_b32_e32 v165, 15, v0
	v_and_b32_e32 v2, 48, v0
	v_lshlrev_b32_e32 v4, 2, v0
	v_rcp_iflag_f32_e32 v6, v6
	v_lshlrev_b32_e32 v5, 6, v0
	v_bfe_u32 v167, v0, 3, 3
	v_and_b32_e32 v0, 7, v0
	s_abs_i32 s57, s33
	v_lshlrev_b32_e32 v168, 4, v0
	v_add_lshl_u32 v169, v0, s10, 4
	v_mul_f32_e32 v0, 0x4f7ffffe, v6
	v_cvt_f32_u32_e32 v6, s57
	s_movk_i32 s0, 0x3c0
	s_mulk_i32 s20, 0x900
	v_cvt_u32_f32_e32 v0, v0
	v_rcp_iflag_f32_e32 v6, v6
	v_and_or_b32 v5, v5, s0, v2
	s_add_i32 s0, s20, 0
	v_lshl_or_b32 v3, v165, 6, v2
	v_and_b32_e32 v4, 32, v4
	s_add_i32 s0, s0, 0x20000
	v_bitop3_b32 v3, v3, s21, v4 bitop3:0xde
	v_bitop3_b32 v166, s23, v5, v4 bitop3:0xf6
	s_movk_i32 s1, 0x90
	v_mov_b32_e32 v4, s0
	v_mad_u32_u24 v5, v165, s1, v4
	v_mad_u32_u24 v4, v167, s1, v4
	v_readfirstlane_b32 s1, v0
	v_mul_f32_e32 v0, 0x4f7ffffe, v6
	v_cvt_u32_f32_e32 v0, v0
	s_sub_i32 s0, 0, s54
	s_mul_i32 s0, s0, s1
	s_mul_hi_u32 s0, s1, s0
	s_add_i32 s59, s1, s0
	s_sub_i32 s0, 0, s57
	v_readfirstlane_b32 s1, v0
	s_waitcnt vmcnt(6)
	s_mul_i32 s0, s0, s1
	v_add_u16_e32 v0, v1, v10
	s_mul_hi_u32 s0, s1, s0
	v_lshrrev_b16_e32 v0, 1, v0
	s_add_i32 s65, 0, 0x10000
	s_add_i32 s66, 0, 0x14000
	s_mov_b32 s23, 0x20000
	s_lshl_b32 s51, s22, 6
	s_waitcnt lgkmcnt(0)
	s_ashr_i32 s52, s11, 31
	s_lshl_b32 s22, s10, 17
	s_and_b32 s21, s9, 0xffff
	s_mov_b32 s20, s8
	s_lshl_b32 s55, s10, 5
	s_mul_i32 s56, s10, 48
	s_bfe_i32 s58, s33, 0x1001c
	s_ashr_i32 s60, s33, 31
	s_add_i32 s61, s1, s0
	s_mul_i32 s62, s10, 0xc0
	s_mul_i32 s63, s10, 0x60
	s_lshl_b32 s64, s10, 4
	v_add_lshl_u32 v152, v11, v0, 1
	v_mov_b32_e32 v153, v147
	v_add_lshl_u32 v154, v12, v0, 1
	v_mov_b32_e32 v155, v147
	v_mov_b64_e32 v[156:157], s[6:7]
	v_add_u32_e32 v170, s65, v166
	v_add_u32_e32 v171, 0, v3
	v_add_u32_e32 v172, s66, v166
	v_add_u32_e32 v173, v5, v2
	v_add_u32_e32 v174, v4, v168
	s_barrier
	s_cmpk_gt_u32 s36, 0xff
	s_cbranch_scc0 .Lprio7_done
	s_setprio 1
.Lprio7_done:
.LBB7_12:
	s_add_i32 s47, s47, 1
	s_mul_i32 s0, s47, s52
	s_mul_hi_u32 s1, s47, s11
	s_add_i32 s1, s1, s0
	s_mul_i32 s0, s47, s11
	s_add_u32 s0, s0, s2
	s_addc_u32 s1, s1, s39
	v_cmp_ge_i64_e32 vcc, s[0:1], v[156:157]
	s_and_b64 s[6:7], exec, vcc
	s_mov_b64 vcc, s[6:7]
	s_cbranch_vccnz .LBB7_22
	s_ashr_i32 s8, s0, 31
	s_lshr_b32 s8, s8, 29
	s_add_i32 s34, s0, s8
	s_and_b32 s8, s34, -8
	s_sub_i32 s35, s0, s8
	s_cmp_ge_i32 s35, s38
	s_mov_b64 s[8:9], -1
	s_cbranch_scc0 .LBB7_15
	s_sub_i32 s8, s35, s38
	s_mul_i32 s8, s8, s37
	s_add_i32 s68, s8, s41
	s_mov_b64 s[8:9], 0

.LBB7_27:
	ds_read_b128 v[128:131], v170
	ds_read_b128 v[132:135], v170 offset:1024
	ds_read_b128 v[136:139], v170 offset:2048
	ds_read_b128 v[140:143], v170 offset:3072
	s_add_u32 s30, s28, 0xfffd0080
	s_addc_u32 s31, s29, -1
	s_cmp_eq_u32 s73, 8
	s_cselect_b32 s35, s9, s31
	s_cselect_b32 s34, s8, s30
	s_cselect_b32 s31, s1, s72
	s_cselect_b32 s30, s0, s71
	v_lshl_add_u64 v[162:163], s[28:29], 0, v[152:153]
	s_add_i32 m0, s43, 0xc000
	ds_read_b128 v[158:161], v171
	ds_read_b128 v[176:179], v171 offset:1024
	ds_read_b128 v[180:183], v171 offset:2048
	ds_read_b128 v[184:187], v171 offset:3072
	ds_read_b128 v[188:191], v171 offset:4096
	ds_read_b128 v[192:195], v171 offset:5120
	ds_read_b128 v[196:199], v171 offset:6144
	ds_read_b128 v[200:203], v171 offset:7168
	global_load_lds_dwordx4 v[162:163], off
	v_lshl_add_u64 v[162:163], s[28:29], 0, v[154:155]
	s_add_i32 m0, s43, 0xe000
	s_nop 0
	global_load_lds_dwordx4 v[162:163], off
	s_waitcnt lgkmcnt(8)
	s_barrier
	s_waitcnt lgkmcnt(0)
	s_waitcnt lgkmcnt(0)
	v_mfma_f32_16x16x32_f16 v[124:127], v[128:131], v[158:161], v[124:127]
	v_mfma_f32_16x16x32_f16 v[120:123], v[136:139], v[158:161], v[120:123]
	v_mfma_f32_16x16x32_f16 v[108:111], v[128:131], v[180:183], v[108:111]
	v_mfma_f32_16x16x32_f16 v[104:107], v[136:139], v[180:183], v[104:107]
	v_mfma_f32_16x16x32_f16 v[96:99], v[128:131], v[188:191], v[96:99]
	v_mfma_f32_16x16x32_f16 v[88:91], v[136:139], v[188:191], v[88:91]
	v_mfma_f32_16x16x32_f16 v[80:83], v[128:131], v[196:199], v[80:83]
	v_mfma_f32_16x16x32_f16 v[72:75], v[136:139], v[196:199], v[72:75]
	v_mfma_f32_16x16x32_f16 v[124:127], v[132:135], v[176:179], v[124:127]
	v_mfma_f32_16x16x32_f16 v[120:123], v[140:143], v[176:179], v[120:123]
	v_mfma_f32_16x16x32_f16 v[108:111], v[132:135], v[184:187], v[108:111]
	v_mfma_f32_16x16x32_f16 v[104:107], v[140:143], v[184:187], v[104:107]
	v_mfma_f32_16x16x32_f16 v[96:99], v[132:135], v[192:195], v[96:99]
	v_mfma_f32_16x16x32_f16 v[88:91], v[140:143], v[192:195], v[88:91]
	v_mfma_f32_16x16x32_f16 v[80:83], v[132:135], v[200:203], v[80:83]
	v_mfma_f32_16x16x32_f16 v[72:75], v[140:143], v[200:203], v[72:75]
	s_barrier
	s_add_i32 s74, s65, s42
	v_lshl_add_u64 v[162:163], s[30:31], 0, v[146:147]
	s_mov_b32 m0, s74
	ds_read_b128 v[204:207], v172
	ds_read_b128 v[208:211], v172 offset:1024
	ds_read_b128 v[212:215], v172 offset:2048
	ds_read_b128 v[216:219], v172 offset:3072
	global_load_lds_dwordx4 v[162:163], off
	v_lshl_add_u64 v[220:221], s[30:31], 0, v[150:151]
	s_add_i32 m0, s74, 0x2000
	s_nop 0
	global_load_lds_dwordx4 v[220:221], off
	s_barrier
	s_waitcnt lgkmcnt(0)
	s_waitcnt lgkmcnt(0)
	v_mfma_f32_16x16x32_f16 v[116:119], v[204:207], v[158:161], v[116:119]
	v_mfma_f32_16x16x32_f16 v[112:115], v[212:215], v[158:161], v[112:115]
	v_mfma_f32_16x16x32_f16 v[100:103], v[204:207], v[180:183], v[100:103]
	v_mfma_f32_16x16x32_f16 v[92:95], v[212:215], v[180:183], v[92:95]
	v_mfma_f32_16x16x32_f16 v[84:87], v[204:207], v[188:191], v[84:87]
	v_mfma_f32_16x16x32_f16 v[76:79], v[212:215], v[188:191], v[76:79]
	v_mfma_f32_16x16x32_f16 v[68:71], v[204:207], v[196:199], v[68:71]
	v_mfma_f32_16x16x32_f16 v[64:67], v[212:215], v[196:199], v[64:67]
	v_mfma_f32_16x16x32_f16 v[116:119], v[208:211], v[176:179], v[116:119]
	v_mfma_f32_16x16x32_f16 v[112:115], v[216:219], v[176:179], v[112:115]
	v_mfma_f32_16x16x32_f16 v[100:103], v[208:211], v[184:187], v[100:103]
	v_mfma_f32_16x16x32_f16 v[92:95], v[216:219], v[184:187], v[92:95]
	v_mfma_f32_16x16x32_f16 v[84:87], v[208:211], v[192:195], v[84:87]
	v_mfma_f32_16x16x32_f16 v[76:79], v[216:219], v[192:195], v[76:79]
	v_mfma_f32_16x16x32_f16 v[68:71], v[208:211], v[200:203], v[68:71]
	v_mfma_f32_16x16x32_f16 v[64:67], v[216:219], v[200:203], v[64:67]
	s_mov_b32 m0, s43
	v_lshl_add_u64 v[222:223], s[34:35], 0, v[144:145]
	s_barrier
	ds_read_b128 v[158:161], v171 offset:16384
	ds_read_b128 v[176:179], v171 offset:17408
	ds_read_b128 v[180:183], v171 offset:18432
	ds_read_b128 v[184:187], v171 offset:19456
	ds_read_b128 v[188:191], v171 offset:20480
	ds_read_b128 v[192:195], v171 offset:21504
	ds_read_b128 v[196:199], v171 offset:22528
	ds_read_b128 v[200:203], v171 offset:23552
	global_load_lds_dwordx4 v[222:223], off
	v_lshl_add_u64 v[224:225], s[34:35], 0, v[148:149]
	s_mov_b32 m0, s44
	s_nop 0
	global_load_lds_dwordx4 v[224:225], off
	s_barrier
	s_waitcnt lgkmcnt(0)
	s_waitcnt lgkmcnt(0)
	v_mfma_f32_16x16x32_f16 v[60:63], v[128:131], v[158:161], v[60:63]
	v_mfma_f32_16x16x32_f16 v[56:59], v[136:139], v[158:161], v[56:59]
	v_mfma_f32_16x16x32_f16 v[48:51], v[128:131], v[180:183], v[48:51]
	v_mfma_f32_16x16x32_f16 v[40:43], v[136:139], v[180:183], v[40:43]
	v_mfma_f32_16x16x32_f16 v[32:35], v[128:131], v[188:191], v[32:35]
	v_mfma_f32_16x16x32_f16 v[24:27], v[136:139], v[188:191], v[24:27]
	v_mfma_f32_16x16x32_f16 v[16:19], v[128:131], v[196:199], v[16:19]
	v_mfma_f32_16x16x32_f16 v[8:11], v[136:139], v[196:199], v[8:11]
	v_mfma_f32_16x16x32_f16 v[60:63], v[132:135], v[176:179], v[60:63]
	v_mfma_f32_16x16x32_f16 v[56:59], v[140:143], v[176:179], v[56:59]
	v_mfma_f32_16x16x32_f16 v[48:51], v[132:135], v[184:187], v[48:51]
	v_mfma_f32_16x16x32_f16 v[40:43], v[140:143], v[184:187], v[40:43]
	v_mfma_f32_16x16x32_f16 v[32:35], v[132:135], v[192:195], v[32:35]
	v_mfma_f32_16x16x32_f16 v[24:27], v[140:143], v[192:195], v[24:27]
	v_mfma_f32_16x16x32_f16 v[16:19], v[132:135], v[200:203], v[16:19]
	v_mfma_f32_16x16x32_f16 v[8:11], v[140:143], v[200:203], v[8:11]
	s_barrier
	s_add_u32 s74, s30, 0xc000
	s_addc_u32 s75, s31, 0
	s_add_i32 s76, s66, s42
	v_lshl_add_u64 v[128:129], s[74:75], 0, v[146:147]
	s_mov_b32 m0, s76
	s_nop 0
	global_load_lds_dwordx4 v[128:129], off
	v_lshl_add_u64 v[128:129], s[74:75], 0, v[150:151]
	s_add_i32 m0, s76, 0x2000
	s_nop 0
	global_load_lds_dwordx4 v[128:129], off
	s_waitcnt vmcnt(6)
	s_barrier
	v_mfma_f32_16x16x32_f16 v[52:55], v[204:207], v[158:161], v[52:55]
	v_mfma_f32_16x16x32_f16 v[44:47], v[212:215], v[158:161], v[44:47]
	v_mfma_f32_16x16x32_f16 v[36:39], v[204:207], v[180:183], v[36:39]
	v_mfma_f32_16x16x32_f16 v[28:31], v[212:215], v[180:183], v[28:31]
	v_mfma_f32_16x16x32_f16 v[20:23], v[204:207], v[188:191], v[20:23]
	v_mfma_f32_16x16x32_f16 v[12:15], v[212:215], v[188:191], v[12:15]
	v_mfma_f32_16x16x32_f16 v[4:7], v[204:207], v[196:199], v[4:7]
	v_mfma_f32_16x16x32_f16 v[0:3], v[212:215], v[196:199], v[0:3]
	v_mfma_f32_16x16x32_f16 v[52:55], v[208:211], v[176:179], v[52:55]
	v_mfma_f32_16x16x32_f16 v[44:47], v[216:219], v[176:179], v[44:47]
	v_mfma_f32_16x16x32_f16 v[36:39], v[208:211], v[184:187], v[36:39]
	v_mfma_f32_16x16x32_f16 v[28:31], v[216:219], v[184:187], v[28:31]
	v_mfma_f32_16x16x32_f16 v[20:23], v[208:211], v[192:195], v[20:23]
	v_mfma_f32_16x16x32_f16 v[12:15], v[216:219], v[192:195], v[12:15]
	v_mfma_f32_16x16x32_f16 v[4:7], v[208:211], v[200:203], v[4:7]
	v_mfma_f32_16x16x32_f16 v[0:3], v[216:219], v[200:203], v[0:3]
	s_add_i32 s74, 0, 0x18000
	v_add_u32_e32 v140, s74, v166
	s_barrier
	ds_read_b128 v[128:131], v140
	ds_read_b128 v[132:135], v140 offset:1024
	ds_read_b128 v[136:139], v140 offset:2048
	ds_read_b128 v[140:143], v140 offset:3072
	s_add_u32 s34, s34, 0x30000
	s_addc_u32 s35, s35, 0
	s_mov_b32 m0, s45
	v_lshl_add_u64 v[204:205], s[34:35], 0, v[144:145]
	ds_read_b128 v[158:161], v171 offset:32768
	ds_read_b128 v[176:179], v171 offset:33792
	ds_read_b128 v[180:183], v171 offset:34816
	ds_read_b128 v[184:187], v171 offset:35840
	ds_read_b128 v[188:191], v171 offset:36864
	ds_read_b128 v[192:195], v171 offset:37888
	ds_read_b128 v[196:199], v171 offset:38912
	ds_read_b128 v[200:203], v171 offset:39936
	global_load_lds_dwordx4 v[204:205], off
	v_lshl_add_u64 v[204:205], s[34:35], 0, v[148:149]
	s_mov_b32 m0, s46
	s_nop 0
	global_load_lds_dwordx4 v[204:205], off
	s_waitcnt lgkmcnt(8)
	s_barrier
	s_waitcnt lgkmcnt(0)
	s_waitcnt lgkmcnt(0)
	v_mfma_f32_16x16x32_f16 v[124:127], v[128:131], v[158:161], v[124:127]
	v_mfma_f32_16x16x32_f16 v[120:123], v[136:139], v[158:161], v[120:123]
	v_mfma_f32_16x16x32_f16 v[108:111], v[128:131], v[180:183], v[108:111]
	v_mfma_f32_16x16x32_f16 v[104:107], v[136:139], v[180:183], v[104:107]
	v_mfma_f32_16x16x32_f16 v[96:99], v[128:131], v[188:191], v[96:99]
	v_mfma_f32_16x16x32_f16 v[88:91], v[136:139], v[188:191], v[88:91]
	v_mfma_f32_16x16x32_f16 v[80:83], v[128:131], v[196:199], v[80:83]
	v_mfma_f32_16x16x32_f16 v[72:75], v[136:139], v[196:199], v[72:75]
	v_mfma_f32_16x16x32_f16 v[124:127], v[132:135], v[176:179], v[124:127]
	v_mfma_f32_16x16x32_f16 v[120:123], v[140:143], v[176:179], v[120:123]
	v_mfma_f32_16x16x32_f16 v[108:111], v[132:135], v[184:187], v[108:111]
	v_mfma_f32_16x16x32_f16 v[104:107], v[140:143], v[184:187], v[104:107]
	v_mfma_f32_16x16x32_f16 v[96:99], v[132:135], v[192:195], v[96:99]
	v_mfma_f32_16x16x32_f16 v[88:91], v[140:143], v[192:195], v[88:91]
	v_mfma_f32_16x16x32_f16 v[80:83], v[132:135], v[200:203], v[80:83]
	v_mfma_f32_16x16x32_f16 v[72:75], v[140:143], v[200:203], v[72:75]
	s_barrier
	s_add_i32 s34, 0, 0x1c000
	s_add_i32 s35, s74, s42
	v_add_u32_e32 v175, s34, v166
	v_lshl_add_u64 v[162:163], v[162:163], 0, s[26:27]
	s_mov_b32 m0, s35
	ds_read_b128 v[204:207], v175
	ds_read_b128 v[208:211], v175 offset:1024
	ds_read_b128 v[212:215], v175 offset:2048
	ds_read_b128 v[216:219], v175 offset:3072
	global_load_lds_dwordx4 v[162:163], off
	v_lshl_add_u64 v[162:163], v[220:221], 0, s[26:27]
	s_add_i32 m0, s35, 0x2000
	s_nop 0
	global_load_lds_dwordx4 v[162:163], off
	s_barrier
	s_waitcnt lgkmcnt(0)
	s_waitcnt lgkmcnt(0)
	v_mfma_f32_16x16x32_f16 v[116:119], v[204:207], v[158:161], v[116:119]
	v_mfma_f32_16x16x32_f16 v[112:115], v[212:215], v[158:161], v[112:115]
	v_mfma_f32_16x16x32_f16 v[100:103], v[204:207], v[180:183], v[100:103]
	v_mfma_f32_16x16x32_f16 v[92:95], v[212:215], v[180:183], v[92:95]
	v_mfma_f32_16x16x32_f16 v[84:87], v[204:207], v[188:191], v[84:87]
	v_mfma_f32_16x16x32_f16 v[76:79], v[212:215], v[188:191], v[76:79]
	v_mfma_f32_16x16x32_f16 v[68:71], v[204:207], v[196:199], v[68:71]
	v_mfma_f32_16x16x32_f16 v[64:67], v[212:215], v[196:199], v[64:67]
	v_mfma_f32_16x16x32_f16 v[116:119], v[208:211], v[176:179], v[116:119]
	v_mfma_f32_16x16x32_f16 v[112:115], v[216:219], v[176:179], v[112:115]
	v_mfma_f32_16x16x32_f16 v[100:103], v[208:211], v[184:187], v[100:103]
	v_mfma_f32_16x16x32_f16 v[92:95], v[216:219], v[184:187], v[92:95]
	v_mfma_f32_16x16x32_f16 v[84:87], v[208:211], v[192:195], v[84:87]
	v_mfma_f32_16x16x32_f16 v[76:79], v[216:219], v[192:195], v[76:79]
	v_mfma_f32_16x16x32_f16 v[68:71], v[208:211], v[200:203], v[68:71]
	v_mfma_f32_16x16x32_f16 v[64:67], v[216:219], v[200:203], v[64:67]
	s_mov_b32 m0, s49
	v_lshl_add_u64 v[162:163], v[222:223], 0, s[26:27]
	s_barrier
	ds_read_b128 v[158:161], v171 offset:49152
	ds_read_b128 v[176:179], v171 offset:50176
	ds_read_b128 v[180:183], v171 offset:51200
	ds_read_b128 v[184:187], v171 offset:52224
	ds_read_b128 v[188:191], v171 offset:53248
	ds_read_b128 v[192:195], v171 offset:54272
	ds_read_b128 v[196:199], v171 offset:55296
	ds_read_b128 v[200:203], v171 offset:56320
	global_load_lds_dwordx4 v[162:163], off
	v_lshl_add_u64 v[162:163], v[224:225], 0, s[26:27]
	s_mov_b32 m0, s50
	s_nop 0
	global_load_lds_dwordx4 v[162:163], off
	s_barrier
	s_waitcnt lgkmcnt(0)
	s_waitcnt lgkmcnt(0)
	v_mfma_f32_16x16x32_f16 v[60:63], v[128:131], v[158:161], v[60:63]
	v_mfma_f32_16x16x32_f16 v[56:59], v[136:139], v[158:161], v[56:59]
	v_mfma_f32_16x16x32_f16 v[48:51], v[128:131], v[180:183], v[48:51]
	v_mfma_f32_16x16x32_f16 v[40:43], v[136:139], v[180:183], v[40:43]
	v_mfma_f32_16x16x32_f16 v[32:35], v[128:131], v[188:191], v[32:35]
	v_mfma_f32_16x16x32_f16 v[24:27], v[136:139], v[188:191], v[24:27]
	v_mfma_f32_16x16x32_f16 v[16:19], v[128:131], v[196:199], v[16:19]
	v_mfma_f32_16x16x32_f16 v[8:11], v[136:139], v[196:199], v[8:11]
	v_mfma_f32_16x16x32_f16 v[60:63], v[132:135], v[176:179], v[60:63]
	v_mfma_f32_16x16x32_f16 v[56:59], v[140:143], v[176:179], v[56:59]
	v_mfma_f32_16x16x32_f16 v[48:51], v[132:135], v[184:187], v[48:51]
	v_mfma_f32_16x16x32_f16 v[40:43], v[140:143], v[184:187], v[40:43]
	v_mfma_f32_16x16x32_f16 v[32:35], v[132:135], v[192:195], v[32:35]
	v_mfma_f32_16x16x32_f16 v[24:27], v[140:143], v[192:195], v[24:27]
	v_mfma_f32_16x16x32_f16 v[16:19], v[132:135], v[200:203], v[16:19]
	v_mfma_f32_16x16x32_f16 v[8:11], v[140:143], v[200:203], v[8:11]
	s_barrier
	s_add_u32 s30, s30, 0xc080
	s_addc_u32 s31, s31, 0
	s_add_i32 s34, s34, s42
	v_lshl_add_u64 v[128:129], s[30:31], 0, v[146:147]
	s_mov_b32 m0, s34
	s_nop 0
	global_load_lds_dwordx4 v[128:129], off
	v_lshl_add_u64 v[128:129], s[30:31], 0, v[150:151]
	s_add_i32 m0, s34, 0x2000
	s_nop 0
	global_load_lds_dwordx4 v[128:129], off
	s_waitcnt vmcnt(6)
	s_barrier
	v_mfma_f32_16x16x32_f16 v[52:55], v[204:207], v[158:161], v[52:55]
	v_mfma_f32_16x16x32_f16 v[44:47], v[212:215], v[158:161], v[44:47]
	v_mfma_f32_16x16x32_f16 v[36:39], v[204:207], v[180:183], v[36:39]
	v_mfma_f32_16x16x32_f16 v[28:31], v[212:215], v[180:183], v[28:31]
	v_mfma_f32_16x16x32_f16 v[20:23], v[204:207], v[188:191], v[20:23]
	v_mfma_f32_16x16x32_f16 v[12:15], v[212:215], v[188:191], v[12:15]
	v_mfma_f32_16x16x32_f16 v[4:7], v[204:207], v[196:199], v[4:7]
	v_mfma_f32_16x16x32_f16 v[0:3], v[212:215], v[196:199], v[0:3]
	v_mfma_f32_16x16x32_f16 v[52:55], v[208:211], v[176:179], v[52:55]
	v_mfma_f32_16x16x32_f16 v[44:47], v[216:219], v[176:179], v[44:47]
	v_mfma_f32_16x16x32_f16 v[36:39], v[208:211], v[184:187], v[36:39]
	v_mfma_f32_16x16x32_f16 v[28:31], v[216:219], v[184:187], v[28:31]
	v_mfma_f32_16x16x32_f16 v[20:23], v[208:211], v[192:195], v[20:23]
	v_mfma_f32_16x16x32_f16 v[12:15], v[216:219], v[192:195], v[12:15]
	v_mfma_f32_16x16x32_f16 v[4:7], v[208:211], v[200:203], v[4:7]
	v_mfma_f32_16x16x32_f16 v[0:3], v[216:219], v[200:203], v[0:3]
	s_add_i32 s73, s73, 2
	s_add_u32 s28, s28, 0x100
	s_addc_u32 s29, s29, 0
	s_add_u32 s71, s71, 0x100
	s_addc_u32 s72, s72, 0
	s_cmp_gt_u32 s73, 9
	s_barrier
	s_cbranch_scc0 .LBB7_27
	s_lshl_b32 s28, s70, 8
	s_add_i32 s28, s28, s48
	s_lshl_b32 s29, s67, 8
	s_or_b32 s29, s29, s51
	s_waitcnt vmcnt(6)
	v_pk_fma_f32 v[126:127], v[126:127], v[226:227], v[236:237] op_sel_hi:[1,0,1]
	v_pk_fma_f32 v[124:125], v[124:125], v[226:227], v[234:235] op_sel_hi:[1,0,1]
	v_pk_fma_f32 v[186:187], v[122:123], v[226:227], v[240:241] op_sel_hi:[1,0,1]
	v_pk_fma_f32 v[122:123], v[120:121], v[226:227], v[238:239] op_sel_hi:[1,0,1]
	v_cvt_pk_f16_f32 v120, v124, v125
	v_cvt_pk_f16_f32 v121, v126, v127
	v_cvt_pk_f16_f32 v122, v122, v123
	v_cvt_pk_f16_f32 v123, v186, v187
	ds_write_b128 v173, v[120:123]
	v_pk_fma_f32 v[118:119], v[118:119], v[226:227], v[244:245] op_sel_hi:[1,0,1]
	v_pk_fma_f32 v[116:117], v[116:117], v[226:227], v[242:243] op_sel_hi:[1,0,1]
	v_pk_fma_f32 v[120:121], v[114:115], v[226:227], v[248:249] op_sel_hi:[1,0,1]
	v_pk_fma_f32 v[114:115], v[112:113], v[226:227], v[246:247] op_sel_hi:[1,0,1]
	v_cvt_pk_f16_f32 v112, v116, v117
	v_cvt_pk_f16_f32 v113, v118, v119
	v_cvt_pk_f16_f32 v114, v114, v115
	v_cvt_pk_f16_f32 v115, v120, v121
	ds_write_b128 v173, v[112:115] offset:64
	v_or_b32_e32 v116, s28, v167
	ds_read_b128 v[112:115], v174
	v_mul_lo_u32 v116, v116, s10
	v_add_u32_e32 v120, s29, v116
	v_lshlrev_b32_e32 v121, 1, v120
	v_add_u32_e32 v122, v121, v168
	ds_read_b128 v[116:119], v174 offset:1152
	s_waitcnt lgkmcnt(0)
	buffer_store_dwordx4 v[112:115], v122, s[20:23], 0 offen nt
	v_pk_fma_f32 v[110:111], v[110:111], v[226:227], v[236:237] op_sel:[0,1,0]
	v_pk_fma_f32 v[108:109], v[108:109], v[226:227], v[234:235] op_sel:[0,1,0]
	v_pk_fma_f32 v[112:113], v[106:107], v[226:227], v[240:241] op_sel:[0,1,0]
	v_pk_fma_f32 v[106:107], v[104:105], v[226:227], v[238:239] op_sel:[0,1,0]
	v_cvt_pk_f16_f32 v104, v108, v109
	v_cvt_pk_f16_f32 v105, v110, v111
	v_cvt_pk_f16_f32 v106, v106, v107
	v_cvt_pk_f16_f32 v107, v112, v113
	ds_write_b128 v173, v[104:107]
	v_pk_fma_f32 v[102:103], v[102:103], v[226:227], v[244:245] op_sel:[0,1,0]
	v_pk_fma_f32 v[100:101], v[100:101], v[226:227], v[242:243] op_sel:[0,1,0]
	v_pk_fma_f32 v[104:105], v[94:95], v[226:227], v[248:249] op_sel:[0,1,0]
	v_pk_fma_f32 v[94:95], v[92:93], v[226:227], v[246:247] op_sel:[0,1,0]
	v_cvt_pk_f16_f32 v92, v100, v101
	v_cvt_pk_f16_f32 v93, v102, v103
	v_cvt_pk_f16_f32 v94, v94, v95
	v_cvt_pk_f16_f32 v95, v104, v105
	ds_write_b128 v173, v[92:95] offset:64
	ds_read_b128 v[92:95], v174
	ds_read_b128 v[100:103], v174 offset:1152
	v_add_u32_e32 v104, s55, v121
	v_add_u32_e32 v114, v121, v169
	v_add_u32_e32 v105, v104, v168
	buffer_store_dwordx4 v[116:119], v114, s[20:23], 0 offen nt
	s_waitcnt lgkmcnt(1)
	buffer_store_dwordx4 v[92:95], v105, s[20:23], 0 offen nt
	v_pk_fma_f32 v[86:87], v[86:87], v[228:229], v[244:245] op_sel_hi:[1,0,1]
	v_pk_fma_f32 v[84:85], v[84:85], v[228:229], v[242:243] op_sel_hi:[1,0,1]
	v_pk_fma_f32 v[92:93], v[98:99], v[228:229], v[236:237] op_sel_hi:[1,0,1]
	v_pk_fma_f32 v[94:95], v[96:97], v[228:229], v[234:235] op_sel_hi:[1,0,1]
	v_pk_fma_f32 v[96:97], v[90:91], v[228:229], v[240:241] op_sel_hi:[1,0,1]
	v_pk_fma_f32 v[90:91], v[88:89], v[228:229], v[238:239] op_sel_hi:[1,0,1]
	v_cvt_pk_f16_f32 v88, v94, v95
	v_cvt_pk_f16_f32 v89, v92, v93
	v_cvt_pk_f16_f32 v90, v90, v91
	v_cvt_pk_f16_f32 v91, v96, v97
	ds_write_b128 v173, v[88:91]
	v_pk_fma_f32 v[88:89], v[78:79], v[228:229], v[248:249] op_sel_hi:[1,0,1]
	v_pk_fma_f32 v[78:79], v[76:77], v[228:229], v[246:247] op_sel_hi:[1,0,1]
	v_cvt_pk_f16_f32 v76, v84, v85
	v_cvt_pk_f16_f32 v77, v86, v87
	v_cvt_pk_f16_f32 v78, v78, v79
	v_cvt_pk_f16_f32 v79, v88, v89
	ds_write_b128 v173, v[76:79] offset:64
	ds_read_b128 v[76:79], v174
	ds_read_b128 v[84:87], v174 offset:1152
	v_add_u32_e32 v88, s55, v104
	v_add_u32_e32 v105, v104, v169
	v_add_u32_e32 v89, v88, v168
	s_waitcnt lgkmcnt(4)
	buffer_store_dwordx4 v[100:103], v105, s[20:23], 0 offen nt
	s_waitcnt lgkmcnt(1)
	buffer_store_dwordx4 v[76:79], v89, s[20:23], 0 offen nt
	v_pk_fma_f32 v[70:71], v[70:71], v[228:229], v[244:245] op_sel:[0,1,0]
	v_pk_fma_f32 v[68:69], v[68:69], v[228:229], v[242:243] op_sel:[0,1,0]
	v_add_u32_e32 v76, v88, v169
	s_waitcnt lgkmcnt(0)
	buffer_store_dwordx4 v[84:87], v76, s[20:23], 0 offen nt
	v_pk_fma_f32 v[76:77], v[82:83], v[228:229], v[236:237] op_sel:[0,1,0]
	v_pk_fma_f32 v[78:79], v[80:81], v[228:229], v[234:235] op_sel:[0,1,0]
	v_pk_fma_f32 v[80:81], v[74:75], v[228:229], v[240:241] op_sel:[0,1,0]
	v_pk_fma_f32 v[74:75], v[72:73], v[228:229], v[238:239] op_sel:[0,1,0]
	v_cvt_pk_f16_f32 v72, v78, v79
	v_cvt_pk_f16_f32 v73, v76, v77
	v_cvt_pk_f16_f32 v74, v74, v75
	v_cvt_pk_f16_f32 v75, v80, v81
	ds_write_b128 v173, v[72:75]
	v_pk_fma_f32 v[72:73], v[66:67], v[228:229], v[248:249] op_sel:[0,1,0]
	v_pk_fma_f32 v[66:67], v[64:65], v[228:229], v[246:247] op_sel:[0,1,0]
	v_cvt_pk_f16_f32 v64, v68, v69
	v_cvt_pk_f16_f32 v65, v70, v71
	v_cvt_pk_f16_f32 v66, v66, v67
	v_cvt_pk_f16_f32 v67, v72, v73
	ds_write_b128 v173, v[64:67] offset:64
	ds_read_b128 v[64:67], v174
	ds_read_b128 v[68:71], v174 offset:1152
	v_add_u32_e32 v72, s56, v120
	v_lshlrev_b32_e32 v73, 1, v72
	v_add_u32_e32 v74, v73, v168
	s_waitcnt lgkmcnt(1)
	buffer_store_dwordx4 v[64:67], v74, s[20:23], 0 offen nt
	v_pk_fma_f32 v[62:63], v[62:63], v[230:231], v[236:237] op_sel_hi:[1,0,1]
	v_pk_fma_f32 v[60:61], v[60:61], v[230:231], v[234:235] op_sel_hi:[1,0,1]
	v_pk_fma_f32 v[64:65], v[58:59], v[230:231], v[240:241] op_sel_hi:[1,0,1]
	v_pk_fma_f32 v[58:59], v[56:57], v[230:231], v[238:239] op_sel_hi:[1,0,1]
	v_cvt_pk_f16_f32 v56, v60, v61
	v_cvt_pk_f16_f32 v57, v62, v63
	v_cvt_pk_f16_f32 v58, v58, v59
	v_cvt_pk_f16_f32 v59, v64, v65
	ds_write_b128 v173, v[56:59]
	v_pk_fma_f32 v[54:55], v[54:55], v[230:231], v[244:245] op_sel_hi:[1,0,1]
	v_pk_fma_f32 v[52:53], v[52:53], v[230:231], v[242:243] op_sel_hi:[1,0,1]
	v_pk_fma_f32 v[56:57], v[46:47], v[230:231], v[248:249] op_sel_hi:[1,0,1]
	v_pk_fma_f32 v[46:47], v[44:45], v[230:231], v[246:247] op_sel_hi:[1,0,1]
	v_cvt_pk_f16_f32 v44, v52, v53
	v_cvt_pk_f16_f32 v45, v54, v55
	v_cvt_pk_f16_f32 v46, v46, v47
	v_cvt_pk_f16_f32 v47, v56, v57
	ds_write_b128 v173, v[44:47] offset:64
	ds_read_b128 v[44:47], v174
	ds_read_b128 v[52:55], v174 offset:1152
	v_add_u32_e32 v56, s62, v88
	v_add_u32_e32 v66, v73, v169
	v_add_u32_e32 v57, v56, v168
	s_waitcnt lgkmcnt(4)
	buffer_store_dwordx4 v[68:71], v66, s[20:23], 0 offen nt
	s_waitcnt lgkmcnt(1)
	buffer_store_dwordx4 v[44:47], v57, s[20:23], 0 offen nt
	v_pk_fma_f32 v[38:39], v[38:39], v[230:231], v[244:245] op_sel:[0,1,0]
	v_pk_fma_f32 v[36:37], v[36:37], v[230:231], v[242:243] op_sel:[0,1,0]
	v_add_u32_e32 v44, v56, v169
	s_waitcnt lgkmcnt(0)
	buffer_store_dwordx4 v[52:55], v44, s[20:23], 0 offen nt
	v_pk_fma_f32 v[44:45], v[50:51], v[230:231], v[236:237] op_sel:[0,1,0]
	v_pk_fma_f32 v[46:47], v[48:49], v[230:231], v[234:235] op_sel:[0,1,0]
	v_pk_fma_f32 v[48:49], v[42:43], v[230:231], v[240:241] op_sel:[0,1,0]
	v_pk_fma_f32 v[42:43], v[40:41], v[230:231], v[238:239] op_sel:[0,1,0]
	v_cvt_pk_f16_f32 v40, v46, v47
	v_cvt_pk_f16_f32 v41, v44, v45
	v_cvt_pk_f16_f32 v42, v42, v43
	v_cvt_pk_f16_f32 v43, v48, v49
	ds_write_b128 v173, v[40:43]
	v_pk_fma_f32 v[40:41], v[30:31], v[230:231], v[248:249] op_sel:[0,1,0]
	v_pk_fma_f32 v[30:31], v[28:29], v[230:231], v[246:247] op_sel:[0,1,0]
	v_cvt_pk_f16_f32 v28, v36, v37
	v_cvt_pk_f16_f32 v29, v38, v39
	v_cvt_pk_f16_f32 v30, v30, v31
	v_cvt_pk_f16_f32 v31, v40, v41
	ds_write_b128 v173, v[28:31] offset:64
	ds_read_b128 v[28:31], v174
	ds_read_b128 v[36:39], v174 offset:1152
	v_add_u32_e32 v40, s63, v72
	v_lshlrev_b32_e32 v41, 1, v40
	v_add_u32_e32 v42, v41, v168
	s_waitcnt lgkmcnt(1)
	buffer_store_dwordx4 v[28:31], v42, s[20:23], 0 offen nt
	v_pk_fma_f32 v[22:23], v[22:23], v[232:233], v[244:245] op_sel_hi:[1,0,1]
	v_pk_fma_f32 v[20:21], v[20:21], v[232:233], v[242:243] op_sel_hi:[1,0,1]
	v_add_u32_e32 v28, v41, v169
	s_waitcnt lgkmcnt(0)
	buffer_store_dwordx4 v[36:39], v28, s[20:23], 0 offen nt
	v_pk_fma_f32 v[28:29], v[34:35], v[232:233], v[236:237] op_sel_hi:[1,0,1]
	v_pk_fma_f32 v[30:31], v[32:33], v[232:233], v[234:235] op_sel_hi:[1,0,1]
	v_pk_fma_f32 v[32:33], v[26:27], v[232:233], v[240:241] op_sel_hi:[1,0,1]
	v_pk_fma_f32 v[26:27], v[24:25], v[232:233], v[238:239] op_sel_hi:[1,0,1]
	v_cvt_pk_f16_f32 v24, v30, v31
	v_cvt_pk_f16_f32 v25, v28, v29
	v_cvt_pk_f16_f32 v26, v26, v27
	v_cvt_pk_f16_f32 v27, v32, v33
	ds_write_b128 v173, v[24:27]
	v_pk_fma_f32 v[24:25], v[14:15], v[232:233], v[248:249] op_sel_hi:[1,0,1]
	v_pk_fma_f32 v[14:15], v[12:13], v[232:233], v[246:247] op_sel_hi:[1,0,1]
	v_cvt_pk_f16_f32 v12, v20, v21
	v_cvt_pk_f16_f32 v13, v22, v23
	v_cvt_pk_f16_f32 v14, v14, v15
	v_cvt_pk_f16_f32 v15, v24, v25
	ds_write_b128 v173, v[12:15] offset:64
	ds_read_b128 v[12:15], v174
	ds_read_b128 v[20:23], v174 offset:1152
	v_add_u32_e32 v24, s64, v40
	v_lshlrev_b32_e32 v25, 1, v24
	v_add_u32_e32 v26, v25, v168
	s_waitcnt lgkmcnt(1)
	buffer_store_dwordx4 v[12:15], v26, s[20:23], 0 offen nt
	v_pk_fma_f32 v[6:7], v[6:7], v[232:233], v[244:245] op_sel:[0,1,0]
	v_pk_fma_f32 v[4:5], v[4:5], v[232:233], v[242:243] op_sel:[0,1,0]
	v_pk_fma_f32 v[12:13], v[18:19], v[232:233], v[236:237] op_sel:[0,1,0]
	v_pk_fma_f32 v[14:15], v[16:17], v[232:233], v[234:235] op_sel:[0,1,0]
	v_pk_fma_f32 v[16:17], v[10:11], v[232:233], v[240:241] op_sel:[0,1,0]
	v_pk_fma_f32 v[10:11], v[8:9], v[232:233], v[238:239] op_sel:[0,1,0]
	v_cvt_pk_f16_f32 v8, v14, v15
	v_cvt_pk_f16_f32 v9, v12, v13
	v_cvt_pk_f16_f32 v10, v10, v11
	v_cvt_pk_f16_f32 v11, v16, v17
	ds_write_b128 v173, v[8:11]
	v_pk_fma_f32 v[8:9], v[2:3], v[232:233], v[248:249] op_sel:[0,1,0]
	v_pk_fma_f32 v[2:3], v[0:1], v[232:233], v[246:247] op_sel:[0,1,0]
	v_cvt_pk_f16_f32 v0, v4, v5
	v_cvt_pk_f16_f32 v1, v6, v7
	v_cvt_pk_f16_f32 v2, v2, v3
	v_cvt_pk_f16_f32 v3, v8, v9
	ds_write_b128 v173, v[0:3] offset:64
	ds_read_b128 v[0:3], v174
	ds_read_b128 v[4:7], v174 offset:1152
	v_add_lshl_u32 v8, v24, s64, 1
	v_add_u32_e32 v25, v25, v169
	v_add_u32_e32 v9, v8, v168
	s_waitcnt lgkmcnt(4)
	buffer_store_dwordx4 v[20:23], v25, s[20:23], 0 offen nt
	s_waitcnt lgkmcnt(1)
	buffer_store_dwordx4 v[0:3], v9, s[20:23], 0 offen nt
	s_mov_b32 s67, s68
	s_mov_b32 s70, s69
	v_add_u32_e32 v0, v8, v169
	s_mov_b64 s[30:31], s[0:1]
	s_mov_b64 s[28:29], s[8:9]
	s_mov_b64 vcc, s[6:7]
	s_waitcnt lgkmcnt(0)
	buffer_store_dwordx4 v[4:7], v0, s[20:23], 0 offen nt
	s_cbranch_vccz .LBB7_12
	s_waitcnt vmcnt(0)
	s_cmpk_gt_u32 s36, 0xff
	s_cbranch_scc1 .LBB7_31
	s_barrier

.LBB7_32:
	s_endpgm
	s_endpgm
	s_endpgm
	s_endpgm
	.section	.rodata,"a",@progbits
	.p2align	6, 0x0

.LBB8_11:
	s_mov_b64 s[36:37], 0x80
	s_and_b32 s34, s24, 3
	s_add_i32 m0, s51, 0x18000
	v_lshl_add_u64 v[8:9], v[8:9], 0, s[36:37]
	s_lshl_b32 s58, s25, 6
	s_lshl_b32 s25, s25, 13
	s_lshl_b32 s26, s34, 12
	s_waitcnt vmcnt(4)
	s_barrier
	global_load_lds_dwordx4 v[8:9], off
	v_lshl_add_u64 v[6:7], v[6:7], 0, s[36:37]
	s_add_i32 m0, s51, 0x1a000
	s_add_i32 s59, s51, 0x8000
	s_add_i32 s60, s51, 0xa000
	global_load_lds_dwordx4 v[6:7], off
	v_lshl_add_u64 v[4:5], v[4:5], 0, s[36:37]
	s_mov_b32 m0, s59
	s_add_u32 s0, s40, 0xc080
	global_load_lds_dwordx4 v[4:5], off
	v_lshl_add_u64 v[2:3], v[2:3], 0, s[36:37]
	s_mov_b32 m0, s60
	s_addc_u32 s1, s41, 0
	global_load_lds_dwordx4 v[2:3], off
	s_add_i32 m0, s51, 0x1c000
	v_lshl_add_u64 v[2:3], s[0:1], 0, v[178:179]
	global_load_lds_dwordx4 v[2:3], off
	v_lshl_add_u64 v[2:3], s[0:1], 0, v[182:183]
	s_add_i32 m0, s51, 0x1e000
	s_lshl_b32 s62, s33, 3
	global_load_lds_dwordx4 v[2:3], off
	s_abs_i32 s63, s62
	v_and_b32_e32 v227, 15, v0
	v_and_b32_e32 v2, 48, v0
	v_lshlrev_b32_e32 v4, 2, v0
	v_lshlrev_b32_e32 v5, 6, v0
	v_bfe_u32 v229, v0, 3, 3
	v_cvt_f32_u32_e32 v0, s63
	s_abs_i32 s65, s33
	v_cvt_f32_u32_e32 v6, s65
	s_movk_i32 s0, 0x3c0
	v_rcp_iflag_f32_e32 v0, v0
	s_mulk_i32 s24, 0x900
	v_rcp_iflag_f32_e32 v6, v6
	v_and_or_b32 v5, v5, s0, v2
	v_mul_f32_e32 v0, 0x4f7ffffe, v0
	v_cvt_u32_f32_e32 v0, v0
	s_add_i32 s0, s24, 0
	v_lshl_or_b32 v3, v227, 6, v2
	v_and_b32_e32 v4, 32, v4
	s_add_i32 s0, s0, 0x20000
	v_bitop3_b32 v3, v3, s25, v4 bitop3:0xde
	v_bitop3_b32 v228, s26, v5, v4 bitop3:0xf6
	s_movk_i32 s1, 0x90
	v_mov_b32_e32 v4, s0
	v_mad_u32_u24 v5, v227, s1, v4
	v_mad_u32_u24 v4, v229, s1, v4
	v_readfirstlane_b32 s1, v0
	v_mul_f32_e32 v0, 0x4f7ffffe, v6
	v_cvt_u32_f32_e32 v0, v0
	s_sub_i32 s0, 0, s63
	s_mul_i32 s0, s0, s1
	s_mul_hi_u32 s0, s1, s0
	s_add_i32 s67, s1, s0
	s_sub_i32 s0, 0, s65
	v_readfirstlane_b32 s1, v0
	v_add_u16_e32 v0, v1, v10
	s_waitcnt vmcnt(6)
	s_mul_i32 s0, s0, s1
	v_lshrrev_b16_e32 v0, 1, v0
	v_and_b32_e32 v230, 0x70, v13
	s_mul_hi_u32 s0, s1, s0
	v_add_lshl_u32 v184, v11, v0, 1
	v_add_lshl_u32 v186, v12, v0, 1
	s_add_i32 s70, 0, 0x10000
	s_add_i32 s71, 0, 0x14000
	v_mbcnt_lo_u32_b32 v0, -1, 0
	s_mov_b32 s27, 0x20000
	s_lshl_b32 s61, s34, 6
	s_waitcnt lgkmcnt(0)
	s_ashr_i32 s64, s55, 31
	s_mov_b32 s26, 0x6000000
	s_and_b32 s25, s9, 0xffff
	s_mov_b32 s24, s8
	s_bfe_i32 s66, s33, 0x1001c
	s_ashr_i32 s68, s33, 31
	s_add_i32 s69, s1, s0
	v_mov_b32_e32 v185, v179
	v_mov_b32_e32 v187, v179
	v_mov_b64_e32 v[188:189], s[6:7]
	v_add_u32_e32 v231, s70, v228
	v_add_u32_e32 v232, 0, v3
	v_add_u32_e32 v233, s71, v228
	s_movk_i32 s72, 0x600
	v_mbcnt_hi_u32_b32 v234, -1, v0
	v_add_u32_e32 v235, v5, v2
	v_add_u32_e32 v236, v4, v230
	s_movk_i32 s73, 0x60
	s_mov_b32 s74, 0x30000
	s_mov_b32 s75, 0x36000
	s_lshl_b32 s34, s34, 3
	s_movk_i32 s76, 0x3000
	s_mov_b32 s77, 0x3c000
	s_mov_b32 s78, 0x42000
	s_movk_i32 s79, 0x1000
	s_mov_b32 s80, s35
	s_barrier
	s_cmpk_gt_u32 s44, 0xff
	s_cbranch_scc0 .Lprio8_done
	s_setprio 1
.Lprio8_done:
.LBB8_12:
	s_add_i32 s80, s80, 1
	s_mul_i32 s0, s80, s64
	s_mul_hi_u32 s1, s80, s55
	s_add_i32 s1, s1, s0
	s_mul_i32 s0, s80, s55
	s_add_u32 s0, s0, s2
	s_addc_u32 s1, s1, s47
	v_cmp_ge_i64_e32 vcc, s[0:1], v[188:189]
	s_and_b64 s[6:7], exec, vcc
	s_mov_b64 vcc, s[6:7]
	s_cbranch_vccnz .LBB8_22
	s_ashr_i32 s8, s0, 31
	s_lshr_b32 s8, s8, 29
	s_add_i32 s42, s0, s8
	s_and_b32 s8, s42, -8
	s_sub_i32 s43, s0, s8
	s_cmp_ge_i32 s43, s46
	s_mov_b64 s[8:9], -1
	s_cbranch_scc0 .LBB8_15
	s_sub_i32 s8, s43, s46
	s_mul_i32 s8, s8, s45
	s_add_i32 s81, s8, s49
	s_mov_b64 s[8:9], 0

.LBB8_27:
	ds_read_b128 v[72:75], v231
	ds_read_b128 v[80:83], v231 offset:1024
	ds_read_b128 v[88:91], v231 offset:2048
	ds_read_b128 v[92:95], v231 offset:3072
	s_add_u32 s40, s38, 0xfffd0080
	s_addc_u32 s41, s39, -1
	s_cmp_eq_u32 s87, 8
	s_cselect_b32 s43, s9, s41
	s_cselect_b32 s42, s8, s40
	s_cselect_b32 s41, s1, s86
	s_cselect_b32 s40, s0, s85
	v_lshl_add_u64 v[190:191], s[38:39], 0, v[184:185]
	s_add_i32 m0, s51, 0xc000
	ds_read_b128 v[136:139], v232
	ds_read_b128 v[148:151], v232 offset:1024
	ds_read_b128 v[152:155], v232 offset:2048
	ds_read_b128 v[156:159], v232 offset:3072
	ds_read_b128 v[160:163], v232 offset:4096
	ds_read_b128 v[164:167], v232 offset:5120
	ds_read_b128 v[168:171], v232 offset:6144
	ds_read_b128 v[172:175], v232 offset:7168
	global_load_lds_dwordx4 v[190:191], off
	v_lshl_add_u64 v[190:191], s[38:39], 0, v[186:187]
	s_add_i32 m0, s51, 0xe000
	s_nop 0
	global_load_lds_dwordx4 v[190:191], off
	s_waitcnt lgkmcnt(8)
	s_barrier
	s_waitcnt lgkmcnt(0)
	s_waitcnt lgkmcnt(0)
	v_mfma_f32_16x16x32_f16 v[144:147], v[72:75], v[136:139], v[144:147]
	v_mfma_f32_16x16x32_f16 v[140:143], v[88:91], v[136:139], v[140:143]
	v_mfma_f32_16x16x32_f16 v[124:127], v[72:75], v[152:155], v[124:127]
	v_mfma_f32_16x16x32_f16 v[120:123], v[88:91], v[152:155], v[120:123]
	v_mfma_f32_16x16x32_f16 v[108:111], v[72:75], v[160:163], v[108:111]
	v_mfma_f32_16x16x32_f16 v[104:107], v[88:91], v[160:163], v[104:107]
	v_mfma_f32_16x16x32_f16 v[84:87], v[72:75], v[168:171], v[84:87]
	v_mfma_f32_16x16x32_f16 v[76:79], v[88:91], v[168:171], v[76:79]
	v_mfma_f32_16x16x32_f16 v[144:147], v[80:83], v[148:151], v[144:147]
	v_mfma_f32_16x16x32_f16 v[140:143], v[92:95], v[148:151], v[140:143]
	v_mfma_f32_16x16x32_f16 v[124:127], v[80:83], v[156:159], v[124:127]
	v_mfma_f32_16x16x32_f16 v[120:123], v[92:95], v[156:159], v[120:123]
	v_mfma_f32_16x16x32_f16 v[108:111], v[80:83], v[164:167], v[108:111]
	v_mfma_f32_16x16x32_f16 v[104:107], v[92:95], v[164:167], v[104:107]
	v_mfma_f32_16x16x32_f16 v[84:87], v[80:83], v[172:175], v[84:87]
	v_mfma_f32_16x16x32_f16 v[76:79], v[92:95], v[172:175], v[76:79]
	s_barrier
	s_add_i32 s88, s70, s50
	v_lshl_add_u64 v[206:207], s[40:41], 0, v[178:179]
	s_mov_b32 m0, s88
	ds_read_b128 v[190:193], v233
	ds_read_b128 v[194:197], v233 offset:1024
	ds_read_b128 v[198:201], v233 offset:2048
	ds_read_b128 v[202:205], v233 offset:3072
	global_load_lds_dwordx4 v[206:207], off
	v_lshl_add_u64 v[208:209], s[40:41], 0, v[182:183]
	s_add_i32 m0, s88, 0x2000
	s_nop 0
	global_load_lds_dwordx4 v[208:209], off
	s_barrier
	s_waitcnt lgkmcnt(0)
	s_waitcnt lgkmcnt(0)
	v_mfma_f32_16x16x32_f16 v[132:135], v[190:193], v[136:139], v[132:135]
	v_mfma_f32_16x16x32_f16 v[128:131], v[198:201], v[136:139], v[128:131]
	v_mfma_f32_16x16x32_f16 v[116:119], v[190:193], v[152:155], v[116:119]
	v_mfma_f32_16x16x32_f16 v[112:115], v[198:201], v[152:155], v[112:115]
	v_mfma_f32_16x16x32_f16 v[100:103], v[190:193], v[160:163], v[100:103]
	v_mfma_f32_16x16x32_f16 v[96:99], v[198:201], v[160:163], v[96:99]
	v_mfma_f32_16x16x32_f16 v[68:71], v[190:193], v[168:171], v[68:71]
	v_mfma_f32_16x16x32_f16 v[64:67], v[198:201], v[168:171], v[64:67]
	v_mfma_f32_16x16x32_f16 v[132:135], v[194:197], v[148:151], v[132:135]
	v_mfma_f32_16x16x32_f16 v[128:131], v[202:205], v[148:151], v[128:131]
	v_mfma_f32_16x16x32_f16 v[116:119], v[194:197], v[156:159], v[116:119]
	v_mfma_f32_16x16x32_f16 v[112:115], v[202:205], v[156:159], v[112:115]
	v_mfma_f32_16x16x32_f16 v[100:103], v[194:197], v[164:167], v[100:103]
	v_mfma_f32_16x16x32_f16 v[96:99], v[202:205], v[164:167], v[96:99]
	v_mfma_f32_16x16x32_f16 v[68:71], v[194:197], v[172:175], v[68:71]
	v_mfma_f32_16x16x32_f16 v[64:67], v[202:205], v[172:175], v[64:67]
	s_mov_b32 m0, s51
	v_lshl_add_u64 v[210:211], s[42:43], 0, v[176:177]
	s_barrier
	ds_read_b128 v[136:139], v232 offset:16384
	ds_read_b128 v[148:151], v232 offset:17408
	ds_read_b128 v[152:155], v232 offset:18432
	ds_read_b128 v[156:159], v232 offset:19456
	ds_read_b128 v[160:163], v232 offset:20480
	ds_read_b128 v[164:167], v232 offset:21504
	ds_read_b128 v[168:171], v232 offset:22528
	ds_read_b128 v[172:175], v232 offset:23552
	global_load_lds_dwordx4 v[210:211], off
	v_lshl_add_u64 v[212:213], s[42:43], 0, v[180:181]
	s_mov_b32 m0, s52
	s_nop 0
	global_load_lds_dwordx4 v[212:213], off
	s_barrier
	s_waitcnt lgkmcnt(0)
	s_waitcnt lgkmcnt(0)
	v_mfma_f32_16x16x32_f16 v[60:63], v[72:75], v[136:139], v[60:63]
	v_mfma_f32_16x16x32_f16 v[56:59], v[88:91], v[136:139], v[56:59]
	v_mfma_f32_16x16x32_f16 v[44:47], v[72:75], v[152:155], v[44:47]
	v_mfma_f32_16x16x32_f16 v[40:43], v[88:91], v[152:155], v[40:43]
	v_mfma_f32_16x16x32_f16 v[28:31], v[72:75], v[160:163], v[28:31]
	v_mfma_f32_16x16x32_f16 v[24:27], v[88:91], v[160:163], v[24:27]
	v_mfma_f32_16x16x32_f16 v[12:15], v[72:75], v[168:171], v[12:15]
	v_mfma_f32_16x16x32_f16 v[8:11], v[88:91], v[168:171], v[8:11]
	v_mfma_f32_16x16x32_f16 v[60:63], v[80:83], v[148:151], v[60:63]
	v_mfma_f32_16x16x32_f16 v[56:59], v[92:95], v[148:151], v[56:59]
	v_mfma_f32_16x16x32_f16 v[44:47], v[80:83], v[156:159], v[44:47]
	v_mfma_f32_16x16x32_f16 v[40:43], v[92:95], v[156:159], v[40:43]
	v_mfma_f32_16x16x32_f16 v[28:31], v[80:83], v[164:167], v[28:31]
	v_mfma_f32_16x16x32_f16 v[24:27], v[92:95], v[164:167], v[24:27]
	v_mfma_f32_16x16x32_f16 v[12:15], v[80:83], v[172:175], v[12:15]
	v_mfma_f32_16x16x32_f16 v[8:11], v[92:95], v[172:175], v[8:11]
	s_barrier
	s_add_u32 s88, s40, 0xc000
	s_addc_u32 s89, s41, 0
	s_add_i32 s90, s71, s50
	v_lshl_add_u64 v[72:73], s[88:89], 0, v[178:179]
	s_mov_b32 m0, s90
	s_nop 0
	global_load_lds_dwordx4 v[72:73], off
	v_lshl_add_u64 v[72:73], s[88:89], 0, v[182:183]
	s_add_i32 m0, s90, 0x2000
	s_nop 0
	global_load_lds_dwordx4 v[72:73], off
	s_waitcnt vmcnt(6)
	s_barrier
	v_mfma_f32_16x16x32_f16 v[52:55], v[190:193], v[136:139], v[52:55]
	v_mfma_f32_16x16x32_f16 v[48:51], v[198:201], v[136:139], v[48:51]
	v_mfma_f32_16x16x32_f16 v[36:39], v[190:193], v[152:155], v[36:39]
	v_mfma_f32_16x16x32_f16 v[32:35], v[198:201], v[152:155], v[32:35]
	v_mfma_f32_16x16x32_f16 v[20:23], v[190:193], v[160:163], v[20:23]
	v_mfma_f32_16x16x32_f16 v[16:19], v[198:201], v[160:163], v[16:19]
	v_mfma_f32_16x16x32_f16 v[4:7], v[190:193], v[168:171], v[4:7]
	v_mfma_f32_16x16x32_f16 v[0:3], v[198:201], v[168:171], v[0:3]
	v_mfma_f32_16x16x32_f16 v[52:55], v[194:197], v[148:151], v[52:55]
	v_mfma_f32_16x16x32_f16 v[48:51], v[202:205], v[148:151], v[48:51]
	v_mfma_f32_16x16x32_f16 v[36:39], v[194:197], v[156:159], v[36:39]
	v_mfma_f32_16x16x32_f16 v[32:35], v[202:205], v[156:159], v[32:35]
	v_mfma_f32_16x16x32_f16 v[20:23], v[194:197], v[164:167], v[20:23]
	v_mfma_f32_16x16x32_f16 v[16:19], v[202:205], v[164:167], v[16:19]
	v_mfma_f32_16x16x32_f16 v[4:7], v[194:197], v[172:175], v[4:7]
	v_mfma_f32_16x16x32_f16 v[0:3], v[202:205], v[172:175], v[0:3]
	s_add_i32 s88, 0, 0x18000
	v_add_u32_e32 v92, s88, v228
	s_barrier
	ds_read_b128 v[72:75], v92
	ds_read_b128 v[80:83], v92 offset:1024
	ds_read_b128 v[88:91], v92 offset:2048
	ds_read_b128 v[92:95], v92 offset:3072
	s_add_u32 s42, s42, 0x30000
	s_addc_u32 s43, s43, 0
	s_mov_b32 m0, s53
	v_lshl_add_u64 v[190:191], s[42:43], 0, v[176:177]
	ds_read_b128 v[136:139], v232 offset:32768
	ds_read_b128 v[148:151], v232 offset:33792
	ds_read_b128 v[152:155], v232 offset:34816
	ds_read_b128 v[156:159], v232 offset:35840
	ds_read_b128 v[160:163], v232 offset:36864
	ds_read_b128 v[164:167], v232 offset:37888
	ds_read_b128 v[168:171], v232 offset:38912
	ds_read_b128 v[172:175], v232 offset:39936
	global_load_lds_dwordx4 v[190:191], off
	v_lshl_add_u64 v[190:191], s[42:43], 0, v[180:181]
	s_mov_b32 m0, s54
	s_nop 0
	global_load_lds_dwordx4 v[190:191], off
	s_waitcnt lgkmcnt(8)
	s_barrier
	s_waitcnt lgkmcnt(0)
	s_waitcnt lgkmcnt(0)
	v_mfma_f32_16x16x32_f16 v[144:147], v[72:75], v[136:139], v[144:147]
	v_mfma_f32_16x16x32_f16 v[140:143], v[88:91], v[136:139], v[140:143]
	v_mfma_f32_16x16x32_f16 v[124:127], v[72:75], v[152:155], v[124:127]
	v_mfma_f32_16x16x32_f16 v[120:123], v[88:91], v[152:155], v[120:123]
	v_mfma_f32_16x16x32_f16 v[108:111], v[72:75], v[160:163], v[108:111]
	v_mfma_f32_16x16x32_f16 v[104:107], v[88:91], v[160:163], v[104:107]
	v_mfma_f32_16x16x32_f16 v[84:87], v[72:75], v[168:171], v[84:87]
	v_mfma_f32_16x16x32_f16 v[76:79], v[88:91], v[168:171], v[76:79]
	v_mfma_f32_16x16x32_f16 v[144:147], v[80:83], v[148:151], v[144:147]
	v_mfma_f32_16x16x32_f16 v[140:143], v[92:95], v[148:151], v[140:143]
	v_mfma_f32_16x16x32_f16 v[124:127], v[80:83], v[156:159], v[124:127]
	v_mfma_f32_16x16x32_f16 v[120:123], v[92:95], v[156:159], v[120:123]
	v_mfma_f32_16x16x32_f16 v[108:111], v[80:83], v[164:167], v[108:111]
	v_mfma_f32_16x16x32_f16 v[104:107], v[92:95], v[164:167], v[104:107]
	v_mfma_f32_16x16x32_f16 v[84:87], v[80:83], v[172:175], v[84:87]
	v_mfma_f32_16x16x32_f16 v[76:79], v[92:95], v[172:175], v[76:79]
	s_barrier
	s_add_i32 s42, 0, 0x1c000
	s_add_i32 s43, s88, s50
	v_add_u32_e32 v202, s42, v228
	v_lshl_add_u64 v[206:207], v[206:207], 0, s[36:37]
	s_mov_b32 m0, s43
	ds_read_b128 v[190:193], v202
	ds_read_b128 v[194:197], v202 offset:1024
	ds_read_b128 v[198:201], v202 offset:2048
	ds_read_b128 v[202:205], v202 offset:3072
	global_load_lds_dwordx4 v[206:207], off
	v_lshl_add_u64 v[206:207], v[208:209], 0, s[36:37]
	s_add_i32 m0, s43, 0x2000
	s_nop 0
	global_load_lds_dwordx4 v[206:207], off
	s_barrier
	s_waitcnt lgkmcnt(0)
	s_waitcnt lgkmcnt(0)
	v_mfma_f32_16x16x32_f16 v[132:135], v[190:193], v[136:139], v[132:135]
	v_mfma_f32_16x16x32_f16 v[128:131], v[198:201], v[136:139], v[128:131]
	v_mfma_f32_16x16x32_f16 v[116:119], v[190:193], v[152:155], v[116:119]
	v_mfma_f32_16x16x32_f16 v[112:115], v[198:201], v[152:155], v[112:115]
	v_mfma_f32_16x16x32_f16 v[100:103], v[190:193], v[160:163], v[100:103]
	v_mfma_f32_16x16x32_f16 v[96:99], v[198:201], v[160:163], v[96:99]
	v_mfma_f32_16x16x32_f16 v[68:71], v[190:193], v[168:171], v[68:71]
	v_mfma_f32_16x16x32_f16 v[64:67], v[198:201], v[168:171], v[64:67]
	v_mfma_f32_16x16x32_f16 v[132:135], v[194:197], v[148:151], v[132:135]
	v_mfma_f32_16x16x32_f16 v[128:131], v[202:205], v[148:151], v[128:131]
	v_mfma_f32_16x16x32_f16 v[116:119], v[194:197], v[156:159], v[116:119]
	v_mfma_f32_16x16x32_f16 v[112:115], v[202:205], v[156:159], v[112:115]
	v_mfma_f32_16x16x32_f16 v[100:103], v[194:197], v[164:167], v[100:103]
	v_mfma_f32_16x16x32_f16 v[96:99], v[202:205], v[164:167], v[96:99]
	v_mfma_f32_16x16x32_f16 v[68:71], v[194:197], v[172:175], v[68:71]
	v_mfma_f32_16x16x32_f16 v[64:67], v[202:205], v[172:175], v[64:67]
	s_mov_b32 m0, s59
	v_lshl_add_u64 v[206:207], v[210:211], 0, s[36:37]
	s_barrier
	ds_read_b128 v[136:139], v232 offset:49152
	ds_read_b128 v[148:151], v232 offset:50176
	ds_read_b128 v[152:155], v232 offset:51200
	ds_read_b128 v[156:159], v232 offset:52224
	ds_read_b128 v[160:163], v232 offset:53248
	ds_read_b128 v[164:167], v232 offset:54272
	ds_read_b128 v[168:171], v232 offset:55296
	ds_read_b128 v[172:175], v232 offset:56320
	global_load_lds_dwordx4 v[206:207], off
	v_lshl_add_u64 v[206:207], v[212:213], 0, s[36:37]
	s_mov_b32 m0, s60
	s_nop 0
	global_load_lds_dwordx4 v[206:207], off
	s_barrier
	s_waitcnt lgkmcnt(0)
	s_waitcnt lgkmcnt(0)
	v_mfma_f32_16x16x32_f16 v[60:63], v[72:75], v[136:139], v[60:63]
	v_mfma_f32_16x16x32_f16 v[56:59], v[88:91], v[136:139], v[56:59]
	v_mfma_f32_16x16x32_f16 v[44:47], v[72:75], v[152:155], v[44:47]
	v_mfma_f32_16x16x32_f16 v[40:43], v[88:91], v[152:155], v[40:43]
	v_mfma_f32_16x16x32_f16 v[28:31], v[72:75], v[160:163], v[28:31]
	v_mfma_f32_16x16x32_f16 v[24:27], v[88:91], v[160:163], v[24:27]
	v_mfma_f32_16x16x32_f16 v[12:15], v[72:75], v[168:171], v[12:15]
	v_mfma_f32_16x16x32_f16 v[8:11], v[88:91], v[168:171], v[8:11]
	v_mfma_f32_16x16x32_f16 v[60:63], v[80:83], v[148:151], v[60:63]
	v_mfma_f32_16x16x32_f16 v[56:59], v[92:95], v[148:151], v[56:59]
	v_mfma_f32_16x16x32_f16 v[44:47], v[80:83], v[156:159], v[44:47]
	v_mfma_f32_16x16x32_f16 v[40:43], v[92:95], v[156:159], v[40:43]
	v_mfma_f32_16x16x32_f16 v[28:31], v[80:83], v[164:167], v[28:31]
	v_mfma_f32_16x16x32_f16 v[24:27], v[92:95], v[164:167], v[24:27]
	v_mfma_f32_16x16x32_f16 v[12:15], v[80:83], v[172:175], v[12:15]
	v_mfma_f32_16x16x32_f16 v[8:11], v[92:95], v[172:175], v[8:11]
	s_barrier
	s_add_u32 s40, s40, 0xc080
	s_addc_u32 s41, s41, 0
	s_add_i32 s42, s42, s50
	v_lshl_add_u64 v[72:73], s[40:41], 0, v[178:179]
	s_mov_b32 m0, s42
	s_nop 0
	global_load_lds_dwordx4 v[72:73], off
	v_lshl_add_u64 v[72:73], s[40:41], 0, v[182:183]
	s_add_i32 m0, s42, 0x2000
	s_nop 0
	global_load_lds_dwordx4 v[72:73], off
	s_waitcnt vmcnt(6)
	s_barrier
	v_mfma_f32_16x16x32_f16 v[52:55], v[190:193], v[136:139], v[52:55]
	v_mfma_f32_16x16x32_f16 v[48:51], v[198:201], v[136:139], v[48:51]
	v_mfma_f32_16x16x32_f16 v[36:39], v[190:193], v[152:155], v[36:39]
	v_mfma_f32_16x16x32_f16 v[32:35], v[198:201], v[152:155], v[32:35]
	v_mfma_f32_16x16x32_f16 v[20:23], v[190:193], v[160:163], v[20:23]
	v_mfma_f32_16x16x32_f16 v[16:19], v[198:201], v[160:163], v[16:19]
	v_mfma_f32_16x16x32_f16 v[4:7], v[190:193], v[168:171], v[4:7]
	v_mfma_f32_16x16x32_f16 v[0:3], v[198:201], v[168:171], v[0:3]
	v_mfma_f32_16x16x32_f16 v[52:55], v[194:197], v[148:151], v[52:55]
	v_mfma_f32_16x16x32_f16 v[48:51], v[202:205], v[148:151], v[48:51]
	v_mfma_f32_16x16x32_f16 v[36:39], v[194:197], v[156:159], v[36:39]
	v_mfma_f32_16x16x32_f16 v[32:35], v[202:205], v[156:159], v[32:35]
	v_mfma_f32_16x16x32_f16 v[20:23], v[194:197], v[164:167], v[20:23]
	v_mfma_f32_16x16x32_f16 v[16:19], v[202:205], v[164:167], v[16:19]
	v_mfma_f32_16x16x32_f16 v[4:7], v[194:197], v[172:175], v[4:7]
	v_mfma_f32_16x16x32_f16 v[0:3], v[202:205], v[172:175], v[0:3]
	s_add_i32 s87, s87, 2
	s_add_u32 s38, s38, 0x100
	s_addc_u32 s39, s39, 0
	s_add_u32 s85, s85, 0x100
	s_addc_u32 s86, s86, 0
	s_cmp_gt_u32 s87, 9
	s_barrier
	s_cbranch_scc0 .LBB8_27
	s_lshl_b32 s92, s84, 8
	s_add_i32 s92, s92, s58
	s_lshl_b32 s93, s83, 8
	s_or_b32 s93, s93, s61
	v_lshlrev_b32_e32 v237, 2, v226
	s_lshl_b32 s96, s93, 2
	s_add_u32 s94, s16, s96
	s_addc_u32 s95, s17, 0
	global_load_dwordx4 v[72:75], v237, s[94:95] offset:0
	global_load_dwordx4 v[80:83], v237, s[94:95] offset:16
	global_load_dwordx4 v[88:91], v237, s[94:95] offset:128
	global_load_dwordx4 v[92:95], v237, s[94:95] offset:144
	s_add_u32 s94, s18, s96
	s_addc_u32 s95, s19, 0
	global_load_dwordx4 v[136:139], v237, s[94:95] offset:0
	global_load_dwordx4 v[148:151], v237, s[94:95] offset:16
	global_load_dwordx4 v[152:155], v237, s[94:95] offset:128
	global_load_dwordx4 v[156:159], v237, s[94:95] offset:144
	s_add_u32 s94, s14, s96
	s_addc_u32 s95, s15, 0
	global_load_dwordx4 v[160:163], v237, s[94:95] offset:0
	global_load_dwordx4 v[164:167], v237, s[94:95] offset:16
	global_load_dwordx4 v[168:171], v237, s[94:95] offset:128
	global_load_dwordx4 v[172:175], v237, s[94:95] offset:144
	v_lshlrev_b32_e32 v190, 3, v227
	s_lshl_b32 s96, s92, 3
	s_add_u32 s94, s12, s96
	s_addc_u32 s95, s13, 0
	global_load_dwordx2 v[238:239], v190, s[94:95] offset:0
	global_load_dwordx2 v[192:193], v190, s[94:95] offset:128
	global_load_dwordx2 v[194:195], v190, s[94:95] offset:256
	global_load_dwordx2 v[196:197], v190, s[94:95] offset:384
	global_load_dwordx2 v[198:199], v190, s[94:95] offset:1024
	global_load_dwordx2 v[200:201], v190, s[94:95] offset:1152
	global_load_dwordx2 v[202:203], v190, s[94:95] offset:1280
	global_load_dwordx2 v[204:205], v190, s[94:95] offset:1408
	v_mul_u32_u24_e32 v191, 0x600, v227
	v_lshl_add_u32 v191, v226, 1, v191
	s_mul_i32 s96, s92, 0x600
	s_lshl_b32 s97, s93, 1
	s_add_u32 s96, s96, s97
	s_add_u32 s98, s10, s96
	s_addc_u32 s99, s11, 0
	s_add_u32 s94, s98, 0x0
	s_addc_u32 s95, s99, 0
	global_load_dwordx4 v[208:211], v191, s[94:95] offset:0 nt
	global_load_dwordx4 v[212:215], v191, s[94:95] offset:64 nt
	s_add_u32 s94, s98, 0x6000
	s_addc_u32 s95, s99, 0
	global_load_dwordx4 v[216:219], v191, s[94:95] offset:0 nt
	global_load_dwordx4 v[220:223], v191, s[94:95] offset:64 nt
	v_add_u32_e32 v224, s92, v229
	v_mul_u32_u24_e32 v224, 0x600, v224
	s_lshl_b32 s97, s93, 1
	v_add3_u32 v224, v224, v230, s97
	s_lshl_b32 s96, s83, 2
	s_lshr_b32 s97, s61, 6
	s_add_u32 s96, s96, s97
	s_lshl_b32 s96, s96, 19
	s_lshl_b32 s97, s92, 3
	s_add_u32 s96, s96, s97
	s_add_u32 s100, s28, s96
	s_addc_u32 s101, s29, 0
	s_waitcnt vmcnt(19)
	v_pk_add_f32 v[72:73], v[72:73], v[136:137]
	v_pk_add_f32 v[74:75], v[74:75], v[138:139]
	s_waitcnt vmcnt(18)
	v_pk_add_f32 v[80:81], v[80:81], v[148:149]
	v_pk_add_f32 v[82:83], v[82:83], v[150:151]
	s_waitcnt vmcnt(17)
	v_pk_add_f32 v[88:89], v[88:89], v[152:153]
	v_pk_add_f32 v[90:91], v[90:91], v[154:155]
	s_waitcnt vmcnt(16)
	v_pk_add_f32 v[92:93], v[92:93], v[156:157]
	v_pk_add_f32 v[94:95], v[94:95], v[158:159]
	v_pk_add_f32 v[144:145], v[144:145], v[72:73]
	v_pk_add_f32 v[146:147], v[146:147], v[74:75]
	v_pk_add_f32 v[124:125], v[124:125], v[72:73]
	v_pk_add_f32 v[126:127], v[126:127], v[74:75]
	v_pk_add_f32 v[108:109], v[108:109], v[72:73]
	v_pk_add_f32 v[110:111], v[110:111], v[74:75]
	v_pk_add_f32 v[84:85], v[84:85], v[72:73]
	v_pk_add_f32 v[86:87], v[86:87], v[74:75]
	v_pk_add_f32 v[60:61], v[60:61], v[72:73]
	v_pk_add_f32 v[62:63], v[62:63], v[74:75]
	v_pk_add_f32 v[44:45], v[44:45], v[72:73]
	v_pk_add_f32 v[46:47], v[46:47], v[74:75]
	v_pk_add_f32 v[28:29], v[28:29], v[72:73]
	v_pk_add_f32 v[30:31], v[30:31], v[74:75]
	v_pk_add_f32 v[12:13], v[12:13], v[72:73]
	v_pk_add_f32 v[14:15], v[14:15], v[74:75]
	v_pk_add_f32 v[140:141], v[140:141], v[80:81]
	v_pk_add_f32 v[142:143], v[142:143], v[82:83]
	v_pk_add_f32 v[120:121], v[120:121], v[80:81]
	v_pk_add_f32 v[122:123], v[122:123], v[82:83]
	v_pk_add_f32 v[104:105], v[104:105], v[80:81]
	v_pk_add_f32 v[106:107], v[106:107], v[82:83]
	v_pk_add_f32 v[76:77], v[76:77], v[80:81]
	v_pk_add_f32 v[78:79], v[78:79], v[82:83]
	v_pk_add_f32 v[56:57], v[56:57], v[80:81]
	v_pk_add_f32 v[58:59], v[58:59], v[82:83]
	v_pk_add_f32 v[40:41], v[40:41], v[80:81]
	v_pk_add_f32 v[42:43], v[42:43], v[82:83]
	v_pk_add_f32 v[24:25], v[24:25], v[80:81]
	v_pk_add_f32 v[26:27], v[26:27], v[82:83]
	v_pk_add_f32 v[8:9], v[8:9], v[80:81]
	v_pk_add_f32 v[10:11], v[10:11], v[82:83]
	v_pk_add_f32 v[132:133], v[132:133], v[88:89]
	v_pk_add_f32 v[134:135], v[134:135], v[90:91]
	v_pk_add_f32 v[116:117], v[116:117], v[88:89]
	v_pk_add_f32 v[118:119], v[118:119], v[90:91]
	v_pk_add_f32 v[100:101], v[100:101], v[88:89]
	v_pk_add_f32 v[102:103], v[102:103], v[90:91]
	v_pk_add_f32 v[68:69], v[68:69], v[88:89]
	v_pk_add_f32 v[70:71], v[70:71], v[90:91]
	v_pk_add_f32 v[52:53], v[52:53], v[88:89]
	v_pk_add_f32 v[54:55], v[54:55], v[90:91]
	v_pk_add_f32 v[36:37], v[36:37], v[88:89]
	v_pk_add_f32 v[38:39], v[38:39], v[90:91]
	v_pk_add_f32 v[20:21], v[20:21], v[88:89]
	v_pk_add_f32 v[22:23], v[22:23], v[90:91]
	v_pk_add_f32 v[4:5], v[4:5], v[88:89]
	v_pk_add_f32 v[6:7], v[6:7], v[90:91]
	v_pk_add_f32 v[128:129], v[128:129], v[92:93]
	v_pk_add_f32 v[130:131], v[130:131], v[94:95]
	v_pk_add_f32 v[112:113], v[112:113], v[92:93]
	v_pk_add_f32 v[114:115], v[114:115], v[94:95]
	v_pk_add_f32 v[96:97], v[96:97], v[92:93]
	v_pk_add_f32 v[98:99], v[98:99], v[94:95]
	v_pk_add_f32 v[64:65], v[64:65], v[92:93]
	v_pk_add_f32 v[66:67], v[66:67], v[94:95]
	v_pk_add_f32 v[48:49], v[48:49], v[92:93]
	v_pk_add_f32 v[50:51], v[50:51], v[94:95]
	v_pk_add_f32 v[32:33], v[32:33], v[92:93]
	v_pk_add_f32 v[34:35], v[34:35], v[94:95]
	v_pk_add_f32 v[16:17], v[16:17], v[92:93]
	v_pk_add_f32 v[18:19], v[18:19], v[94:95]
	v_pk_add_f32 v[0:1], v[0:1], v[92:93]
	v_pk_add_f32 v[2:3], v[2:3], v[94:95]
	s_add_u32 s94, s98, 0xc000
	s_addc_u32 s95, s99, 0
	global_load_dwordx4 v[240:243], v191, s[94:95] offset:0 nt
	global_load_dwordx4 v[244:247], v191, s[94:95] offset:64 nt
	s_add_u32 s94, s98, 0x12000
	s_addc_u32 s95, s99, 0
	global_load_dwordx4 v[248:251], v191, s[94:95] offset:0 nt
	global_load_dwordx4 v[252:255], v191, s[94:95] offset:64 nt
	s_add_u32 s94, s98, 0x30000
	s_addc_u32 s95, s99, 0
	global_load_dwordx4 v[136:139], v191, s[94:95] offset:0 nt
	global_load_dwordx4 v[148:151], v191, s[94:95] offset:64 nt
	s_add_u32 s94, s98, 0x36000
	s_addc_u32 s95, s99, 0
	global_load_dwordx4 v[152:155], v191, s[94:95] offset:0 nt
	global_load_dwordx4 v[156:159], v191, s[94:95] offset:64 nt
	s_waitcnt vmcnt(19)
	s_waitcnt vmcnt(11)
	v_cvt_f32_f16_e32 v72, v208
	v_cvt_f32_f16_sdwa v73, v208 dst_sel:DWORD dst_unused:UNUSED_PAD src0_sel:WORD_1
	v_cvt_f32_f16_e32 v74, v209
	v_cvt_f32_f16_sdwa v75, v209 dst_sel:DWORD dst_unused:UNUSED_PAD src0_sel:WORD_1
	v_cvt_f32_f16_e32 v80, v210
	v_cvt_f32_f16_sdwa v81, v210 dst_sel:DWORD dst_unused:UNUSED_PAD src0_sel:WORD_1
	v_cvt_f32_f16_e32 v82, v211
	v_cvt_f32_f16_sdwa v83, v211 dst_sel:DWORD dst_unused:UNUSED_PAD src0_sel:WORD_1
	v_sub_f32_e32 v72, v72, v238
	v_sub_f32_e32 v73, v73, v238
	v_sub_f32_e32 v74, v74, v238
	v_sub_f32_e32 v75, v75, v238
	v_sub_f32_e32 v80, v80, v238
	v_sub_f32_e32 v81, v81, v238
	v_sub_f32_e32 v82, v82, v238
	v_sub_f32_e32 v83, v83, v238
	v_pk_mul_f32 v[72:73], v[238:239], v[72:73] op_sel:[1,0]
	v_pk_mul_f32 v[74:75], v[238:239], v[74:75] op_sel:[1,0]
	v_pk_mul_f32 v[80:81], v[238:239], v[80:81] op_sel:[1,0]
	v_pk_mul_f32 v[82:83], v[238:239], v[82:83] op_sel:[1,0]
	v_pk_fma_f32 v[144:145], v[72:73], v[160:161], v[144:145]
	v_pk_fma_f32 v[146:147], v[74:75], v[162:163], v[146:147]
	v_pk_fma_f32 v[140:141], v[80:81], v[164:165], v[140:141]
	v_pk_fma_f32 v[142:143], v[82:83], v[166:167], v[142:143]
	v_cvt_pk_f16_f32 v144, v144, v145
	v_cvt_pk_f16_f32 v145, v146, v147
	v_cvt_pk_f16_f32 v146, v140, v141
	v_cvt_pk_f16_f32 v147, v142, v143
	ds_write_b128 v235, v[144:147]
	v_fma_mix_f32 v206, v144, 1.0, 0 op_sel_hi:[1,0,0]
	v_fma_mix_f32 v207, v144, v144, 0 op_sel_hi:[1,1,0]
	v_fma_mix_f32 v206, v144, 1.0, v206 op_sel:[1,0,0] op_sel_hi:[1,0,0]
	v_fma_mix_f32 v207, v144, v144, v207 op_sel:[1,1,0] op_sel_hi:[1,1,0]
	v_fma_mix_f32 v206, v145, 1.0, v206 op_sel_hi:[1,0,0]
	v_fma_mix_f32 v207, v145, v145, v207 op_sel_hi:[1,1,0]
	v_fma_mix_f32 v206, v145, 1.0, v206 op_sel:[1,0,0] op_sel_hi:[1,0,0]
	v_fma_mix_f32 v207, v145, v145, v207 op_sel:[1,1,0] op_sel_hi:[1,1,0]
	v_fma_mix_f32 v206, v146, 1.0, v206 op_sel_hi:[1,0,0]
	v_fma_mix_f32 v207, v146, v146, v207 op_sel_hi:[1,1,0]
	v_fma_mix_f32 v206, v146, 1.0, v206 op_sel:[1,0,0] op_sel_hi:[1,0,0]
	v_fma_mix_f32 v207, v146, v146, v207 op_sel:[1,1,0] op_sel_hi:[1,1,0]
	v_fma_mix_f32 v206, v147, 1.0, v206 op_sel_hi:[1,0,0]
	v_fma_mix_f32 v207, v147, v147, v207 op_sel_hi:[1,1,0]
	v_fma_mix_f32 v206, v147, 1.0, v206 op_sel:[1,0,0] op_sel_hi:[1,0,0]
	v_fma_mix_f32 v207, v147, v147, v207 op_sel:[1,1,0] op_sel_hi:[1,1,0]
	s_waitcnt vmcnt(10)
	v_cvt_f32_f16_e32 v72, v212
	v_cvt_f32_f16_sdwa v73, v212 dst_sel:DWORD dst_unused:UNUSED_PAD src0_sel:WORD_1
	v_cvt_f32_f16_e32 v74, v213
	v_cvt_f32_f16_sdwa v75, v213 dst_sel:DWORD dst_unused:UNUSED_PAD src0_sel:WORD_1
	v_cvt_f32_f16_e32 v80, v214
	v_cvt_f32_f16_sdwa v81, v214 dst_sel:DWORD dst_unused:UNUSED_PAD src0_sel:WORD_1
	v_cvt_f32_f16_e32 v82, v215
	v_cvt_f32_f16_sdwa v83, v215 dst_sel:DWORD dst_unused:UNUSED_PAD src0_sel:WORD_1
	v_sub_f32_e32 v72, v72, v238
	v_sub_f32_e32 v73, v73, v238
	v_sub_f32_e32 v74, v74, v238
	v_sub_f32_e32 v75, v75, v238
	v_sub_f32_e32 v80, v80, v238
	v_sub_f32_e32 v81, v81, v238
	v_sub_f32_e32 v82, v82, v238
	v_sub_f32_e32 v83, v83, v238
	v_pk_mul_f32 v[72:73], v[238:239], v[72:73] op_sel:[1,0]
	v_pk_mul_f32 v[74:75], v[238:239], v[74:75] op_sel:[1,0]
	v_pk_mul_f32 v[80:81], v[238:239], v[80:81] op_sel:[1,0]
	v_pk_mul_f32 v[82:83], v[238:239], v[82:83] op_sel:[1,0]
	v_pk_fma_f32 v[132:133], v[72:73], v[168:169], v[132:133]
	v_pk_fma_f32 v[134:135], v[74:75], v[170:171], v[134:135]
	v_pk_fma_f32 v[128:129], v[80:81], v[172:173], v[128:129]
	v_pk_fma_f32 v[130:131], v[82:83], v[174:175], v[130:131]
	v_cvt_pk_f16_f32 v132, v132, v133
	v_cvt_pk_f16_f32 v133, v134, v135
	v_cvt_pk_f16_f32 v134, v128, v129
	v_cvt_pk_f16_f32 v135, v130, v131
	ds_write_b128 v235, v[132:135] offset:64
	v_fma_mix_f32 v206, v132, 1.0, v206 op_sel_hi:[1,0,0]
	v_fma_mix_f32 v207, v132, v132, v207 op_sel_hi:[1,1,0]
	v_fma_mix_f32 v206, v132, 1.0, v206 op_sel:[1,0,0] op_sel_hi:[1,0,0]
	v_fma_mix_f32 v207, v132, v132, v207 op_sel:[1,1,0] op_sel_hi:[1,1,0]
	v_fma_mix_f32 v206, v133, 1.0, v206 op_sel_hi:[1,0,0]
	v_fma_mix_f32 v207, v133, v133, v207 op_sel_hi:[1,1,0]
	v_fma_mix_f32 v206, v133, 1.0, v206 op_sel:[1,0,0] op_sel_hi:[1,0,0]
	v_fma_mix_f32 v207, v133, v133, v207 op_sel:[1,1,0] op_sel_hi:[1,1,0]
	v_fma_mix_f32 v206, v134, 1.0, v206 op_sel_hi:[1,0,0]
	v_fma_mix_f32 v207, v134, v134, v207 op_sel_hi:[1,1,0]
	v_fma_mix_f32 v206, v134, 1.0, v206 op_sel:[1,0,0] op_sel_hi:[1,0,0]
	v_fma_mix_f32 v207, v134, v134, v207 op_sel:[1,1,0] op_sel_hi:[1,1,0]
	v_fma_mix_f32 v206, v135, 1.0, v206 op_sel_hi:[1,0,0]
	v_fma_mix_f32 v207, v135, v135, v207 op_sel_hi:[1,1,0]
	v_fma_mix_f32 v206, v135, 1.0, v206 op_sel:[1,0,0] op_sel_hi:[1,0,0]
	v_fma_mix_f32 v207, v135, v135, v207 op_sel:[1,1,0] op_sel_hi:[1,1,0]
	ds_read_b128 v[88:91], v236
	ds_read_b128 v[92:95], v236 offset:1152
	s_waitcnt vmcnt(9)
	v_cvt_f32_f16_e32 v72, v216
	v_cvt_f32_f16_sdwa v73, v216 dst_sel:DWORD dst_unused:UNUSED_PAD src0_sel:WORD_1
	v_cvt_f32_f16_e32 v74, v217
	v_cvt_f32_f16_sdwa v75, v217 dst_sel:DWORD dst_unused:UNUSED_PAD src0_sel:WORD_1
	v_cvt_f32_f16_e32 v80, v218
	v_cvt_f32_f16_sdwa v81, v218 dst_sel:DWORD dst_unused:UNUSED_PAD src0_sel:WORD_1
	v_cvt_f32_f16_e32 v82, v219
	v_cvt_f32_f16_sdwa v83, v219 dst_sel:DWORD dst_unused:UNUSED_PAD src0_sel:WORD_1
	v_sub_f32_e32 v72, v72, v192
	v_sub_f32_e32 v73, v73, v192
	v_sub_f32_e32 v74, v74, v192
	v_sub_f32_e32 v75, v75, v192
	v_sub_f32_e32 v80, v80, v192
	v_sub_f32_e32 v81, v81, v192
	v_sub_f32_e32 v82, v82, v192
	v_sub_f32_e32 v83, v83, v192
	v_pk_mul_f32 v[72:73], v[192:193], v[72:73] op_sel:[1,0]
	v_pk_mul_f32 v[74:75], v[192:193], v[74:75] op_sel:[1,0]
	v_pk_mul_f32 v[80:81], v[192:193], v[80:81] op_sel:[1,0]
	v_pk_mul_f32 v[82:83], v[192:193], v[82:83] op_sel:[1,0]
	v_pk_fma_f32 v[124:125], v[72:73], v[160:161], v[124:125]
	v_pk_fma_f32 v[126:127], v[74:75], v[162:163], v[126:127]
	v_pk_fma_f32 v[120:121], v[80:81], v[164:165], v[120:121]
	v_pk_fma_f32 v[122:123], v[82:83], v[166:167], v[122:123]
	v_cvt_pk_f16_f32 v124, v124, v125
	v_cvt_pk_f16_f32 v125, v126, v127
	v_cvt_pk_f16_f32 v126, v120, v121
	v_cvt_pk_f16_f32 v127, v122, v123
	s_waitcnt lgkmcnt(0)
	buffer_store_dwordx4 v[88:91], v224, s[24:27], 0 offen nt
	v_add_u32_e32 v82, 0x3000, v224
	buffer_store_dwordx4 v[92:95], v82, s[24:27], 0 offen nt
	ds_write_b128 v235, v[124:127]
	v_fma_mix_f32 v140, v124, 1.0, 0 op_sel_hi:[1,0,0]
	v_fma_mix_f32 v141, v124, v124, 0 op_sel_hi:[1,1,0]
	v_fma_mix_f32 v140, v124, 1.0, v140 op_sel:[1,0,0] op_sel_hi:[1,0,0]
	v_fma_mix_f32 v141, v124, v124, v141 op_sel:[1,1,0] op_sel_hi:[1,1,0]
	v_fma_mix_f32 v140, v125, 1.0, v140 op_sel_hi:[1,0,0]
	v_fma_mix_f32 v141, v125, v125, v141 op_sel_hi:[1,1,0]
	v_fma_mix_f32 v140, v125, 1.0, v140 op_sel:[1,0,0] op_sel_hi:[1,0,0]
	v_fma_mix_f32 v141, v125, v125, v141 op_sel:[1,1,0] op_sel_hi:[1,1,0]
	v_fma_mix_f32 v140, v126, 1.0, v140 op_sel_hi:[1,0,0]
	v_fma_mix_f32 v141, v126, v126, v141 op_sel_hi:[1,1,0]
	v_fma_mix_f32 v140, v126, 1.0, v140 op_sel:[1,0,0] op_sel_hi:[1,0,0]
	v_fma_mix_f32 v141, v126, v126, v141 op_sel:[1,1,0] op_sel_hi:[1,1,0]
	v_fma_mix_f32 v140, v127, 1.0, v140 op_sel_hi:[1,0,0]
	v_fma_mix_f32 v141, v127, v127, v141 op_sel_hi:[1,1,0]
	v_fma_mix_f32 v140, v127, 1.0, v140 op_sel:[1,0,0] op_sel_hi:[1,0,0]
	v_fma_mix_f32 v141, v127, v127, v141 op_sel:[1,1,0] op_sel_hi:[1,1,0]
	s_waitcnt vmcnt(10)
	v_cvt_f32_f16_e32 v72, v220
	v_cvt_f32_f16_sdwa v73, v220 dst_sel:DWORD dst_unused:UNUSED_PAD src0_sel:WORD_1
	v_cvt_f32_f16_e32 v74, v221
	v_cvt_f32_f16_sdwa v75, v221 dst_sel:DWORD dst_unused:UNUSED_PAD src0_sel:WORD_1
	v_cvt_f32_f16_e32 v80, v222
	v_cvt_f32_f16_sdwa v81, v222 dst_sel:DWORD dst_unused:UNUSED_PAD src0_sel:WORD_1
	v_cvt_f32_f16_e32 v82, v223
	v_cvt_f32_f16_sdwa v83, v223 dst_sel:DWORD dst_unused:UNUSED_PAD src0_sel:WORD_1
	v_sub_f32_e32 v72, v72, v192
	v_sub_f32_e32 v73, v73, v192
	v_sub_f32_e32 v74, v74, v192
	v_sub_f32_e32 v75, v75, v192
	v_sub_f32_e32 v80, v80, v192
	v_sub_f32_e32 v81, v81, v192
	v_sub_f32_e32 v82, v82, v192
	v_sub_f32_e32 v83, v83, v192
	v_pk_mul_f32 v[72:73], v[192:193], v[72:73] op_sel:[1,0]
	v_pk_mul_f32 v[74:75], v[192:193], v[74:75] op_sel:[1,0]
	v_pk_mul_f32 v[80:81], v[192:193], v[80:81] op_sel:[1,0]
	v_pk_mul_f32 v[82:83], v[192:193], v[82:83] op_sel:[1,0]
	v_pk_fma_f32 v[116:117], v[72:73], v[168:169], v[116:117]
	v_pk_fma_f32 v[118:119], v[74:75], v[170:171], v[118:119]
	v_pk_fma_f32 v[112:113], v[80:81], v[172:173], v[112:113]
	v_pk_fma_f32 v[114:115], v[82:83], v[174:175], v[114:115]
	v_cvt_pk_f16_f32 v116, v116, v117
	v_cvt_pk_f16_f32 v117, v118, v119
	v_cvt_pk_f16_f32 v118, v112, v113
	v_cvt_pk_f16_f32 v119, v114, v115
	ds_write_b128 v235, v[116:119] offset:64
	v_fma_mix_f32 v140, v116, 1.0, v140 op_sel_hi:[1,0,0]
	v_fma_mix_f32 v141, v116, v116, v141 op_sel_hi:[1,1,0]
	v_fma_mix_f32 v140, v116, 1.0, v140 op_sel:[1,0,0] op_sel_hi:[1,0,0]
	v_fma_mix_f32 v141, v116, v116, v141 op_sel:[1,1,0] op_sel_hi:[1,1,0]
	v_fma_mix_f32 v140, v117, 1.0, v140 op_sel_hi:[1,0,0]
	v_fma_mix_f32 v141, v117, v117, v141 op_sel_hi:[1,1,0]
	v_fma_mix_f32 v140, v117, 1.0, v140 op_sel:[1,0,0] op_sel_hi:[1,0,0]
	v_fma_mix_f32 v141, v117, v117, v141 op_sel:[1,1,0] op_sel_hi:[1,1,0]
	v_fma_mix_f32 v140, v118, 1.0, v140 op_sel_hi:[1,0,0]
	v_fma_mix_f32 v141, v118, v118, v141 op_sel_hi:[1,1,0]
	v_fma_mix_f32 v140, v118, 1.0, v140 op_sel:[1,0,0] op_sel_hi:[1,0,0]
	v_fma_mix_f32 v141, v118, v118, v141 op_sel:[1,1,0] op_sel_hi:[1,1,0]
	v_fma_mix_f32 v140, v119, 1.0, v140 op_sel_hi:[1,0,0]
	v_fma_mix_f32 v141, v119, v119, v141 op_sel_hi:[1,1,0]
	v_fma_mix_f32 v140, v119, 1.0, v140 op_sel:[1,0,0] op_sel_hi:[1,0,0]
	v_fma_mix_f32 v141, v119, v119, v141 op_sel:[1,1,0] op_sel_hi:[1,1,0]
	ds_read_b128 v[208:211], v236
	ds_read_b128 v[128:131], v236 offset:1152
	s_add_u32 s94, s98, 0x3c000
	s_addc_u32 s95, s99, 0
	global_load_dwordx4 v[212:215], v191, s[94:95] offset:0 nt
	global_load_dwordx4 v[144:147], v191, s[94:95] offset:64 nt
	s_add_u32 s94, s98, 0x42000
	s_addc_u32 s95, s99, 0
	global_load_dwordx4 v[132:135], v191, s[94:95] offset:0 nt
	global_load_dwordx4 v[88:91], v191, s[94:95] offset:64 nt
	s_waitcnt vmcnt(13)
	v_cvt_f32_f16_e32 v72, v240
	v_cvt_f32_f16_sdwa v73, v240 dst_sel:DWORD dst_unused:UNUSED_PAD src0_sel:WORD_1
	v_cvt_f32_f16_e32 v74, v241
	v_cvt_f32_f16_sdwa v75, v241 dst_sel:DWORD dst_unused:UNUSED_PAD src0_sel:WORD_1
	v_cvt_f32_f16_e32 v80, v242
	v_cvt_f32_f16_sdwa v81, v242 dst_sel:DWORD dst_unused:UNUSED_PAD src0_sel:WORD_1
	v_cvt_f32_f16_e32 v82, v243
	v_cvt_f32_f16_sdwa v83, v243 dst_sel:DWORD dst_unused:UNUSED_PAD src0_sel:WORD_1
	v_sub_f32_e32 v72, v72, v194
	v_sub_f32_e32 v73, v73, v194
	v_sub_f32_e32 v74, v74, v194
	v_sub_f32_e32 v75, v75, v194
	v_sub_f32_e32 v80, v80, v194
	v_sub_f32_e32 v81, v81, v194
	v_sub_f32_e32 v82, v82, v194
	v_sub_f32_e32 v83, v83, v194
	v_pk_mul_f32 v[72:73], v[194:195], v[72:73] op_sel:[1,0]
	v_pk_mul_f32 v[74:75], v[194:195], v[74:75] op_sel:[1,0]
	v_pk_mul_f32 v[80:81], v[194:195], v[80:81] op_sel:[1,0]
	v_pk_mul_f32 v[82:83], v[194:195], v[82:83] op_sel:[1,0]
	v_pk_fma_f32 v[108:109], v[72:73], v[160:161], v[108:109]
	v_pk_fma_f32 v[110:111], v[74:75], v[162:163], v[110:111]
	v_pk_fma_f32 v[104:105], v[80:81], v[164:165], v[104:105]
	v_pk_fma_f32 v[106:107], v[82:83], v[166:167], v[106:107]
	v_cvt_pk_f16_f32 v108, v108, v109
	v_cvt_pk_f16_f32 v109, v110, v111
	v_cvt_pk_f16_f32 v110, v104, v105
	v_cvt_pk_f16_f32 v111, v106, v107
	s_waitcnt lgkmcnt(0)
	v_add_u32_e32 v83, 0x6000, v224
	buffer_store_dwordx4 v[208:211], v83, s[24:27], 0 offen nt
	v_add_u32_e32 v82, 0x9000, v224
	buffer_store_dwordx4 v[128:131], v82, s[24:27], 0 offen nt
	ds_write_b128 v235, v[108:111]
	v_fma_mix_f32 v142, v108, 1.0, 0 op_sel_hi:[1,0,0]
	v_fma_mix_f32 v143, v108, v108, 0 op_sel_hi:[1,1,0]
	v_fma_mix_f32 v142, v108, 1.0, v142 op_sel:[1,0,0] op_sel_hi:[1,0,0]
	v_fma_mix_f32 v143, v108, v108, v143 op_sel:[1,1,0] op_sel_hi:[1,1,0]
	v_fma_mix_f32 v142, v109, 1.0, v142 op_sel_hi:[1,0,0]
	v_fma_mix_f32 v143, v109, v109, v143 op_sel_hi:[1,1,0]
	v_fma_mix_f32 v142, v109, 1.0, v142 op_sel:[1,0,0] op_sel_hi:[1,0,0]
	v_fma_mix_f32 v143, v109, v109, v143 op_sel:[1,1,0] op_sel_hi:[1,1,0]
	v_fma_mix_f32 v142, v110, 1.0, v142 op_sel_hi:[1,0,0]
	v_fma_mix_f32 v143, v110, v110, v143 op_sel_hi:[1,1,0]
	v_fma_mix_f32 v142, v110, 1.0, v142 op_sel:[1,0,0] op_sel_hi:[1,0,0]
	v_fma_mix_f32 v143, v110, v110, v143 op_sel:[1,1,0] op_sel_hi:[1,1,0]
	v_fma_mix_f32 v142, v111, 1.0, v142 op_sel_hi:[1,0,0]
	v_fma_mix_f32 v143, v111, v111, v143 op_sel_hi:[1,1,0]
	v_fma_mix_f32 v142, v111, 1.0, v142 op_sel:[1,0,0] op_sel_hi:[1,0,0]
	v_fma_mix_f32 v143, v111, v111, v143 op_sel:[1,1,0] op_sel_hi:[1,1,0]
	s_waitcnt vmcnt(14)
	v_cvt_f32_f16_e32 v72, v244
	v_cvt_f32_f16_sdwa v73, v244 dst_sel:DWORD dst_unused:UNUSED_PAD src0_sel:WORD_1
	v_cvt_f32_f16_e32 v74, v245
	v_cvt_f32_f16_sdwa v75, v245 dst_sel:DWORD dst_unused:UNUSED_PAD src0_sel:WORD_1
	v_cvt_f32_f16_e32 v80, v246
	v_cvt_f32_f16_sdwa v81, v246 dst_sel:DWORD dst_unused:UNUSED_PAD src0_sel:WORD_1
	v_cvt_f32_f16_e32 v82, v247
	v_cvt_f32_f16_sdwa v83, v247 dst_sel:DWORD dst_unused:UNUSED_PAD src0_sel:WORD_1
	v_sub_f32_e32 v72, v72, v194
	v_sub_f32_e32 v73, v73, v194
	v_sub_f32_e32 v74, v74, v194
	v_sub_f32_e32 v75, v75, v194
	v_sub_f32_e32 v80, v80, v194
	v_sub_f32_e32 v81, v81, v194
	v_sub_f32_e32 v82, v82, v194
	v_sub_f32_e32 v83, v83, v194
	v_pk_mul_f32 v[72:73], v[194:195], v[72:73] op_sel:[1,0]
	v_pk_mul_f32 v[74:75], v[194:195], v[74:75] op_sel:[1,0]
	v_pk_mul_f32 v[80:81], v[194:195], v[80:81] op_sel:[1,0]
	v_pk_mul_f32 v[82:83], v[194:195], v[82:83] op_sel:[1,0]
	v_pk_fma_f32 v[100:101], v[72:73], v[168:169], v[100:101]
	v_pk_fma_f32 v[102:103], v[74:75], v[170:171], v[102:103]
	v_pk_fma_f32 v[96:97], v[80:81], v[172:173], v[96:97]
	v_pk_fma_f32 v[98:99], v[82:83], v[174:175], v[98:99]
	v_cvt_pk_f16_f32 v100, v100, v101
	v_cvt_pk_f16_f32 v101, v102, v103
	v_cvt_pk_f16_f32 v102, v96, v97
	v_cvt_pk_f16_f32 v103, v98, v99
	ds_write_b128 v235, v[100:103] offset:64
	v_fma_mix_f32 v142, v100, 1.0, v142 op_sel_hi:[1,0,0]
	v_fma_mix_f32 v143, v100, v100, v143 op_sel_hi:[1,1,0]
	v_fma_mix_f32 v142, v100, 1.0, v142 op_sel:[1,0,0] op_sel_hi:[1,0,0]
	v_fma_mix_f32 v143, v100, v100, v143 op_sel:[1,1,0] op_sel_hi:[1,1,0]
	v_fma_mix_f32 v142, v101, 1.0, v142 op_sel_hi:[1,0,0]
	v_fma_mix_f32 v143, v101, v101, v143 op_sel_hi:[1,1,0]
	v_fma_mix_f32 v142, v101, 1.0, v142 op_sel:[1,0,0] op_sel_hi:[1,0,0]
	v_fma_mix_f32 v143, v101, v101, v143 op_sel:[1,1,0] op_sel_hi:[1,1,0]
	v_fma_mix_f32 v142, v102, 1.0, v142 op_sel_hi:[1,0,0]
	v_fma_mix_f32 v143, v102, v102, v143 op_sel_hi:[1,1,0]
	v_fma_mix_f32 v142, v102, 1.0, v142 op_sel:[1,0,0] op_sel_hi:[1,0,0]
	v_fma_mix_f32 v143, v102, v102, v143 op_sel:[1,1,0] op_sel_hi:[1,1,0]
	v_fma_mix_f32 v142, v103, 1.0, v142 op_sel_hi:[1,0,0]
	v_fma_mix_f32 v143, v103, v103, v143 op_sel_hi:[1,1,0]
	v_fma_mix_f32 v142, v103, 1.0, v142 op_sel:[1,0,0] op_sel_hi:[1,0,0]
	v_fma_mix_f32 v143, v103, v103, v143 op_sel:[1,1,0] op_sel_hi:[1,1,0]
	ds_read_b128 v[92:95], v236
	ds_read_b128 v[120:123], v236 offset:1152
	s_waitcnt vmcnt(13)
	v_cvt_f32_f16_e32 v72, v248
	v_cvt_f32_f16_sdwa v73, v248 dst_sel:DWORD dst_unused:UNUSED_PAD src0_sel:WORD_1
	v_cvt_f32_f16_e32 v74, v249
	v_cvt_f32_f16_sdwa v75, v249 dst_sel:DWORD dst_unused:UNUSED_PAD src0_sel:WORD_1
	v_cvt_f32_f16_e32 v80, v250
	v_cvt_f32_f16_sdwa v81, v250 dst_sel:DWORD dst_unused:UNUSED_PAD src0_sel:WORD_1
	v_cvt_f32_f16_e32 v82, v251
	v_cvt_f32_f16_sdwa v83, v251 dst_sel:DWORD dst_unused:UNUSED_PAD src0_sel:WORD_1
	v_sub_f32_e32 v72, v72, v196
	v_sub_f32_e32 v73, v73, v196
	v_sub_f32_e32 v74, v74, v196
	v_sub_f32_e32 v75, v75, v196
	v_sub_f32_e32 v80, v80, v196
	v_sub_f32_e32 v81, v81, v196
	v_sub_f32_e32 v82, v82, v196
	v_sub_f32_e32 v83, v83, v196
	v_pk_mul_f32 v[72:73], v[196:197], v[72:73] op_sel:[1,0]
	v_pk_mul_f32 v[74:75], v[196:197], v[74:75] op_sel:[1,0]
	v_pk_mul_f32 v[80:81], v[196:197], v[80:81] op_sel:[1,0]
	v_pk_mul_f32 v[82:83], v[196:197], v[82:83] op_sel:[1,0]
	v_pk_fma_f32 v[84:85], v[72:73], v[160:161], v[84:85]
	v_pk_fma_f32 v[86:87], v[74:75], v[162:163], v[86:87]
	v_pk_fma_f32 v[76:77], v[80:81], v[164:165], v[76:77]
	v_pk_fma_f32 v[78:79], v[82:83], v[166:167], v[78:79]
	v_cvt_pk_f16_f32 v84, v84, v85
	v_cvt_pk_f16_f32 v85, v86, v87
	v_cvt_pk_f16_f32 v86, v76, v77
	v_cvt_pk_f16_f32 v87, v78, v79
	s_waitcnt lgkmcnt(0)
	v_add_u32_e32 v83, 0xc000, v224
	buffer_store_dwordx4 v[92:95], v83, s[24:27], 0 offen nt
	v_add_u32_e32 v82, 0xf000, v224
	buffer_store_dwordx4 v[120:123], v82, s[24:27], 0 offen nt
	ds_write_b128 v235, v[84:87]
	v_fma_mix_f32 v216, v84, 1.0, 0 op_sel_hi:[1,0,0]
	v_fma_mix_f32 v217, v84, v84, 0 op_sel_hi:[1,1,0]
	v_fma_mix_f32 v216, v84, 1.0, v216 op_sel:[1,0,0] op_sel_hi:[1,0,0]
	v_fma_mix_f32 v217, v84, v84, v217 op_sel:[1,1,0] op_sel_hi:[1,1,0]
	v_fma_mix_f32 v216, v85, 1.0, v216 op_sel_hi:[1,0,0]
	v_fma_mix_f32 v217, v85, v85, v217 op_sel_hi:[1,1,0]
	v_fma_mix_f32 v216, v85, 1.0, v216 op_sel:[1,0,0] op_sel_hi:[1,0,0]
	v_fma_mix_f32 v217, v85, v85, v217 op_sel:[1,1,0] op_sel_hi:[1,1,0]
	v_fma_mix_f32 v216, v86, 1.0, v216 op_sel_hi:[1,0,0]
	v_fma_mix_f32 v217, v86, v86, v217 op_sel_hi:[1,1,0]
	v_fma_mix_f32 v216, v86, 1.0, v216 op_sel:[1,0,0] op_sel_hi:[1,0,0]
	v_fma_mix_f32 v217, v86, v86, v217 op_sel:[1,1,0] op_sel_hi:[1,1,0]
	v_fma_mix_f32 v216, v87, 1.0, v216 op_sel_hi:[1,0,0]
	v_fma_mix_f32 v217, v87, v87, v217 op_sel_hi:[1,1,0]
	v_fma_mix_f32 v216, v87, 1.0, v216 op_sel:[1,0,0] op_sel_hi:[1,0,0]
	v_fma_mix_f32 v217, v87, v87, v217 op_sel:[1,1,0] op_sel_hi:[1,1,0]
	s_waitcnt vmcnt(14)
	v_cvt_f32_f16_e32 v72, v252
	v_cvt_f32_f16_sdwa v73, v252 dst_sel:DWORD dst_unused:UNUSED_PAD src0_sel:WORD_1
	v_cvt_f32_f16_e32 v74, v253
	v_cvt_f32_f16_sdwa v75, v253 dst_sel:DWORD dst_unused:UNUSED_PAD src0_sel:WORD_1
	v_cvt_f32_f16_e32 v80, v254
	v_cvt_f32_f16_sdwa v81, v254 dst_sel:DWORD dst_unused:UNUSED_PAD src0_sel:WORD_1
	v_cvt_f32_f16_e32 v82, v255
	v_cvt_f32_f16_sdwa v83, v255 dst_sel:DWORD dst_unused:UNUSED_PAD src0_sel:WORD_1
	v_sub_f32_e32 v72, v72, v196
	v_sub_f32_e32 v73, v73, v196
	v_sub_f32_e32 v74, v74, v196
	v_sub_f32_e32 v75, v75, v196
	v_sub_f32_e32 v80, v80, v196
	v_sub_f32_e32 v81, v81, v196
	v_sub_f32_e32 v82, v82, v196
	v_sub_f32_e32 v83, v83, v196
	v_pk_mul_f32 v[72:73], v[196:197], v[72:73] op_sel:[1,0]
	v_pk_mul_f32 v[74:75], v[196:197], v[74:75] op_sel:[1,0]
	v_pk_mul_f32 v[80:81], v[196:197], v[80:81] op_sel:[1,0]
	v_pk_mul_f32 v[82:83], v[196:197], v[82:83] op_sel:[1,0]
	v_pk_fma_f32 v[68:69], v[72:73], v[168:169], v[68:69]
	v_pk_fma_f32 v[70:71], v[74:75], v[170:171], v[70:71]
	v_pk_fma_f32 v[64:65], v[80:81], v[172:173], v[64:65]
	v_pk_fma_f32 v[66:67], v[82:83], v[174:175], v[66:67]
	v_cvt_pk_f16_f32 v68, v68, v69
	v_cvt_pk_f16_f32 v69, v70, v71
	v_cvt_pk_f16_f32 v70, v64, v65
	v_cvt_pk_f16_f32 v71, v66, v67
	ds_write_b128 v235, v[68:71] offset:64
	v_fma_mix_f32 v216, v68, 1.0, v216 op_sel_hi:[1,0,0]
	v_fma_mix_f32 v217, v68, v68, v217 op_sel_hi:[1,1,0]
	v_fma_mix_f32 v216, v68, 1.0, v216 op_sel:[1,0,0] op_sel_hi:[1,0,0]
	v_fma_mix_f32 v217, v68, v68, v217 op_sel:[1,1,0] op_sel_hi:[1,1,0]
	v_fma_mix_f32 v216, v69, 1.0, v216 op_sel_hi:[1,0,0]
	v_fma_mix_f32 v217, v69, v69, v217 op_sel_hi:[1,1,0]
	v_fma_mix_f32 v216, v69, 1.0, v216 op_sel:[1,0,0] op_sel_hi:[1,0,0]
	v_fma_mix_f32 v217, v69, v69, v217 op_sel:[1,1,0] op_sel_hi:[1,1,0]
	v_fma_mix_f32 v216, v70, 1.0, v216 op_sel_hi:[1,0,0]
	v_fma_mix_f32 v217, v70, v70, v217 op_sel_hi:[1,1,0]
	v_fma_mix_f32 v216, v70, 1.0, v216 op_sel:[1,0,0] op_sel_hi:[1,0,0]
	v_fma_mix_f32 v217, v70, v70, v217 op_sel:[1,1,0] op_sel_hi:[1,1,0]
	v_fma_mix_f32 v216, v71, 1.0, v216 op_sel_hi:[1,0,0]
	v_fma_mix_f32 v217, v71, v71, v217 op_sel_hi:[1,1,0]
	v_fma_mix_f32 v216, v71, 1.0, v216 op_sel:[1,0,0] op_sel_hi:[1,0,0]
	v_fma_mix_f32 v217, v71, v71, v217 op_sel:[1,1,0] op_sel_hi:[1,1,0]
	ds_read_b128 v[112:115], v236
	ds_read_b128 v[220:223], v236 offset:1152
	s_waitcnt vmcnt(13)
	v_cvt_f32_f16_e32 v72, v136
	v_cvt_f32_f16_sdwa v73, v136 dst_sel:DWORD dst_unused:UNUSED_PAD src0_sel:WORD_1
	v_cvt_f32_f16_e32 v74, v137
	v_cvt_f32_f16_sdwa v75, v137 dst_sel:DWORD dst_unused:UNUSED_PAD src0_sel:WORD_1
	v_cvt_f32_f16_e32 v80, v138
	v_cvt_f32_f16_sdwa v81, v138 dst_sel:DWORD dst_unused:UNUSED_PAD src0_sel:WORD_1
	v_cvt_f32_f16_e32 v82, v139
	v_cvt_f32_f16_sdwa v83, v139 dst_sel:DWORD dst_unused:UNUSED_PAD src0_sel:WORD_1
	v_sub_f32_e32 v72, v72, v198
	v_sub_f32_e32 v73, v73, v198
	v_sub_f32_e32 v74, v74, v198
	v_sub_f32_e32 v75, v75, v198
	v_sub_f32_e32 v80, v80, v198
	v_sub_f32_e32 v81, v81, v198
	v_sub_f32_e32 v82, v82, v198
	v_sub_f32_e32 v83, v83, v198
	v_pk_mul_f32 v[72:73], v[198:199], v[72:73] op_sel:[1,0]
	v_pk_mul_f32 v[74:75], v[198:199], v[74:75] op_sel:[1,0]
	v_pk_mul_f32 v[80:81], v[198:199], v[80:81] op_sel:[1,0]
	v_pk_mul_f32 v[82:83], v[198:199], v[82:83] op_sel:[1,0]
	v_pk_fma_f32 v[60:61], v[72:73], v[160:161], v[60:61]
	v_pk_fma_f32 v[62:63], v[74:75], v[162:163], v[62:63]
	v_pk_fma_f32 v[56:57], v[80:81], v[164:165], v[56:57]
	v_pk_fma_f32 v[58:59], v[82:83], v[166:167], v[58:59]
	v_cvt_pk_f16_f32 v60, v60, v61
	v_cvt_pk_f16_f32 v61, v62, v63
	v_cvt_pk_f16_f32 v62, v56, v57
	v_cvt_pk_f16_f32 v63, v58, v59
	s_waitcnt lgkmcnt(0)
	v_add_u32_e32 v83, 0x12000, v224
	buffer_store_dwordx4 v[112:115], v83, s[24:27], 0 offen nt
	v_add_u32_e32 v82, 0x15000, v224
	buffer_store_dwordx4 v[220:223], v82, s[24:27], 0 offen nt
	ds_write_b128 v235, v[60:63]
	v_fma_mix_f32 v218, v60, 1.0, 0 op_sel_hi:[1,0,0]
	v_fma_mix_f32 v219, v60, v60, 0 op_sel_hi:[1,1,0]
	v_fma_mix_f32 v218, v60, 1.0, v218 op_sel:[1,0,0] op_sel_hi:[1,0,0]
	v_fma_mix_f32 v219, v60, v60, v219 op_sel:[1,1,0] op_sel_hi:[1,1,0]
	v_fma_mix_f32 v218, v61, 1.0, v218 op_sel_hi:[1,0,0]
	v_fma_mix_f32 v219, v61, v61, v219 op_sel_hi:[1,1,0]
	v_fma_mix_f32 v218, v61, 1.0, v218 op_sel:[1,0,0] op_sel_hi:[1,0,0]
	v_fma_mix_f32 v219, v61, v61, v219 op_sel:[1,1,0] op_sel_hi:[1,1,0]
	v_fma_mix_f32 v218, v62, 1.0, v218 op_sel_hi:[1,0,0]
	v_fma_mix_f32 v219, v62, v62, v219 op_sel_hi:[1,1,0]
	v_fma_mix_f32 v218, v62, 1.0, v218 op_sel:[1,0,0] op_sel_hi:[1,0,0]
	v_fma_mix_f32 v219, v62, v62, v219 op_sel:[1,1,0] op_sel_hi:[1,1,0]
	v_fma_mix_f32 v218, v63, 1.0, v218 op_sel_hi:[1,0,0]
	v_fma_mix_f32 v219, v63, v63, v219 op_sel_hi:[1,1,0]
	v_fma_mix_f32 v218, v63, 1.0, v218 op_sel:[1,0,0] op_sel_hi:[1,0,0]
	v_fma_mix_f32 v219, v63, v63, v219 op_sel:[1,1,0] op_sel_hi:[1,1,0]
	s_waitcnt vmcnt(14)
	v_cvt_f32_f16_e32 v72, v148
	v_cvt_f32_f16_sdwa v73, v148 dst_sel:DWORD dst_unused:UNUSED_PAD src0_sel:WORD_1
	v_cvt_f32_f16_e32 v74, v149
	v_cvt_f32_f16_sdwa v75, v149 dst_sel:DWORD dst_unused:UNUSED_PAD src0_sel:WORD_1
	v_cvt_f32_f16_e32 v80, v150
	v_cvt_f32_f16_sdwa v81, v150 dst_sel:DWORD dst_unused:UNUSED_PAD src0_sel:WORD_1
	v_cvt_f32_f16_e32 v82, v151
	v_cvt_f32_f16_sdwa v83, v151 dst_sel:DWORD dst_unused:UNUSED_PAD src0_sel:WORD_1
	v_sub_f32_e32 v72, v72, v198
	v_sub_f32_e32 v73, v73, v198
	v_sub_f32_e32 v74, v74, v198
	v_sub_f32_e32 v75, v75, v198
	v_sub_f32_e32 v80, v80, v198
	v_sub_f32_e32 v81, v81, v198
	v_sub_f32_e32 v82, v82, v198
	v_sub_f32_e32 v83, v83, v198
	v_pk_mul_f32 v[72:73], v[198:199], v[72:73] op_sel:[1,0]
	v_pk_mul_f32 v[74:75], v[198:199], v[74:75] op_sel:[1,0]
	v_pk_mul_f32 v[80:81], v[198:199], v[80:81] op_sel:[1,0]
	v_pk_mul_f32 v[82:83], v[198:199], v[82:83] op_sel:[1,0]
	v_pk_fma_f32 v[52:53], v[72:73], v[168:169], v[52:53]
	v_pk_fma_f32 v[54:55], v[74:75], v[170:171], v[54:55]
	v_pk_fma_f32 v[48:49], v[80:81], v[172:173], v[48:49]
	v_pk_fma_f32 v[50:51], v[82:83], v[174:175], v[50:51]
	v_cvt_pk_f16_f32 v52, v52, v53
	v_cvt_pk_f16_f32 v53, v54, v55
	v_cvt_pk_f16_f32 v54, v48, v49
	v_cvt_pk_f16_f32 v55, v50, v51
	ds_write_b128 v235, v[52:55] offset:64
	v_fma_mix_f32 v218, v52, 1.0, v218 op_sel_hi:[1,0,0]
	v_fma_mix_f32 v219, v52, v52, v219 op_sel_hi:[1,1,0]
	v_fma_mix_f32 v218, v52, 1.0, v218 op_sel:[1,0,0] op_sel_hi:[1,0,0]
	v_fma_mix_f32 v219, v52, v52, v219 op_sel:[1,1,0] op_sel_hi:[1,1,0]
	v_fma_mix_f32 v218, v53, 1.0, v218 op_sel_hi:[1,0,0]
	v_fma_mix_f32 v219, v53, v53, v219 op_sel_hi:[1,1,0]
	v_fma_mix_f32 v218, v53, 1.0, v218 op_sel:[1,0,0] op_sel_hi:[1,0,0]
	v_fma_mix_f32 v219, v53, v53, v219 op_sel:[1,1,0] op_sel_hi:[1,1,0]
	v_fma_mix_f32 v218, v54, 1.0, v218 op_sel_hi:[1,0,0]
	v_fma_mix_f32 v219, v54, v54, v219 op_sel_hi:[1,1,0]
	v_fma_mix_f32 v218, v54, 1.0, v218 op_sel:[1,0,0] op_sel_hi:[1,0,0]
	v_fma_mix_f32 v219, v54, v54, v219 op_sel:[1,1,0] op_sel_hi:[1,1,0]
	v_fma_mix_f32 v218, v55, 1.0, v218 op_sel_hi:[1,0,0]
	v_fma_mix_f32 v219, v55, v55, v219 op_sel_hi:[1,1,0]
	v_fma_mix_f32 v218, v55, 1.0, v218 op_sel:[1,0,0] op_sel_hi:[1,0,0]
	v_fma_mix_f32 v219, v55, v55, v219 op_sel:[1,1,0] op_sel_hi:[1,1,0]
	ds_read_b128 v[124:127], v236
	ds_read_b128 v[116:119], v236 offset:1152
	s_waitcnt vmcnt(13)
	v_cvt_f32_f16_e32 v72, v152
	v_cvt_f32_f16_sdwa v73, v152 dst_sel:DWORD dst_unused:UNUSED_PAD src0_sel:WORD_1
	v_cvt_f32_f16_e32 v74, v153
	v_cvt_f32_f16_sdwa v75, v153 dst_sel:DWORD dst_unused:UNUSED_PAD src0_sel:WORD_1
	v_cvt_f32_f16_e32 v80, v154
	v_cvt_f32_f16_sdwa v81, v154 dst_sel:DWORD dst_unused:UNUSED_PAD src0_sel:WORD_1
	v_cvt_f32_f16_e32 v82, v155
	v_cvt_f32_f16_sdwa v83, v155 dst_sel:DWORD dst_unused:UNUSED_PAD src0_sel:WORD_1
	v_sub_f32_e32 v72, v72, v200
	v_sub_f32_e32 v73, v73, v200
	v_sub_f32_e32 v74, v74, v200
	v_sub_f32_e32 v75, v75, v200
	v_sub_f32_e32 v80, v80, v200
	v_sub_f32_e32 v81, v81, v200
	v_sub_f32_e32 v82, v82, v200
	v_sub_f32_e32 v83, v83, v200
	v_pk_mul_f32 v[72:73], v[200:201], v[72:73] op_sel:[1,0]
	v_pk_mul_f32 v[74:75], v[200:201], v[74:75] op_sel:[1,0]
	v_pk_mul_f32 v[80:81], v[200:201], v[80:81] op_sel:[1,0]
	v_pk_mul_f32 v[82:83], v[200:201], v[82:83] op_sel:[1,0]
	v_pk_fma_f32 v[44:45], v[72:73], v[160:161], v[44:45]
	v_pk_fma_f32 v[46:47], v[74:75], v[162:163], v[46:47]
	v_pk_fma_f32 v[40:41], v[80:81], v[164:165], v[40:41]
	v_pk_fma_f32 v[42:43], v[82:83], v[166:167], v[42:43]
	v_cvt_pk_f16_f32 v44, v44, v45
	v_cvt_pk_f16_f32 v45, v46, v47
	v_cvt_pk_f16_f32 v46, v40, v41
	v_cvt_pk_f16_f32 v47, v42, v43
	s_waitcnt lgkmcnt(0)
	v_add_u32_e32 v83, 0x30000, v224
	buffer_store_dwordx4 v[124:127], v83, s[24:27], 0 offen nt
	v_add_u32_e32 v82, 0x33000, v224
	buffer_store_dwordx4 v[116:119], v82, s[24:27], 0 offen nt
	ds_write_b128 v235, v[44:47]
	v_fma_mix_f32 v208, v44, 1.0, 0 op_sel_hi:[1,0,0]
	v_fma_mix_f32 v209, v44, v44, 0 op_sel_hi:[1,1,0]
	v_fma_mix_f32 v208, v44, 1.0, v208 op_sel:[1,0,0] op_sel_hi:[1,0,0]
	v_fma_mix_f32 v209, v44, v44, v209 op_sel:[1,1,0] op_sel_hi:[1,1,0]
	v_fma_mix_f32 v208, v45, 1.0, v208 op_sel_hi:[1,0,0]
	v_fma_mix_f32 v209, v45, v45, v209 op_sel_hi:[1,1,0]
	v_fma_mix_f32 v208, v45, 1.0, v208 op_sel:[1,0,0] op_sel_hi:[1,0,0]
	v_fma_mix_f32 v209, v45, v45, v209 op_sel:[1,1,0] op_sel_hi:[1,1,0]
	v_fma_mix_f32 v208, v46, 1.0, v208 op_sel_hi:[1,0,0]
	v_fma_mix_f32 v209, v46, v46, v209 op_sel_hi:[1,1,0]
	v_fma_mix_f32 v208, v46, 1.0, v208 op_sel:[1,0,0] op_sel_hi:[1,0,0]
	v_fma_mix_f32 v209, v46, v46, v209 op_sel:[1,1,0] op_sel_hi:[1,1,0]
	v_fma_mix_f32 v208, v47, 1.0, v208 op_sel_hi:[1,0,0]
	v_fma_mix_f32 v209, v47, v47, v209 op_sel_hi:[1,1,0]
	v_fma_mix_f32 v208, v47, 1.0, v208 op_sel:[1,0,0] op_sel_hi:[1,0,0]
	v_fma_mix_f32 v209, v47, v47, v209 op_sel:[1,1,0] op_sel_hi:[1,1,0]
	s_waitcnt vmcnt(14)
	v_cvt_f32_f16_e32 v72, v156
	v_cvt_f32_f16_sdwa v73, v156 dst_sel:DWORD dst_unused:UNUSED_PAD src0_sel:WORD_1
	v_cvt_f32_f16_e32 v74, v157
	v_cvt_f32_f16_sdwa v75, v157 dst_sel:DWORD dst_unused:UNUSED_PAD src0_sel:WORD_1
	v_cvt_f32_f16_e32 v80, v158
	v_cvt_f32_f16_sdwa v81, v158 dst_sel:DWORD dst_unused:UNUSED_PAD src0_sel:WORD_1
	v_cvt_f32_f16_e32 v82, v159
	v_cvt_f32_f16_sdwa v83, v159 dst_sel:DWORD dst_unused:UNUSED_PAD src0_sel:WORD_1
	v_sub_f32_e32 v72, v72, v200
	v_sub_f32_e32 v73, v73, v200
	v_sub_f32_e32 v74, v74, v200
	v_sub_f32_e32 v75, v75, v200
	v_sub_f32_e32 v80, v80, v200
	v_sub_f32_e32 v81, v81, v200
	v_sub_f32_e32 v82, v82, v200
	v_sub_f32_e32 v83, v83, v200
	v_pk_mul_f32 v[72:73], v[200:201], v[72:73] op_sel:[1,0]
	v_pk_mul_f32 v[74:75], v[200:201], v[74:75] op_sel:[1,0]
	v_pk_mul_f32 v[80:81], v[200:201], v[80:81] op_sel:[1,0]
	v_pk_mul_f32 v[82:83], v[200:201], v[82:83] op_sel:[1,0]
	v_pk_fma_f32 v[36:37], v[72:73], v[168:169], v[36:37]
	v_pk_fma_f32 v[38:39], v[74:75], v[170:171], v[38:39]
	v_pk_fma_f32 v[32:33], v[80:81], v[172:173], v[32:33]
	v_pk_fma_f32 v[34:35], v[82:83], v[174:175], v[34:35]
	v_cvt_pk_f16_f32 v36, v36, v37
	v_cvt_pk_f16_f32 v37, v38, v39
	v_cvt_pk_f16_f32 v38, v32, v33
	v_cvt_pk_f16_f32 v39, v34, v35
	ds_write_b128 v235, v[36:39] offset:64
	v_fma_mix_f32 v208, v36, 1.0, v208 op_sel_hi:[1,0,0]
	v_fma_mix_f32 v209, v36, v36, v209 op_sel_hi:[1,1,0]
	v_fma_mix_f32 v208, v36, 1.0, v208 op_sel:[1,0,0] op_sel_hi:[1,0,0]
	v_fma_mix_f32 v209, v36, v36, v209 op_sel:[1,1,0] op_sel_hi:[1,1,0]
	v_fma_mix_f32 v208, v37, 1.0, v208 op_sel_hi:[1,0,0]
	v_fma_mix_f32 v209, v37, v37, v209 op_sel_hi:[1,1,0]
	v_fma_mix_f32 v208, v37, 1.0, v208 op_sel:[1,0,0] op_sel_hi:[1,0,0]
	v_fma_mix_f32 v209, v37, v37, v209 op_sel:[1,1,0] op_sel_hi:[1,1,0]
	v_fma_mix_f32 v208, v38, 1.0, v208 op_sel_hi:[1,0,0]
	v_fma_mix_f32 v209, v38, v38, v209 op_sel_hi:[1,1,0]
	v_fma_mix_f32 v208, v38, 1.0, v208 op_sel:[1,0,0] op_sel_hi:[1,0,0]
	v_fma_mix_f32 v209, v38, v38, v209 op_sel:[1,1,0] op_sel_hi:[1,1,0]
	v_fma_mix_f32 v208, v39, 1.0, v208 op_sel_hi:[1,0,0]
	v_fma_mix_f32 v209, v39, v39, v209 op_sel_hi:[1,1,0]
	v_fma_mix_f32 v208, v39, 1.0, v208 op_sel:[1,0,0] op_sel_hi:[1,0,0]
	v_fma_mix_f32 v209, v39, v39, v209 op_sel:[1,1,0] op_sel_hi:[1,1,0]
	ds_read_b128 v[128:131], v236
	ds_read_b128 v[104:107], v236 offset:1152
	s_waitcnt vmcnt(11)
	v_cvt_f32_f16_e32 v72, v212
	v_cvt_f32_f16_sdwa v73, v212 dst_sel:DWORD dst_unused:UNUSED_PAD src0_sel:WORD_1
	v_cvt_f32_f16_e32 v74, v213
	v_cvt_f32_f16_sdwa v75, v213 dst_sel:DWORD dst_unused:UNUSED_PAD src0_sel:WORD_1
	v_cvt_f32_f16_e32 v80, v214
	v_cvt_f32_f16_sdwa v81, v214 dst_sel:DWORD dst_unused:UNUSED_PAD src0_sel:WORD_1
	v_cvt_f32_f16_e32 v82, v215
	v_cvt_f32_f16_sdwa v83, v215 dst_sel:DWORD dst_unused:UNUSED_PAD src0_sel:WORD_1
	v_sub_f32_e32 v72, v72, v202
	v_sub_f32_e32 v73, v73, v202
	v_sub_f32_e32 v74, v74, v202
	v_sub_f32_e32 v75, v75, v202
	v_sub_f32_e32 v80, v80, v202
	v_sub_f32_e32 v81, v81, v202
	v_sub_f32_e32 v82, v82, v202
	v_sub_f32_e32 v83, v83, v202
	v_pk_mul_f32 v[72:73], v[202:203], v[72:73] op_sel:[1,0]
	v_pk_mul_f32 v[74:75], v[202:203], v[74:75] op_sel:[1,0]
	v_pk_mul_f32 v[80:81], v[202:203], v[80:81] op_sel:[1,0]
	v_pk_mul_f32 v[82:83], v[202:203], v[82:83] op_sel:[1,0]
	v_pk_fma_f32 v[28:29], v[72:73], v[160:161], v[28:29]
	v_pk_fma_f32 v[30:31], v[74:75], v[162:163], v[30:31]
	v_pk_fma_f32 v[24:25], v[80:81], v[164:165], v[24:25]
	v_pk_fma_f32 v[26:27], v[82:83], v[166:167], v[26:27]
	v_cvt_pk_f16_f32 v28, v28, v29
	v_cvt_pk_f16_f32 v29, v30, v31
	v_cvt_pk_f16_f32 v30, v24, v25
	v_cvt_pk_f16_f32 v31, v26, v27
	s_waitcnt lgkmcnt(0)
	v_add_u32_e32 v83, 0x36000, v224
	buffer_store_dwordx4 v[128:131], v83, s[24:27], 0 offen nt
	v_add_u32_e32 v82, 0x39000, v224
	buffer_store_dwordx4 v[104:107], v82, s[24:27], 0 offen nt
	ds_write_b128 v235, v[28:31]
	v_fma_mix_f32 v210, v28, 1.0, 0 op_sel_hi:[1,0,0]
	v_fma_mix_f32 v211, v28, v28, 0 op_sel_hi:[1,1,0]
	v_fma_mix_f32 v210, v28, 1.0, v210 op_sel:[1,0,0] op_sel_hi:[1,0,0]
	v_fma_mix_f32 v211, v28, v28, v211 op_sel:[1,1,0] op_sel_hi:[1,1,0]
	v_fma_mix_f32 v210, v29, 1.0, v210 op_sel_hi:[1,0,0]
	v_fma_mix_f32 v211, v29, v29, v211 op_sel_hi:[1,1,0]
	v_fma_mix_f32 v210, v29, 1.0, v210 op_sel:[1,0,0] op_sel_hi:[1,0,0]
	v_fma_mix_f32 v211, v29, v29, v211 op_sel:[1,1,0] op_sel_hi:[1,1,0]
	v_fma_mix_f32 v210, v30, 1.0, v210 op_sel_hi:[1,0,0]
	v_fma_mix_f32 v211, v30, v30, v211 op_sel_hi:[1,1,0]
	v_fma_mix_f32 v210, v30, 1.0, v210 op_sel:[1,0,0] op_sel_hi:[1,0,0]
	v_fma_mix_f32 v211, v30, v30, v211 op_sel:[1,1,0] op_sel_hi:[1,1,0]
	v_fma_mix_f32 v210, v31, 1.0, v210 op_sel_hi:[1,0,0]
	v_fma_mix_f32 v211, v31, v31, v211 op_sel_hi:[1,1,0]
	v_fma_mix_f32 v210, v31, 1.0, v210 op_sel:[1,0,0] op_sel_hi:[1,0,0]
	v_fma_mix_f32 v211, v31, v31, v211 op_sel:[1,1,0] op_sel_hi:[1,1,0]
	s_waitcnt vmcnt(12)
	v_cvt_f32_f16_e32 v72, v144
	v_cvt_f32_f16_sdwa v73, v144 dst_sel:DWORD dst_unused:UNUSED_PAD src0_sel:WORD_1
	v_cvt_f32_f16_e32 v74, v145
	v_cvt_f32_f16_sdwa v75, v145 dst_sel:DWORD dst_unused:UNUSED_PAD src0_sel:WORD_1
	v_cvt_f32_f16_e32 v80, v146
	v_cvt_f32_f16_sdwa v81, v146 dst_sel:DWORD dst_unused:UNUSED_PAD src0_sel:WORD_1
	v_cvt_f32_f16_e32 v82, v147
	v_cvt_f32_f16_sdwa v83, v147 dst_sel:DWORD dst_unused:UNUSED_PAD src0_sel:WORD_1
	v_sub_f32_e32 v72, v72, v202
	v_sub_f32_e32 v73, v73, v202
	v_sub_f32_e32 v74, v74, v202
	v_sub_f32_e32 v75, v75, v202
	v_sub_f32_e32 v80, v80, v202
	v_sub_f32_e32 v81, v81, v202
	v_sub_f32_e32 v82, v82, v202
	v_sub_f32_e32 v83, v83, v202
	v_pk_mul_f32 v[72:73], v[202:203], v[72:73] op_sel:[1,0]
	v_pk_mul_f32 v[74:75], v[202:203], v[74:75] op_sel:[1,0]
	v_pk_mul_f32 v[80:81], v[202:203], v[80:81] op_sel:[1,0]
	v_pk_mul_f32 v[82:83], v[202:203], v[82:83] op_sel:[1,0]
	v_pk_fma_f32 v[20:21], v[72:73], v[168:169], v[20:21]
	v_pk_fma_f32 v[22:23], v[74:75], v[170:171], v[22:23]
	v_pk_fma_f32 v[16:17], v[80:81], v[172:173], v[16:17]
	v_pk_fma_f32 v[18:19], v[82:83], v[174:175], v[18:19]
	v_cvt_pk_f16_f32 v20, v20, v21
	v_cvt_pk_f16_f32 v21, v22, v23
	v_cvt_pk_f16_f32 v22, v16, v17
	v_cvt_pk_f16_f32 v23, v18, v19
	ds_write_b128 v235, v[20:23] offset:64
	v_fma_mix_f32 v210, v20, 1.0, v210 op_sel_hi:[1,0,0]
	v_fma_mix_f32 v211, v20, v20, v211 op_sel_hi:[1,1,0]
	v_fma_mix_f32 v210, v20, 1.0, v210 op_sel:[1,0,0] op_sel_hi:[1,0,0]
	v_fma_mix_f32 v211, v20, v20, v211 op_sel:[1,1,0] op_sel_hi:[1,1,0]
	v_fma_mix_f32 v210, v21, 1.0, v210 op_sel_hi:[1,0,0]
	v_fma_mix_f32 v211, v21, v21, v211 op_sel_hi:[1,1,0]
	v_fma_mix_f32 v210, v21, 1.0, v210 op_sel:[1,0,0] op_sel_hi:[1,0,0]
	v_fma_mix_f32 v211, v21, v21, v211 op_sel:[1,1,0] op_sel_hi:[1,1,0]
	v_fma_mix_f32 v210, v22, 1.0, v210 op_sel_hi:[1,0,0]
	v_fma_mix_f32 v211, v22, v22, v211 op_sel_hi:[1,1,0]
	v_fma_mix_f32 v210, v22, 1.0, v210 op_sel:[1,0,0] op_sel_hi:[1,0,0]
	v_fma_mix_f32 v211, v22, v22, v211 op_sel:[1,1,0] op_sel_hi:[1,1,0]
	v_fma_mix_f32 v210, v23, 1.0, v210 op_sel_hi:[1,0,0]
	v_fma_mix_f32 v211, v23, v23, v211 op_sel_hi:[1,1,0]
	v_fma_mix_f32 v210, v23, 1.0, v210 op_sel:[1,0,0] op_sel_hi:[1,0,0]
	v_fma_mix_f32 v211, v23, v23, v211 op_sel:[1,1,0] op_sel_hi:[1,1,0]
	ds_read_b128 v[240:243], v236
	ds_read_b128 v[96:99], v236 offset:1152
	s_waitcnt vmcnt(11)
	v_cvt_f32_f16_e32 v72, v132
	v_cvt_f32_f16_sdwa v73, v132 dst_sel:DWORD dst_unused:UNUSED_PAD src0_sel:WORD_1
	v_cvt_f32_f16_e32 v74, v133
	v_cvt_f32_f16_sdwa v75, v133 dst_sel:DWORD dst_unused:UNUSED_PAD src0_sel:WORD_1
	v_cvt_f32_f16_e32 v80, v134
	v_cvt_f32_f16_sdwa v81, v134 dst_sel:DWORD dst_unused:UNUSED_PAD src0_sel:WORD_1
	v_cvt_f32_f16_e32 v82, v135
	v_cvt_f32_f16_sdwa v83, v135 dst_sel:DWORD dst_unused:UNUSED_PAD src0_sel:WORD_1
	v_sub_f32_e32 v72, v72, v204
	v_sub_f32_e32 v73, v73, v204
	v_sub_f32_e32 v74, v74, v204
	v_sub_f32_e32 v75, v75, v204
	v_sub_f32_e32 v80, v80, v204
	v_sub_f32_e32 v81, v81, v204
	v_sub_f32_e32 v82, v82, v204
	v_sub_f32_e32 v83, v83, v204
	v_pk_mul_f32 v[72:73], v[204:205], v[72:73] op_sel:[1,0]
	v_pk_mul_f32 v[74:75], v[204:205], v[74:75] op_sel:[1,0]
	v_pk_mul_f32 v[80:81], v[204:205], v[80:81] op_sel:[1,0]
	v_pk_mul_f32 v[82:83], v[204:205], v[82:83] op_sel:[1,0]
	v_pk_fma_f32 v[12:13], v[72:73], v[160:161], v[12:13]
	v_pk_fma_f32 v[14:15], v[74:75], v[162:163], v[14:15]
	v_pk_fma_f32 v[8:9], v[80:81], v[164:165], v[8:9]
	v_pk_fma_f32 v[10:11], v[82:83], v[166:167], v[10:11]
	v_cvt_pk_f16_f32 v12, v12, v13
	v_cvt_pk_f16_f32 v13, v14, v15
	v_cvt_pk_f16_f32 v14, v8, v9
	v_cvt_pk_f16_f32 v15, v10, v11
	s_waitcnt lgkmcnt(0)
	v_add_u32_e32 v83, 0x3c000, v224
	buffer_store_dwordx4 v[240:243], v83, s[24:27], 0 offen nt
	v_add_u32_e32 v82, 0x3f000, v224
	buffer_store_dwordx4 v[96:99], v82, s[24:27], 0 offen nt
	ds_write_b128 v235, v[12:15]
	v_fma_mix_f32 v244, v12, 1.0, 0 op_sel_hi:[1,0,0]
	v_fma_mix_f32 v245, v12, v12, 0 op_sel_hi:[1,1,0]
	v_fma_mix_f32 v244, v12, 1.0, v244 op_sel:[1,0,0] op_sel_hi:[1,0,0]
	v_fma_mix_f32 v245, v12, v12, v245 op_sel:[1,1,0] op_sel_hi:[1,1,0]
	v_fma_mix_f32 v244, v13, 1.0, v244 op_sel_hi:[1,0,0]
	v_fma_mix_f32 v245, v13, v13, v245 op_sel_hi:[1,1,0]
	v_fma_mix_f32 v244, v13, 1.0, v244 op_sel:[1,0,0] op_sel_hi:[1,0,0]
	v_fma_mix_f32 v245, v13, v13, v245 op_sel:[1,1,0] op_sel_hi:[1,1,0]
	v_fma_mix_f32 v244, v14, 1.0, v244 op_sel_hi:[1,0,0]
	v_fma_mix_f32 v245, v14, v14, v245 op_sel_hi:[1,1,0]
	v_fma_mix_f32 v244, v14, 1.0, v244 op_sel:[1,0,0] op_sel_hi:[1,0,0]
	v_fma_mix_f32 v245, v14, v14, v245 op_sel:[1,1,0] op_sel_hi:[1,1,0]
	v_fma_mix_f32 v244, v15, 1.0, v244 op_sel_hi:[1,0,0]
	v_fma_mix_f32 v245, v15, v15, v245 op_sel_hi:[1,1,0]
	v_fma_mix_f32 v244, v15, 1.0, v244 op_sel:[1,0,0] op_sel_hi:[1,0,0]
	v_fma_mix_f32 v245, v15, v15, v245 op_sel:[1,1,0] op_sel_hi:[1,1,0]
	s_waitcnt vmcnt(12)
	v_cvt_f32_f16_e32 v72, v88
	v_cvt_f32_f16_sdwa v73, v88 dst_sel:DWORD dst_unused:UNUSED_PAD src0_sel:WORD_1
	v_cvt_f32_f16_e32 v74, v89
	v_cvt_f32_f16_sdwa v75, v89 dst_sel:DWORD dst_unused:UNUSED_PAD src0_sel:WORD_1
	v_cvt_f32_f16_e32 v80, v90
	v_cvt_f32_f16_sdwa v81, v90 dst_sel:DWORD dst_unused:UNUSED_PAD src0_sel:WORD_1
	v_cvt_f32_f16_e32 v82, v91
	v_cvt_f32_f16_sdwa v83, v91 dst_sel:DWORD dst_unused:UNUSED_PAD src0_sel:WORD_1
	v_sub_f32_e32 v72, v72, v204
	v_sub_f32_e32 v73, v73, v204
	v_sub_f32_e32 v74, v74, v204
	v_sub_f32_e32 v75, v75, v204
	v_sub_f32_e32 v80, v80, v204
	v_sub_f32_e32 v81, v81, v204
	v_sub_f32_e32 v82, v82, v204
	v_sub_f32_e32 v83, v83, v204
	v_pk_mul_f32 v[72:73], v[204:205], v[72:73] op_sel:[1,0]
	v_pk_mul_f32 v[74:75], v[204:205], v[74:75] op_sel:[1,0]
	v_pk_mul_f32 v[80:81], v[204:205], v[80:81] op_sel:[1,0]
	v_pk_mul_f32 v[82:83], v[204:205], v[82:83] op_sel:[1,0]
	v_pk_fma_f32 v[4:5], v[72:73], v[168:169], v[4:5]
	v_pk_fma_f32 v[6:7], v[74:75], v[170:171], v[6:7]
	v_pk_fma_f32 v[0:1], v[80:81], v[172:173], v[0:1]
	v_pk_fma_f32 v[2:3], v[82:83], v[174:175], v[2:3]
	v_cvt_pk_f16_f32 v4, v4, v5
	v_cvt_pk_f16_f32 v5, v6, v7
	v_cvt_pk_f16_f32 v6, v0, v1
	v_cvt_pk_f16_f32 v7, v2, v3
	ds_write_b128 v235, v[4:7] offset:64
	v_fma_mix_f32 v244, v4, 1.0, v244 op_sel_hi:[1,0,0]
	v_fma_mix_f32 v245, v4, v4, v245 op_sel_hi:[1,1,0]
	v_fma_mix_f32 v244, v4, 1.0, v244 op_sel:[1,0,0] op_sel_hi:[1,0,0]
	v_fma_mix_f32 v245, v4, v4, v245 op_sel:[1,1,0] op_sel_hi:[1,1,0]
	v_fma_mix_f32 v244, v5, 1.0, v244 op_sel_hi:[1,0,0]
	v_fma_mix_f32 v245, v5, v5, v245 op_sel_hi:[1,1,0]
	v_fma_mix_f32 v244, v5, 1.0, v244 op_sel:[1,0,0] op_sel_hi:[1,0,0]
	v_fma_mix_f32 v245, v5, v5, v245 op_sel:[1,1,0] op_sel_hi:[1,1,0]
	v_fma_mix_f32 v244, v6, 1.0, v244 op_sel_hi:[1,0,0]
	v_fma_mix_f32 v245, v6, v6, v245 op_sel_hi:[1,1,0]
	v_fma_mix_f32 v244, v6, 1.0, v244 op_sel:[1,0,0] op_sel_hi:[1,0,0]
	v_fma_mix_f32 v245, v6, v6, v245 op_sel:[1,1,0] op_sel_hi:[1,1,0]
	v_fma_mix_f32 v244, v7, 1.0, v244 op_sel_hi:[1,0,0]
	v_fma_mix_f32 v245, v7, v7, v245 op_sel_hi:[1,1,0]
	v_fma_mix_f32 v244, v7, 1.0, v244 op_sel:[1,0,0] op_sel_hi:[1,0,0]
	v_fma_mix_f32 v245, v7, v7, v245 op_sel:[1,1,0] op_sel_hi:[1,1,0]
	ds_read_b128 v[108:111], v236
	ds_read_b128 v[100:103], v236 offset:1152
	s_waitcnt lgkmcnt(0)
	v_add_u32_e32 v83, 0x42000, v224
	buffer_store_dwordx4 v[108:111], v83, s[24:27], 0 offen nt
	v_add_u32_e32 v82, 0x45000, v224
	buffer_store_dwordx4 v[100:103], v82, s[24:27], 0 offen nt
	v_xor_b32_e32 v225, 16, v234
	v_lshlrev_b32_e32 v225, 2, v225
	v_xor_b32_e32 v246, 32, v234
	v_lshlrev_b32_e32 v246, 2, v246
	ds_bpermute_b32 v92, v225, v206
	ds_bpermute_b32 v93, v225, v207
	ds_bpermute_b32 v94, v225, v140
	ds_bpermute_b32 v95, v225, v141
	ds_bpermute_b32 v120, v225, v142
	ds_bpermute_b32 v121, v225, v143
	ds_bpermute_b32 v122, v225, v216
	ds_bpermute_b32 v123, v225, v217
	s_waitcnt lgkmcnt(0)
	v_pk_add_f32 v[206:207], v[206:207], v[92:93]
	v_pk_add_f32 v[140:141], v[140:141], v[94:95]
	v_pk_add_f32 v[142:143], v[142:143], v[120:121]
	v_pk_add_f32 v[216:217], v[216:217], v[122:123]
	ds_bpermute_b32 v92, v225, v218
	ds_bpermute_b32 v93, v225, v219
	ds_bpermute_b32 v94, v225, v208
	ds_bpermute_b32 v95, v225, v209
	ds_bpermute_b32 v120, v225, v210
	ds_bpermute_b32 v121, v225, v211
	ds_bpermute_b32 v122, v225, v244
	ds_bpermute_b32 v123, v225, v245
	s_waitcnt lgkmcnt(0)
	v_pk_add_f32 v[218:219], v[218:219], v[92:93]
	v_pk_add_f32 v[208:209], v[208:209], v[94:95]
	v_pk_add_f32 v[210:211], v[210:211], v[120:121]
	v_pk_add_f32 v[244:245], v[244:245], v[122:123]
	ds_bpermute_b32 v92, v246, v206
	ds_bpermute_b32 v93, v246, v207
	ds_bpermute_b32 v94, v246, v140
	ds_bpermute_b32 v95, v246, v141
	ds_bpermute_b32 v120, v246, v142
	ds_bpermute_b32 v121, v246, v143
	ds_bpermute_b32 v122, v246, v216
	ds_bpermute_b32 v123, v246, v217
	s_waitcnt lgkmcnt(0)
	v_pk_add_f32 v[206:207], v[206:207], v[92:93]
	v_pk_add_f32 v[140:141], v[140:141], v[94:95]
	v_pk_add_f32 v[142:143], v[142:143], v[120:121]
	v_pk_add_f32 v[216:217], v[216:217], v[122:123]
	ds_bpermute_b32 v92, v246, v218
	ds_bpermute_b32 v93, v246, v219
	ds_bpermute_b32 v94, v246, v208
	ds_bpermute_b32 v95, v246, v209
	ds_bpermute_b32 v120, v246, v210
	ds_bpermute_b32 v121, v246, v211
	ds_bpermute_b32 v122, v246, v244
	ds_bpermute_b32 v123, v246, v245
	s_waitcnt lgkmcnt(0)
	v_pk_add_f32 v[218:219], v[218:219], v[92:93]
	v_pk_add_f32 v[208:209], v[208:209], v[94:95]
	v_pk_add_f32 v[210:211], v[210:211], v[120:121]
	v_pk_add_f32 v[244:245], v[244:245], v[122:123]
	s_mov_b64 exec, 0xffff
	global_store_dwordx2 v190, v[206:207], s[100:101] offset:0
	global_store_dwordx2 v190, v[140:141], s[100:101] offset:128
	global_store_dwordx2 v190, v[142:143], s[100:101] offset:256
	global_store_dwordx2 v190, v[216:217], s[100:101] offset:384
	global_store_dwordx2 v190, v[218:219], s[100:101] offset:1024
	global_store_dwordx2 v190, v[208:209], s[100:101] offset:1152
	global_store_dwordx2 v190, v[210:211], s[100:101] offset:1280
	global_store_dwordx2 v190, v[244:245], s[100:101] offset:1408
	s_mov_b64 exec, -1
	s_mov_b32 s83, s81
	s_mov_b32 s84, s82
	s_mov_b64 s[40:41], s[0:1]
	s_mov_b64 s[38:39], s[8:9]
	s_mov_b64 vcc, s[6:7]
	s_cbranch_vccz .LBB8_12
	s_waitcnt vmcnt(0)
	s_cmpk_gt_u32 s44, 0xff
	s_cbranch_scc1 .LBB8_31
	s_barrier

.LBB9_11:
	s_mov_b64 s[26:27], 0x80
	s_and_b32 s22, s20, 3
	s_add_i32 m0, s43, 0x18000
	v_lshl_add_u64 v[8:9], v[8:9], 0, s[26:27]
	s_lshl_b32 s48, s21, 6
	s_lshl_b32 s21, s21, 13
	s_lshl_b32 s23, s22, 12
	s_waitcnt vmcnt(4)
	s_barrier
	global_load_lds_dwordx4 v[8:9], off
	v_lshl_add_u64 v[6:7], v[6:7], 0, s[26:27]
	s_add_i32 m0, s43, 0x1a000
	s_add_i32 s49, s43, 0x8000
	s_add_i32 s50, s43, 0xa000
	global_load_lds_dwordx4 v[6:7], off
	v_lshl_add_u64 v[4:5], v[4:5], 0, s[26:27]
	s_mov_b32 m0, s49
	s_add_u32 s0, s30, 0xc080
	global_load_lds_dwordx4 v[4:5], off
	v_lshl_add_u64 v[2:3], v[2:3], 0, s[26:27]
	s_mov_b32 m0, s50
	s_addc_u32 s1, s31, 0
	global_load_lds_dwordx4 v[2:3], off
	s_add_i32 m0, s43, 0x1c000
	v_lshl_add_u64 v[2:3], s[0:1], 0, v[146:147]
	global_load_lds_dwordx4 v[2:3], off
	v_lshl_add_u64 v[2:3], s[0:1], 0, v[150:151]
	s_add_i32 m0, s43, 0x1e000
	s_lshl_b32 s53, s33, 2
	global_load_lds_dwordx4 v[2:3], off
	s_abs_i32 s54, s53
	v_cvt_f32_u32_e32 v6, s54
	v_and_b32_e32 v167, 15, v0
	v_and_b32_e32 v2, 48, v0
	v_lshlrev_b32_e32 v4, 2, v0
	v_rcp_iflag_f32_e32 v6, v6
	v_lshlrev_b32_e32 v5, 6, v0
	v_bfe_u32 v169, v0, 3, 3
	v_and_b32_e32 v0, 7, v0
	s_abs_i32 s57, s33
	v_lshlrev_b32_e32 v170, 4, v0
	v_add_lshl_u32 v171, v0, s10, 4
	v_mul_f32_e32 v0, 0x4f7ffffe, v6
	v_cvt_f32_u32_e32 v6, s57
	s_movk_i32 s0, 0x3c0
	s_mulk_i32 s20, 0x900
	v_cvt_u32_f32_e32 v0, v0
	v_rcp_iflag_f32_e32 v6, v6
	v_and_or_b32 v5, v5, s0, v2
	s_add_i32 s0, s20, 0
	v_lshl_or_b32 v3, v167, 6, v2
	v_and_b32_e32 v4, 32, v4
	s_add_i32 s0, s0, 0x20000
	v_bitop3_b32 v3, v3, s21, v4 bitop3:0xde
	v_bitop3_b32 v168, s23, v5, v4 bitop3:0xf6
	s_movk_i32 s1, 0x90
	v_mov_b32_e32 v4, s0
	v_mad_u32_u24 v5, v167, s1, v4
	v_mad_u32_u24 v4, v169, s1, v4
	v_readfirstlane_b32 s1, v0
	v_mul_f32_e32 v0, 0x4f7ffffe, v6
	v_cvt_u32_f32_e32 v0, v0
	s_sub_i32 s0, 0, s54
	s_mul_i32 s0, s0, s1
	s_mul_hi_u32 s0, s1, s0
	s_add_i32 s59, s1, s0
	s_sub_i32 s0, 0, s57
	v_readfirstlane_b32 s1, v0
	s_waitcnt vmcnt(6)
	s_mul_i32 s0, s0, s1
	v_add_u16_e32 v0, v1, v10
	s_mul_hi_u32 s0, s1, s0
	v_lshrrev_b16_e32 v0, 1, v0
	s_add_i32 s65, 0, 0x10000
	s_add_i32 s66, 0, 0x14000
	s_mov_b32 s23, 0x20000
	s_lshl_b32 s51, s22, 6
	s_waitcnt lgkmcnt(0)
	s_ashr_i32 s52, s11, 31
	s_lshl_b32 s22, s10, 17
	s_and_b32 s21, s9, 0xffff
	s_mov_b32 s20, s8
	s_lshl_b32 s55, s10, 5
	s_mul_i32 s56, s10, 48
	s_bfe_i32 s58, s33, 0x1001c
	s_ashr_i32 s60, s33, 31
	s_add_i32 s61, s1, s0
	s_mul_i32 s62, s10, 0xc0
	s_mul_i32 s63, s10, 0x60
	s_lshl_b32 s64, s10, 4
	v_add_lshl_u32 v152, v11, v0, 1
	v_mov_b32_e32 v153, v147
	v_add_lshl_u32 v154, v12, v0, 1
	v_mov_b32_e32 v155, v147
	v_mov_b64_e32 v[156:157], s[6:7]
	v_add_u32_e32 v172, s65, v168
	v_add_u32_e32 v173, 0, v3
	v_add_u32_e32 v174, s66, v168
	v_add_u32_e32 v175, v5, v2
	v_add_u32_e32 v176, v4, v170
	s_barrier
	s_cmpk_gt_u32 s36, 0xff
	s_cbranch_scc0 .Lprio9_done
	s_setprio 1
.Lprio9_done:
.LBB9_12:
	s_add_i32 s47, s47, 1
	s_mul_i32 s0, s47, s52
	s_mul_hi_u32 s1, s47, s11
	s_add_i32 s1, s1, s0
	s_mul_i32 s0, s47, s11
	s_add_u32 s0, s0, s2
	s_addc_u32 s1, s1, s39
	v_cmp_ge_i64_e32 vcc, s[0:1], v[156:157]
	s_and_b64 s[6:7], exec, vcc
	s_mov_b64 vcc, s[6:7]
	s_cbranch_vccnz .LBB9_22
	s_ashr_i32 s8, s0, 31
	s_lshr_b32 s8, s8, 29
	s_add_i32 s34, s0, s8
	s_and_b32 s8, s34, -8
	s_sub_i32 s35, s0, s8
	s_cmp_ge_i32 s35, s38
	s_mov_b64 s[8:9], -1
	s_cbranch_scc0 .LBB9_15
	s_sub_i32 s8, s35, s38
	s_mul_i32 s8, s8, s37
	s_add_i32 s67, s8, s41
	s_mov_b64 s[8:9], 0

.LBB9_27:
	ds_read_b128 v[128:131], v172
	ds_read_b128 v[132:135], v172 offset:1024
	ds_read_b128 v[136:139], v172 offset:2048
	ds_read_b128 v[140:143], v172 offset:3072
	s_add_u32 s30, s28, 0xfffd0080
	s_addc_u32 s31, s29, -1
	s_cmp_eq_u32 s73, 8
	s_cselect_b32 s35, s9, s31
	s_cselect_b32 s34, s8, s30
	s_cselect_b32 s31, s1, s72
	s_cselect_b32 s30, s0, s71
	v_lshl_add_u64 v[202:203], s[28:29], 0, v[152:153]
	s_add_i32 m0, s43, 0xc000
	ds_read_b128 v[158:161], v173
	ds_read_b128 v[162:165], v173 offset:1024
	ds_read_b128 v[178:181], v173 offset:2048
	ds_read_b128 v[182:185], v173 offset:3072
	ds_read_b128 v[186:189], v173 offset:4096
	ds_read_b128 v[190:193], v173 offset:5120
	ds_read_b128 v[194:197], v173 offset:6144
	ds_read_b128 v[198:201], v173 offset:7168
	global_load_lds_dwordx4 v[202:203], off
	v_lshl_add_u64 v[202:203], s[28:29], 0, v[154:155]
	s_add_i32 m0, s43, 0xe000
	s_nop 0
	global_load_lds_dwordx4 v[202:203], off
	s_waitcnt lgkmcnt(8)
	s_barrier
	s_waitcnt lgkmcnt(0)
	s_waitcnt lgkmcnt(0)
	v_mfma_f32_16x16x32_f16 v[124:127], v[128:131], v[158:161], v[124:127]
	v_mfma_f32_16x16x32_f16 v[120:123], v[136:139], v[158:161], v[120:123]
	v_mfma_f32_16x16x32_f16 v[108:111], v[128:131], v[178:181], v[108:111]
	v_mfma_f32_16x16x32_f16 v[104:107], v[136:139], v[178:181], v[104:107]
	v_mfma_f32_16x16x32_f16 v[96:99], v[128:131], v[186:189], v[96:99]
	v_mfma_f32_16x16x32_f16 v[88:91], v[136:139], v[186:189], v[88:91]
	v_mfma_f32_16x16x32_f16 v[80:83], v[128:131], v[194:197], v[80:83]
	v_mfma_f32_16x16x32_f16 v[72:75], v[136:139], v[194:197], v[72:75]
	v_mfma_f32_16x16x32_f16 v[124:127], v[132:135], v[162:165], v[124:127]
	v_mfma_f32_16x16x32_f16 v[120:123], v[140:143], v[162:165], v[120:123]
	v_mfma_f32_16x16x32_f16 v[108:111], v[132:135], v[182:185], v[108:111]
	v_mfma_f32_16x16x32_f16 v[104:107], v[140:143], v[182:185], v[104:107]
	v_mfma_f32_16x16x32_f16 v[96:99], v[132:135], v[190:193], v[96:99]
	v_mfma_f32_16x16x32_f16 v[88:91], v[140:143], v[190:193], v[88:91]
	v_mfma_f32_16x16x32_f16 v[80:83], v[132:135], v[198:201], v[80:83]
	v_mfma_f32_16x16x32_f16 v[72:75], v[140:143], v[198:201], v[72:75]
	s_barrier
	s_add_i32 s74, s65, s42
	v_lshl_add_u64 v[218:219], s[30:31], 0, v[146:147]
	s_mov_b32 m0, s74
	ds_read_b128 v[202:205], v174
	ds_read_b128 v[206:209], v174 offset:1024
	ds_read_b128 v[210:213], v174 offset:2048
	ds_read_b128 v[214:217], v174 offset:3072
	global_load_lds_dwordx4 v[218:219], off
	v_lshl_add_u64 v[220:221], s[30:31], 0, v[150:151]
	s_add_i32 m0, s74, 0x2000
	s_nop 0
	global_load_lds_dwordx4 v[220:221], off
	s_barrier
	s_waitcnt lgkmcnt(0)
	s_waitcnt lgkmcnt(0)
	v_mfma_f32_16x16x32_f16 v[116:119], v[202:205], v[158:161], v[116:119]
	v_mfma_f32_16x16x32_f16 v[112:115], v[210:213], v[158:161], v[112:115]
	v_mfma_f32_16x16x32_f16 v[100:103], v[202:205], v[178:181], v[100:103]
	v_mfma_f32_16x16x32_f16 v[92:95], v[210:213], v[178:181], v[92:95]
	v_mfma_f32_16x16x32_f16 v[84:87], v[202:205], v[186:189], v[84:87]
	v_mfma_f32_16x16x32_f16 v[76:79], v[210:213], v[186:189], v[76:79]
	v_mfma_f32_16x16x32_f16 v[68:71], v[202:205], v[194:197], v[68:71]
	v_mfma_f32_16x16x32_f16 v[64:67], v[210:213], v[194:197], v[64:67]
	v_mfma_f32_16x16x32_f16 v[116:119], v[206:209], v[162:165], v[116:119]
	v_mfma_f32_16x16x32_f16 v[112:115], v[214:217], v[162:165], v[112:115]
	v_mfma_f32_16x16x32_f16 v[100:103], v[206:209], v[182:185], v[100:103]
	v_mfma_f32_16x16x32_f16 v[92:95], v[214:217], v[182:185], v[92:95]
	v_mfma_f32_16x16x32_f16 v[84:87], v[206:209], v[190:193], v[84:87]
	v_mfma_f32_16x16x32_f16 v[76:79], v[214:217], v[190:193], v[76:79]
	v_mfma_f32_16x16x32_f16 v[68:71], v[206:209], v[198:201], v[68:71]
	v_mfma_f32_16x16x32_f16 v[64:67], v[214:217], v[198:201], v[64:67]
	s_mov_b32 m0, s43
	v_lshl_add_u64 v[222:223], s[34:35], 0, v[144:145]
	s_barrier
	ds_read_b128 v[158:161], v173 offset:16384
	ds_read_b128 v[162:165], v173 offset:17408
	ds_read_b128 v[178:181], v173 offset:18432
	ds_read_b128 v[182:185], v173 offset:19456
	ds_read_b128 v[186:189], v173 offset:20480
	ds_read_b128 v[190:193], v173 offset:21504
	ds_read_b128 v[194:197], v173 offset:22528
	ds_read_b128 v[198:201], v173 offset:23552
	global_load_lds_dwordx4 v[222:223], off
	v_lshl_add_u64 v[224:225], s[34:35], 0, v[148:149]
	s_mov_b32 m0, s44
	s_nop 0
	global_load_lds_dwordx4 v[224:225], off
	s_barrier
	s_waitcnt lgkmcnt(0)
	s_waitcnt lgkmcnt(0)
	v_mfma_f32_16x16x32_f16 v[60:63], v[128:131], v[158:161], v[60:63]
	v_mfma_f32_16x16x32_f16 v[56:59], v[136:139], v[158:161], v[56:59]
	v_mfma_f32_16x16x32_f16 v[48:51], v[128:131], v[178:181], v[48:51]
	v_mfma_f32_16x16x32_f16 v[40:43], v[136:139], v[178:181], v[40:43]
	v_mfma_f32_16x16x32_f16 v[32:35], v[128:131], v[186:189], v[32:35]
	v_mfma_f32_16x16x32_f16 v[24:27], v[136:139], v[186:189], v[24:27]
	v_mfma_f32_16x16x32_f16 v[16:19], v[128:131], v[194:197], v[16:19]
	v_mfma_f32_16x16x32_f16 v[8:11], v[136:139], v[194:197], v[8:11]
	v_mfma_f32_16x16x32_f16 v[60:63], v[132:135], v[162:165], v[60:63]
	v_mfma_f32_16x16x32_f16 v[56:59], v[140:143], v[162:165], v[56:59]
	v_mfma_f32_16x16x32_f16 v[48:51], v[132:135], v[182:185], v[48:51]
	v_mfma_f32_16x16x32_f16 v[40:43], v[140:143], v[182:185], v[40:43]
	v_mfma_f32_16x16x32_f16 v[32:35], v[132:135], v[190:193], v[32:35]
	v_mfma_f32_16x16x32_f16 v[24:27], v[140:143], v[190:193], v[24:27]
	v_mfma_f32_16x16x32_f16 v[16:19], v[132:135], v[198:201], v[16:19]
	v_mfma_f32_16x16x32_f16 v[8:11], v[140:143], v[198:201], v[8:11]
	s_barrier
	s_add_u32 s74, s30, 0xc000
	s_addc_u32 s75, s31, 0
	s_add_i32 s76, s66, s42
	v_lshl_add_u64 v[128:129], s[74:75], 0, v[146:147]
	s_mov_b32 m0, s76
	s_nop 0
	global_load_lds_dwordx4 v[128:129], off
	v_lshl_add_u64 v[128:129], s[74:75], 0, v[150:151]
	s_add_i32 m0, s76, 0x2000
	s_nop 0
	global_load_lds_dwordx4 v[128:129], off
	s_waitcnt vmcnt(6)
	s_barrier
	v_mfma_f32_16x16x32_f16 v[52:55], v[202:205], v[158:161], v[52:55]
	v_mfma_f32_16x16x32_f16 v[44:47], v[210:213], v[158:161], v[44:47]
	v_mfma_f32_16x16x32_f16 v[36:39], v[202:205], v[178:181], v[36:39]
	v_mfma_f32_16x16x32_f16 v[28:31], v[210:213], v[178:181], v[28:31]
	v_mfma_f32_16x16x32_f16 v[20:23], v[202:205], v[186:189], v[20:23]
	v_mfma_f32_16x16x32_f16 v[12:15], v[210:213], v[186:189], v[12:15]
	v_mfma_f32_16x16x32_f16 v[4:7], v[202:205], v[194:197], v[4:7]
	v_mfma_f32_16x16x32_f16 v[0:3], v[210:213], v[194:197], v[0:3]
	v_mfma_f32_16x16x32_f16 v[52:55], v[206:209], v[162:165], v[52:55]
	v_mfma_f32_16x16x32_f16 v[44:47], v[214:217], v[162:165], v[44:47]
	v_mfma_f32_16x16x32_f16 v[36:39], v[206:209], v[182:185], v[36:39]
	v_mfma_f32_16x16x32_f16 v[28:31], v[214:217], v[182:185], v[28:31]
	v_mfma_f32_16x16x32_f16 v[20:23], v[206:209], v[190:193], v[20:23]
	v_mfma_f32_16x16x32_f16 v[12:15], v[214:217], v[190:193], v[12:15]
	v_mfma_f32_16x16x32_f16 v[4:7], v[206:209], v[198:201], v[4:7]
	v_mfma_f32_16x16x32_f16 v[0:3], v[214:217], v[198:201], v[0:3]
	s_add_i32 s74, 0, 0x18000
	v_add_u32_e32 v140, s74, v168
	s_barrier
	ds_read_b128 v[128:131], v140
	ds_read_b128 v[132:135], v140 offset:1024
	ds_read_b128 v[136:139], v140 offset:2048
	ds_read_b128 v[140:143], v140 offset:3072
	s_add_u32 s34, s34, 0x30000
	s_addc_u32 s35, s35, 0
	s_mov_b32 m0, s45
	v_lshl_add_u64 v[202:203], s[34:35], 0, v[144:145]
	ds_read_b128 v[158:161], v173 offset:32768
	ds_read_b128 v[162:165], v173 offset:33792
	ds_read_b128 v[178:181], v173 offset:34816
	ds_read_b128 v[182:185], v173 offset:35840
	ds_read_b128 v[186:189], v173 offset:36864
	ds_read_b128 v[190:193], v173 offset:37888
	ds_read_b128 v[194:197], v173 offset:38912
	ds_read_b128 v[198:201], v173 offset:39936
	global_load_lds_dwordx4 v[202:203], off
	v_lshl_add_u64 v[202:203], s[34:35], 0, v[148:149]
	s_mov_b32 m0, s46
	s_nop 0
	global_load_lds_dwordx4 v[202:203], off
	s_waitcnt lgkmcnt(8)
	s_barrier
	s_waitcnt lgkmcnt(0)
	s_waitcnt lgkmcnt(0)
	v_mfma_f32_16x16x32_f16 v[124:127], v[128:131], v[158:161], v[124:127]
	v_mfma_f32_16x16x32_f16 v[120:123], v[136:139], v[158:161], v[120:123]
	v_mfma_f32_16x16x32_f16 v[108:111], v[128:131], v[178:181], v[108:111]
	v_mfma_f32_16x16x32_f16 v[104:107], v[136:139], v[178:181], v[104:107]
	v_mfma_f32_16x16x32_f16 v[96:99], v[128:131], v[186:189], v[96:99]
	v_mfma_f32_16x16x32_f16 v[88:91], v[136:139], v[186:189], v[88:91]
	v_mfma_f32_16x16x32_f16 v[80:83], v[128:131], v[194:197], v[80:83]
	v_mfma_f32_16x16x32_f16 v[72:75], v[136:139], v[194:197], v[72:75]
	v_mfma_f32_16x16x32_f16 v[124:127], v[132:135], v[162:165], v[124:127]
	v_mfma_f32_16x16x32_f16 v[120:123], v[140:143], v[162:165], v[120:123]
	v_mfma_f32_16x16x32_f16 v[108:111], v[132:135], v[182:185], v[108:111]
	v_mfma_f32_16x16x32_f16 v[104:107], v[140:143], v[182:185], v[104:107]
	v_mfma_f32_16x16x32_f16 v[96:99], v[132:135], v[190:193], v[96:99]
	v_mfma_f32_16x16x32_f16 v[88:91], v[140:143], v[190:193], v[88:91]
	v_mfma_f32_16x16x32_f16 v[80:83], v[132:135], v[198:201], v[80:83]
	v_mfma_f32_16x16x32_f16 v[72:75], v[140:143], v[198:201], v[72:75]
	s_barrier
	s_add_i32 s34, 0, 0x1c000
	s_add_i32 s35, s74, s42
	v_add_u32_e32 v177, s34, v168
	v_lshl_add_u64 v[218:219], v[218:219], 0, s[26:27]
	s_mov_b32 m0, s35
	ds_read_b128 v[202:205], v177
	ds_read_b128 v[206:209], v177 offset:1024
	ds_read_b128 v[210:213], v177 offset:2048
	ds_read_b128 v[214:217], v177 offset:3072
	global_load_lds_dwordx4 v[218:219], off
	v_lshl_add_u64 v[218:219], v[220:221], 0, s[26:27]
	s_add_i32 m0, s35, 0x2000
	s_nop 0
	global_load_lds_dwordx4 v[218:219], off
	s_barrier
	s_waitcnt lgkmcnt(0)
	s_waitcnt lgkmcnt(0)
	v_mfma_f32_16x16x32_f16 v[116:119], v[202:205], v[158:161], v[116:119]
	v_mfma_f32_16x16x32_f16 v[112:115], v[210:213], v[158:161], v[112:115]
	v_mfma_f32_16x16x32_f16 v[100:103], v[202:205], v[178:181], v[100:103]
	v_mfma_f32_16x16x32_f16 v[92:95], v[210:213], v[178:181], v[92:95]
	v_mfma_f32_16x16x32_f16 v[84:87], v[202:205], v[186:189], v[84:87]
	v_mfma_f32_16x16x32_f16 v[76:79], v[210:213], v[186:189], v[76:79]
	v_mfma_f32_16x16x32_f16 v[68:71], v[202:205], v[194:197], v[68:71]
	v_mfma_f32_16x16x32_f16 v[64:67], v[210:213], v[194:197], v[64:67]
	v_mfma_f32_16x16x32_f16 v[116:119], v[206:209], v[162:165], v[116:119]
	v_mfma_f32_16x16x32_f16 v[112:115], v[214:217], v[162:165], v[112:115]
	v_mfma_f32_16x16x32_f16 v[100:103], v[206:209], v[182:185], v[100:103]
	v_mfma_f32_16x16x32_f16 v[92:95], v[214:217], v[182:185], v[92:95]
	v_mfma_f32_16x16x32_f16 v[84:87], v[206:209], v[190:193], v[84:87]
	v_mfma_f32_16x16x32_f16 v[76:79], v[214:217], v[190:193], v[76:79]
	v_mfma_f32_16x16x32_f16 v[68:71], v[206:209], v[198:201], v[68:71]
	v_mfma_f32_16x16x32_f16 v[64:67], v[214:217], v[198:201], v[64:67]
	s_mov_b32 m0, s49
	v_lshl_add_u64 v[218:219], v[222:223], 0, s[26:27]
	s_barrier
	ds_read_b128 v[158:161], v173 offset:49152
	ds_read_b128 v[162:165], v173 offset:50176
	ds_read_b128 v[178:181], v173 offset:51200
	ds_read_b128 v[182:185], v173 offset:52224
	ds_read_b128 v[186:189], v173 offset:53248
	ds_read_b128 v[190:193], v173 offset:54272
	ds_read_b128 v[194:197], v173 offset:55296
	ds_read_b128 v[198:201], v173 offset:56320
	global_load_lds_dwordx4 v[218:219], off
	v_lshl_add_u64 v[218:219], v[224:225], 0, s[26:27]
	s_mov_b32 m0, s50
	s_nop 0
	global_load_lds_dwordx4 v[218:219], off
	s_barrier
	s_waitcnt lgkmcnt(0)
	s_waitcnt lgkmcnt(0)
	v_mfma_f32_16x16x32_f16 v[60:63], v[128:131], v[158:161], v[60:63]
	v_mfma_f32_16x16x32_f16 v[56:59], v[136:139], v[158:161], v[56:59]
	v_mfma_f32_16x16x32_f16 v[48:51], v[128:131], v[178:181], v[48:51]
	v_mfma_f32_16x16x32_f16 v[40:43], v[136:139], v[178:181], v[40:43]
	v_mfma_f32_16x16x32_f16 v[32:35], v[128:131], v[186:189], v[32:35]
	v_mfma_f32_16x16x32_f16 v[24:27], v[136:139], v[186:189], v[24:27]
	v_mfma_f32_16x16x32_f16 v[16:19], v[128:131], v[194:197], v[16:19]
	v_mfma_f32_16x16x32_f16 v[8:11], v[136:139], v[194:197], v[8:11]
	v_mfma_f32_16x16x32_f16 v[60:63], v[132:135], v[162:165], v[60:63]
	v_mfma_f32_16x16x32_f16 v[56:59], v[140:143], v[162:165], v[56:59]
	v_mfma_f32_16x16x32_f16 v[48:51], v[132:135], v[182:185], v[48:51]
	v_mfma_f32_16x16x32_f16 v[40:43], v[140:143], v[182:185], v[40:43]
	v_mfma_f32_16x16x32_f16 v[32:35], v[132:135], v[190:193], v[32:35]
	v_mfma_f32_16x16x32_f16 v[24:27], v[140:143], v[190:193], v[24:27]
	v_mfma_f32_16x16x32_f16 v[16:19], v[132:135], v[198:201], v[16:19]
	v_mfma_f32_16x16x32_f16 v[8:11], v[140:143], v[198:201], v[8:11]
	s_barrier
	s_add_u32 s30, s30, 0xc080
	s_addc_u32 s31, s31, 0
	s_add_i32 s34, s34, s42
	v_lshl_add_u64 v[128:129], s[30:31], 0, v[146:147]
	s_mov_b32 m0, s34
	s_nop 0
	global_load_lds_dwordx4 v[128:129], off
	v_lshl_add_u64 v[128:129], s[30:31], 0, v[150:151]
	s_add_i32 m0, s34, 0x2000
	s_nop 0
	global_load_lds_dwordx4 v[128:129], off
	s_waitcnt vmcnt(6)
	s_barrier
	v_mfma_f32_16x16x32_f16 v[52:55], v[202:205], v[158:161], v[52:55]
	v_mfma_f32_16x16x32_f16 v[44:47], v[210:213], v[158:161], v[44:47]
	v_mfma_f32_16x16x32_f16 v[36:39], v[202:205], v[178:181], v[36:39]
	v_mfma_f32_16x16x32_f16 v[28:31], v[210:213], v[178:181], v[28:31]
	v_mfma_f32_16x16x32_f16 v[20:23], v[202:205], v[186:189], v[20:23]
	v_mfma_f32_16x16x32_f16 v[12:15], v[210:213], v[186:189], v[12:15]
	v_mfma_f32_16x16x32_f16 v[4:7], v[202:205], v[194:197], v[4:7]
	v_mfma_f32_16x16x32_f16 v[0:3], v[210:213], v[194:197], v[0:3]
	v_mfma_f32_16x16x32_f16 v[52:55], v[206:209], v[162:165], v[52:55]
	v_mfma_f32_16x16x32_f16 v[44:47], v[214:217], v[162:165], v[44:47]
	v_mfma_f32_16x16x32_f16 v[36:39], v[206:209], v[182:185], v[36:39]
	v_mfma_f32_16x16x32_f16 v[28:31], v[214:217], v[182:185], v[28:31]
	v_mfma_f32_16x16x32_f16 v[20:23], v[206:209], v[190:193], v[20:23]
	v_mfma_f32_16x16x32_f16 v[12:15], v[214:217], v[190:193], v[12:15]
	v_mfma_f32_16x16x32_f16 v[4:7], v[206:209], v[198:201], v[4:7]
	v_mfma_f32_16x16x32_f16 v[0:3], v[214:217], v[198:201], v[0:3]
	s_add_i32 s73, s73, 2
	s_add_u32 s28, s28, 0x100
	s_addc_u32 s29, s29, 0
	s_add_u32 s71, s71, 0x100
	s_addc_u32 s72, s72, 0
	s_cmp_gt_u32 s73, 9
	s_barrier
	s_cbranch_scc0 .LBB9_27
	s_lshl_b32 s28, s70, 8
	s_add_i32 s28, s28, s48
	s_lshl_b32 s29, s68, 8
	s_or_b32 s29, s29, s51
	s_waitcnt vmcnt(6)
	v_pk_fma_f32 v[126:127], v[126:127], v[226:227], v[236:237] op_sel_hi:[1,0,1]
	v_pk_fma_f32 v[124:125], v[124:125], v[226:227], v[234:235] op_sel_hi:[1,0,1]
	v_pk_fma_f32 v[122:123], v[122:123], v[226:227], v[240:241] op_sel_hi:[1,0,1]
	v_pk_fma_f32 v[120:121], v[120:121], v[226:227], v[238:239] op_sel_hi:[1,0,1]
	v_cvt_pk_f16_f32 v124, v124, v125
	v_cvt_pk_f16_f32 v125, v126, v127
	v_cvt_pk_f16_f32 v126, v120, v121
	v_cvt_pk_f16_f32 v123, v122, v123
	v_pk_fma_f32 v[118:119], v[118:119], v[226:227], v[244:245] op_sel_hi:[1,0,1]
	v_pk_fma_f32 v[116:117], v[116:117], v[226:227], v[242:243] op_sel_hi:[1,0,1]
	v_pk_fma_f32 v[114:115], v[114:115], v[226:227], v[248:249] op_sel_hi:[1,0,1]
	v_pk_fma_f32 v[112:113], v[112:113], v[226:227], v[246:247] op_sel_hi:[1,0,1]
	v_pk_max_f16 v120, v124, 0
	v_pk_max_f16 v121, v125, 0
	v_pk_max_f16 v122, v126, 0
	v_pk_max_f16 v123, v123, 0
	v_cvt_pk_f16_f32 v116, v116, v117
	v_cvt_pk_f16_f32 v117, v118, v119
	v_cvt_pk_f16_f32 v118, v112, v113
	v_cvt_pk_f16_f32 v115, v114, v115
	v_pk_fma_f32 v[110:111], v[110:111], v[226:227], v[236:237] op_sel:[0,1,0]
	v_pk_fma_f32 v[108:109], v[108:109], v[226:227], v[234:235] op_sel:[0,1,0]
	v_pk_fma_f32 v[106:107], v[106:107], v[226:227], v[240:241] op_sel:[0,1,0]
	v_pk_fma_f32 v[104:105], v[104:105], v[226:227], v[238:239] op_sel:[0,1,0]
	v_pk_fma_f32 v[102:103], v[102:103], v[226:227], v[244:245] op_sel:[0,1,0]
	v_pk_fma_f32 v[100:101], v[100:101], v[226:227], v[242:243] op_sel:[0,1,0]
	v_pk_fma_f32 v[94:95], v[94:95], v[226:227], v[248:249] op_sel:[0,1,0]
	v_pk_fma_f32 v[92:93], v[92:93], v[226:227], v[246:247] op_sel:[0,1,0]
	ds_write_b128 v175, v[120:123]
	v_or_b32_e32 v120, s28, v169
	v_pk_max_f16 v112, v116, 0
	v_pk_max_f16 v113, v117, 0
	v_pk_max_f16 v114, v118, 0
	v_pk_max_f16 v115, v115, 0
	v_cvt_pk_f16_f32 v108, v108, v109
	v_cvt_pk_f16_f32 v109, v110, v111
	v_cvt_pk_f16_f32 v110, v104, v105
	v_cvt_pk_f16_f32 v107, v106, v107
	v_cvt_pk_f16_f32 v100, v100, v101
	v_cvt_pk_f16_f32 v101, v102, v103
	v_cvt_pk_f16_f32 v102, v92, v93
	v_cvt_pk_f16_f32 v95, v94, v95
	ds_write_b128 v175, v[112:115] offset:64
	v_mul_lo_u32 v116, v120, s10
	v_pk_max_f16 v104, v108, 0
	v_pk_max_f16 v105, v109, 0
	v_pk_max_f16 v106, v110, 0
	v_pk_max_f16 v107, v107, 0
	v_pk_max_f16 v92, v100, 0
	v_pk_max_f16 v93, v101, 0
	v_pk_max_f16 v94, v102, 0
	v_pk_max_f16 v95, v95, 0
	ds_read_b128 v[112:115], v176
	v_add_u32_e32 v120, s29, v116
	ds_read_b128 v[116:119], v176 offset:1152
	ds_write_b128 v175, v[104:107]
	ds_write_b128 v175, v[92:95] offset:64
	ds_read_b128 v[92:95], v176
	ds_read_b128 v[100:103], v176 offset:1152
	v_lshlrev_b32_e32 v121, 1, v120
	v_add_u32_e32 v122, v121, v170
	v_add_u32_e32 v104, s55, v121
	s_waitcnt lgkmcnt(0)
	buffer_store_dwordx4 v[112:115], v122, s[20:23], 0 offen nt
	v_add_u32_e32 v105, v104, v170
	v_pk_fma_f32 v[90:91], v[90:91], v[228:229], v[240:241] op_sel_hi:[1,0,1]
	v_add_u32_e32 v112, v121, v171
	buffer_store_dwordx4 v[116:119], v112, s[20:23], 0 offen nt
	buffer_store_dwordx4 v[92:95], v105, s[20:23], 0 offen nt
	v_pk_fma_f32 v[88:89], v[88:89], v[228:229], v[238:239] op_sel_hi:[1,0,1]
	v_pk_fma_f32 v[86:87], v[86:87], v[228:229], v[244:245] op_sel_hi:[1,0,1]
	v_pk_fma_f32 v[92:93], v[98:99], v[228:229], v[236:237] op_sel_hi:[1,0,1]
	v_pk_fma_f32 v[94:95], v[96:97], v[228:229], v[234:235] op_sel_hi:[1,0,1]
	v_pk_fma_f32 v[84:85], v[84:85], v[228:229], v[242:243] op_sel_hi:[1,0,1]
	v_pk_fma_f32 v[78:79], v[78:79], v[228:229], v[248:249] op_sel_hi:[1,0,1]
	v_pk_fma_f32 v[76:77], v[76:77], v[228:229], v[246:247] op_sel_hi:[1,0,1]
	v_cvt_pk_f16_f32 v94, v94, v95
	v_cvt_pk_f16_f32 v92, v92, v93
	v_cvt_pk_f16_f32 v93, v88, v89
	v_cvt_pk_f16_f32 v91, v90, v91
	v_cvt_pk_f16_f32 v84, v84, v85
	v_cvt_pk_f16_f32 v85, v86, v87
	v_cvt_pk_f16_f32 v86, v76, v77
	v_cvt_pk_f16_f32 v79, v78, v79
	v_pk_max_f16 v88, v94, 0
	v_pk_max_f16 v89, v92, 0
	v_pk_max_f16 v90, v93, 0
	v_pk_max_f16 v91, v91, 0
	v_pk_max_f16 v76, v84, 0
	v_pk_max_f16 v77, v85, 0
	v_pk_max_f16 v78, v86, 0
	v_pk_max_f16 v79, v79, 0
	ds_write_b128 v175, v[88:91]
	ds_write_b128 v175, v[76:79] offset:64
	ds_read_b128 v[76:79], v176
	ds_read_b128 v[84:87], v176 offset:1152
	v_add_u32_e32 v88, s55, v104
	v_add_u32_e32 v105, v104, v171
	v_add_u32_e32 v89, v88, v170
	buffer_store_dwordx4 v[100:103], v105, s[20:23], 0 offen nt
	s_waitcnt lgkmcnt(1)
	buffer_store_dwordx4 v[76:79], v89, s[20:23], 0 offen nt
	v_pk_fma_f32 v[74:75], v[74:75], v[228:229], v[240:241] op_sel:[0,1,0]
	v_pk_fma_f32 v[72:73], v[72:73], v[228:229], v[238:239] op_sel:[0,1,0]
	v_add_u32_e32 v76, v88, v171
	s_waitcnt lgkmcnt(0)
	buffer_store_dwordx4 v[84:87], v76, s[20:23], 0 offen nt
	v_pk_fma_f32 v[76:77], v[82:83], v[228:229], v[236:237] op_sel:[0,1,0]
	v_pk_fma_f32 v[78:79], v[80:81], v[228:229], v[234:235] op_sel:[0,1,0]
	v_pk_fma_f32 v[70:71], v[70:71], v[228:229], v[244:245] op_sel:[0,1,0]
	v_pk_fma_f32 v[68:69], v[68:69], v[228:229], v[242:243] op_sel:[0,1,0]
	v_pk_fma_f32 v[66:67], v[66:67], v[228:229], v[248:249] op_sel:[0,1,0]
	v_pk_fma_f32 v[64:65], v[64:65], v[228:229], v[246:247] op_sel:[0,1,0]
	v_cvt_pk_f16_f32 v78, v78, v79
	v_cvt_pk_f16_f32 v76, v76, v77
	v_cvt_pk_f16_f32 v77, v72, v73
	v_cvt_pk_f16_f32 v75, v74, v75
	v_cvt_pk_f16_f32 v68, v68, v69
	v_cvt_pk_f16_f32 v69, v70, v71
	v_cvt_pk_f16_f32 v70, v64, v65
	v_cvt_pk_f16_f32 v67, v66, v67
	v_pk_fma_f32 v[62:63], v[62:63], v[230:231], v[236:237] op_sel_hi:[1,0,1]
	v_pk_fma_f32 v[60:61], v[60:61], v[230:231], v[234:235] op_sel_hi:[1,0,1]
	v_pk_fma_f32 v[58:59], v[58:59], v[230:231], v[240:241] op_sel_hi:[1,0,1]
	v_pk_fma_f32 v[56:57], v[56:57], v[230:231], v[238:239] op_sel_hi:[1,0,1]
	v_pk_fma_f32 v[54:55], v[54:55], v[230:231], v[244:245] op_sel_hi:[1,0,1]
	v_pk_fma_f32 v[52:53], v[52:53], v[230:231], v[242:243] op_sel_hi:[1,0,1]
	v_pk_fma_f32 v[46:47], v[46:47], v[230:231], v[248:249] op_sel_hi:[1,0,1]
	v_pk_fma_f32 v[44:45], v[44:45], v[230:231], v[246:247] op_sel_hi:[1,0,1]
	v_pk_max_f16 v72, v78, 0
	v_pk_max_f16 v73, v76, 0
	v_pk_max_f16 v74, v77, 0
	v_pk_max_f16 v75, v75, 0
	v_pk_max_f16 v64, v68, 0
	v_pk_max_f16 v65, v69, 0
	v_pk_max_f16 v66, v70, 0
	v_pk_max_f16 v67, v67, 0
	v_cvt_pk_f16_f32 v60, v60, v61
	v_cvt_pk_f16_f32 v61, v62, v63
	v_cvt_pk_f16_f32 v62, v56, v57
	v_cvt_pk_f16_f32 v59, v58, v59
	v_cvt_pk_f16_f32 v52, v52, v53
	v_cvt_pk_f16_f32 v53, v54, v55
	v_cvt_pk_f16_f32 v54, v44, v45
	v_cvt_pk_f16_f32 v47, v46, v47
	ds_write_b128 v175, v[72:75]
	ds_write_b128 v175, v[64:67] offset:64
	v_pk_max_f16 v56, v60, 0
	v_pk_max_f16 v57, v61, 0
	v_pk_max_f16 v58, v62, 0
	v_pk_max_f16 v59, v59, 0
	v_pk_max_f16 v44, v52, 0
	v_pk_max_f16 v45, v53, 0
	v_pk_max_f16 v46, v54, 0
	v_pk_max_f16 v47, v47, 0
	ds_read_b128 v[64:67], v176
	ds_read_b128 v[68:71], v176 offset:1152
	ds_write_b128 v175, v[56:59]
	ds_write_b128 v175, v[44:47] offset:64
	ds_read_b128 v[44:47], v176
	ds_read_b128 v[52:55], v176 offset:1152
	v_add_u32_e32 v72, s56, v120
	v_lshlrev_b32_e32 v73, 1, v72
	v_add_u32_e32 v74, v73, v170
	v_add_u32_e32 v56, s62, v88
	s_waitcnt lgkmcnt(5)
	buffer_store_dwordx4 v[64:67], v74, s[20:23], 0 offen nt
	v_add_u32_e32 v57, v56, v170
	v_pk_fma_f32 v[42:43], v[42:43], v[230:231], v[240:241] op_sel:[0,1,0]
	v_add_u32_e32 v64, v73, v171
	s_waitcnt lgkmcnt(4)
	buffer_store_dwordx4 v[68:71], v64, s[20:23], 0 offen nt
	s_waitcnt lgkmcnt(1)
	buffer_store_dwordx4 v[44:47], v57, s[20:23], 0 offen nt
	v_pk_fma_f32 v[40:41], v[40:41], v[230:231], v[238:239] op_sel:[0,1,0]
	v_pk_fma_f32 v[38:39], v[38:39], v[230:231], v[244:245] op_sel:[0,1,0]
	v_add_u32_e32 v44, v56, v171
	s_waitcnt lgkmcnt(0)
	buffer_store_dwordx4 v[52:55], v44, s[20:23], 0 offen nt
	v_pk_fma_f32 v[44:45], v[50:51], v[230:231], v[236:237] op_sel:[0,1,0]
	v_pk_fma_f32 v[46:47], v[48:49], v[230:231], v[234:235] op_sel:[0,1,0]
	v_pk_fma_f32 v[36:37], v[36:37], v[230:231], v[242:243] op_sel:[0,1,0]
	v_pk_fma_f32 v[30:31], v[30:31], v[230:231], v[248:249] op_sel:[0,1,0]
	v_pk_fma_f32 v[28:29], v[28:29], v[230:231], v[246:247] op_sel:[0,1,0]
	v_cvt_pk_f16_f32 v46, v46, v47
	v_cvt_pk_f16_f32 v44, v44, v45
	v_cvt_pk_f16_f32 v45, v40, v41
	v_cvt_pk_f16_f32 v43, v42, v43
	v_cvt_pk_f16_f32 v36, v36, v37
	v_cvt_pk_f16_f32 v37, v38, v39
	v_cvt_pk_f16_f32 v38, v28, v29
	v_cvt_pk_f16_f32 v31, v30, v31
	v_pk_max_f16 v40, v46, 0
	v_pk_max_f16 v41, v44, 0
	v_pk_max_f16 v42, v45, 0
	v_pk_max_f16 v43, v43, 0
	v_pk_max_f16 v28, v36, 0
	v_pk_max_f16 v29, v37, 0
	v_pk_max_f16 v30, v38, 0
	v_pk_max_f16 v31, v31, 0
	ds_write_b128 v175, v[40:43]
	ds_write_b128 v175, v[28:31] offset:64
	ds_read_b128 v[28:31], v176
	ds_read_b128 v[36:39], v176 offset:1152
	v_add_u32_e32 v40, s63, v72
	v_lshlrev_b32_e32 v41, 1, v40
	v_add_u32_e32 v42, v41, v170
	s_waitcnt lgkmcnt(1)
	buffer_store_dwordx4 v[28:31], v42, s[20:23], 0 offen nt
	v_pk_fma_f32 v[26:27], v[26:27], v[232:233], v[240:241] op_sel_hi:[1,0,1]
	v_pk_fma_f32 v[24:25], v[24:25], v[232:233], v[238:239] op_sel_hi:[1,0,1]
	v_add_u32_e32 v28, v41, v171
	s_waitcnt lgkmcnt(0)
	buffer_store_dwordx4 v[36:39], v28, s[20:23], 0 offen nt
	v_pk_fma_f32 v[28:29], v[34:35], v[232:233], v[236:237] op_sel_hi:[1,0,1]
	v_pk_fma_f32 v[30:31], v[32:33], v[232:233], v[234:235] op_sel_hi:[1,0,1]
	v_pk_fma_f32 v[22:23], v[22:23], v[232:233], v[244:245] op_sel_hi:[1,0,1]
	v_pk_fma_f32 v[20:21], v[20:21], v[232:233], v[242:243] op_sel_hi:[1,0,1]
	v_pk_fma_f32 v[14:15], v[14:15], v[232:233], v[248:249] op_sel_hi:[1,0,1]
	v_pk_fma_f32 v[12:13], v[12:13], v[232:233], v[246:247] op_sel_hi:[1,0,1]
	v_cvt_pk_f16_f32 v30, v30, v31
	v_cvt_pk_f16_f32 v28, v28, v29
	v_cvt_pk_f16_f32 v29, v24, v25
	v_cvt_pk_f16_f32 v27, v26, v27
	v_cvt_pk_f16_f32 v20, v20, v21
	v_cvt_pk_f16_f32 v21, v22, v23
	v_cvt_pk_f16_f32 v22, v12, v13
	v_cvt_pk_f16_f32 v15, v14, v15
	v_pk_max_f16 v24, v30, 0
	v_pk_max_f16 v25, v28, 0
	v_pk_max_f16 v26, v29, 0
	v_pk_max_f16 v27, v27, 0
	v_pk_max_f16 v12, v20, 0
	v_pk_max_f16 v13, v21, 0
	v_pk_max_f16 v14, v22, 0
	v_pk_max_f16 v15, v15, 0
	ds_write_b128 v175, v[24:27]
	ds_write_b128 v175, v[12:15] offset:64
	ds_read_b128 v[12:15], v176
	ds_read_b128 v[20:23], v176 offset:1152
	v_add_u32_e32 v24, s64, v40
	v_lshlrev_b32_e32 v25, 1, v24
	v_add_u32_e32 v26, v25, v170
	s_waitcnt lgkmcnt(1)
	buffer_store_dwordx4 v[12:15], v26, s[20:23], 0 offen nt
	v_pk_fma_f32 v[10:11], v[10:11], v[232:233], v[240:241] op_sel:[0,1,0]
	v_pk_fma_f32 v[8:9], v[8:9], v[232:233], v[238:239] op_sel:[0,1,0]
	v_pk_fma_f32 v[12:13], v[18:19], v[232:233], v[236:237] op_sel:[0,1,0]
	v_pk_fma_f32 v[14:15], v[16:17], v[232:233], v[234:235] op_sel:[0,1,0]
	v_pk_fma_f32 v[6:7], v[6:7], v[232:233], v[244:245] op_sel:[0,1,0]
	v_pk_fma_f32 v[4:5], v[4:5], v[232:233], v[242:243] op_sel:[0,1,0]
	v_pk_fma_f32 v[2:3], v[2:3], v[232:233], v[248:249] op_sel:[0,1,0]
	v_pk_fma_f32 v[0:1], v[0:1], v[232:233], v[246:247] op_sel:[0,1,0]
	v_cvt_pk_f16_f32 v14, v14, v15
	v_cvt_pk_f16_f32 v12, v12, v13
	v_cvt_pk_f16_f32 v13, v8, v9
	v_cvt_pk_f16_f32 v11, v10, v11
	v_cvt_pk_f16_f32 v4, v4, v5
	v_cvt_pk_f16_f32 v5, v6, v7
	v_cvt_pk_f16_f32 v6, v0, v1
	v_cvt_pk_f16_f32 v3, v2, v3
	v_pk_max_f16 v8, v14, 0
	v_pk_max_f16 v9, v12, 0
	v_pk_max_f16 v10, v13, 0
	v_pk_max_f16 v11, v11, 0
	v_pk_max_f16 v0, v4, 0
	v_pk_max_f16 v1, v5, 0
	v_pk_max_f16 v2, v6, 0
	v_pk_max_f16 v3, v3, 0
	ds_write_b128 v175, v[8:11]
	ds_write_b128 v175, v[0:3] offset:64
	ds_read_b128 v[0:3], v176
	ds_read_b128 v[4:7], v176 offset:1152
	v_add_lshl_u32 v8, v24, s64, 1
	v_add_u32_e32 v25, v25, v171
	v_add_u32_e32 v9, v8, v170
	s_waitcnt lgkmcnt(4)
	buffer_store_dwordx4 v[20:23], v25, s[20:23], 0 offen nt
	s_waitcnt lgkmcnt(1)
	buffer_store_dwordx4 v[0:3], v9, s[20:23], 0 offen nt
	s_mov_b32 s68, s67
	s_mov_b32 s70, s69
	v_add_u32_e32 v0, v8, v171
	s_mov_b64 s[30:31], s[0:1]
	s_mov_b64 s[28:29], s[8:9]
	s_mov_b64 vcc, s[6:7]
	s_waitcnt lgkmcnt(0)
	buffer_store_dwordx4 v[4:7], v0, s[20:23], 0 offen nt
	s_cbranch_vccz .LBB9_12
	s_waitcnt vmcnt(0)
	s_cmpk_gt_u32 s36, 0xff
	s_cbranch_scc1 .LBB9_31
	s_barrier

.LBB9_32:
	s_endpgm
	s_endpgm
	s_endpgm
	s_endpgm
	s_endpgm
	s_endpgm
	.section	.rodata,"a",@progbits
	.p2align	6, 0x0

.LBB10_11:
	s_mov_b64 s[36:37], 0x80
	s_and_b32 s34, s24, 3
	s_add_i32 m0, s51, 0x18000
	v_lshl_add_u64 v[8:9], v[8:9], 0, s[36:37]
	s_lshl_b32 s57, s25, 6
	s_lshl_b32 s25, s25, 13
	s_lshl_b32 s26, s34, 12
	s_waitcnt vmcnt(4)
	s_barrier
	global_load_lds_dwordx4 v[8:9], off
	v_lshl_add_u64 v[6:7], v[6:7], 0, s[36:37]
	s_add_i32 m0, s51, 0x1a000
	s_add_i32 s58, s51, 0x8000
	s_add_i32 s59, s51, 0xa000
	global_load_lds_dwordx4 v[6:7], off
	v_lshl_add_u64 v[4:5], v[4:5], 0, s[36:37]
	s_mov_b32 m0, s58
	s_add_u32 s0, s40, 0x30080
	global_load_lds_dwordx4 v[4:5], off
	v_lshl_add_u64 v[2:3], v[2:3], 0, s[36:37]
	s_mov_b32 m0, s59
	s_addc_u32 s1, s41, 0
	global_load_lds_dwordx4 v[2:3], off
	s_add_i32 m0, s51, 0x1c000
	v_lshl_add_u64 v[2:3], s[0:1], 0, v[178:179]
	global_load_lds_dwordx4 v[2:3], off
	v_lshl_add_u64 v[2:3], s[0:1], 0, v[182:183]
	s_add_i32 m0, s51, 0x1e000
	s_lshl_b32 s61, s33, 3
	global_load_lds_dwordx4 v[2:3], off
	s_abs_i32 s62, s61
	v_and_b32_e32 v227, 15, v0
	v_and_b32_e32 v2, 48, v0
	v_lshlrev_b32_e32 v4, 2, v0
	v_lshlrev_b32_e32 v5, 6, v0
	v_bfe_u32 v229, v0, 3, 3
	v_cvt_f32_u32_e32 v0, s62
	s_abs_i32 s64, s33
	v_cvt_f32_u32_e32 v6, s64
	s_movk_i32 s0, 0x3c0
	v_rcp_iflag_f32_e32 v0, v0
	s_mulk_i32 s24, 0x900
	v_rcp_iflag_f32_e32 v6, v6
	v_and_or_b32 v5, v5, s0, v2
	v_mul_f32_e32 v0, 0x4f7ffffe, v0
	v_cvt_u32_f32_e32 v0, v0
	s_add_i32 s0, s24, 0
	v_lshl_or_b32 v3, v227, 6, v2
	v_and_b32_e32 v4, 32, v4
	s_add_i32 s0, s0, 0x20000
	v_bitop3_b32 v3, v3, s25, v4 bitop3:0xde
	v_bitop3_b32 v228, s26, v5, v4 bitop3:0xf6
	s_movk_i32 s1, 0x90
	v_mov_b32_e32 v4, s0
	v_mad_u32_u24 v5, v227, s1, v4
	v_mad_u32_u24 v4, v229, s1, v4
	v_readfirstlane_b32 s1, v0
	v_mul_f32_e32 v0, 0x4f7ffffe, v6
	v_cvt_u32_f32_e32 v0, v0
	s_sub_i32 s0, 0, s62
	s_mul_i32 s0, s0, s1
	s_mul_hi_u32 s0, s1, s0
	s_add_i32 s66, s1, s0
	s_sub_i32 s0, 0, s64
	v_readfirstlane_b32 s1, v0
	v_add_u16_e32 v0, v1, v10
	s_waitcnt vmcnt(6)
	s_mul_i32 s0, s0, s1
	v_lshrrev_b16_e32 v0, 1, v0
	v_and_b32_e32 v230, 0x70, v13
	s_mul_hi_u32 s0, s1, s0
	v_add_lshl_u32 v184, v11, v0, 1
	v_add_lshl_u32 v186, v12, v0, 1
	s_add_i32 s69, 0, 0x10000
	s_add_i32 s70, 0, 0x14000
	v_mbcnt_lo_u32_b32 v0, -1, 0
	s_mov_b32 s27, 0x20000
	s_lshl_b32 s60, s34, 6
	s_waitcnt lgkmcnt(0)
	s_ashr_i32 s63, s55, 31
	s_mov_b32 s26, 0x6000000
	s_and_b32 s25, s9, 0xffff
	s_mov_b32 s24, s8
	s_bfe_i32 s65, s33, 0x1001c
	s_ashr_i32 s67, s33, 31
	s_add_i32 s68, s1, s0
	v_mov_b32_e32 v185, v179
	v_mov_b32_e32 v187, v179
	v_mov_b64_e32 v[188:189], s[6:7]
	v_add_u32_e32 v231, s69, v228
	v_add_u32_e32 v232, 0, v3
	v_add_u32_e32 v233, s70, v228
	s_movk_i32 s71, 0x600
	s_movk_i32 s72, 0x300
	v_mbcnt_hi_u32_b32 v234, -1, v0
	v_add_u32_e32 v235, v5, v2
	v_add_u32_e32 v236, v4, v230
	s_movk_i32 s73, 0x60
	s_mov_b32 s74, 0x30000
	s_mov_b32 s75, 0x36000
	s_lshl_b32 s34, s34, 3
	s_movk_i32 s76, 0x3000
	s_mov_b32 s77, 0x3c000
	s_mov_b32 s78, 0x42000
	s_movk_i32 s79, 0x1000
	s_mov_b32 s80, s35
	s_barrier
	s_cmpk_gt_u32 s44, 0xff
	s_cbranch_scc0 .Lprio10_done
	s_setprio 1
.Lprio10_done:
.LBB10_12:
	s_add_i32 s80, s80, 1
	s_mul_i32 s0, s80, s63
	s_mul_hi_u32 s1, s80, s55
	s_add_i32 s1, s1, s0
	s_mul_i32 s0, s80, s55
	s_add_u32 s0, s0, s2
	s_addc_u32 s1, s1, s47
	v_cmp_ge_i64_e32 vcc, s[0:1], v[188:189]
	s_and_b64 s[6:7], exec, vcc
	s_mov_b64 vcc, s[6:7]
	s_cbranch_vccnz .LBB10_22
	s_ashr_i32 s8, s0, 31
	s_lshr_b32 s8, s8, 29
	s_add_i32 s42, s0, s8
	s_and_b32 s8, s42, -8
	s_sub_i32 s43, s0, s8
	s_cmp_ge_i32 s43, s46
	s_mov_b64 s[8:9], -1
	s_cbranch_scc0 .LBB10_15
	s_sub_i32 s8, s43, s46
	s_mul_i32 s8, s8, s45
	s_add_i32 s81, s8, s49
	s_mov_b64 s[8:9], 0

.LBB10_27:
	ds_read_b128 v[72:75], v231
	ds_read_b128 v[80:83], v231 offset:1024
	ds_read_b128 v[88:91], v231 offset:2048
	ds_read_b128 v[92:95], v231 offset:3072
	s_add_u32 s40, s38, 0xfff40080
	s_addc_u32 s41, s39, -1
	s_cmp_eq_u32 s87, 44
	s_cselect_b32 s43, s9, s41
	s_cselect_b32 s42, s8, s40
	s_cselect_b32 s41, s1, s86
	s_cselect_b32 s40, s0, s85
	v_lshl_add_u64 v[190:191], s[38:39], 0, v[184:185]
	s_add_i32 m0, s51, 0xc000
	ds_read_b128 v[136:139], v232
	ds_read_b128 v[148:151], v232 offset:1024
	ds_read_b128 v[152:155], v232 offset:2048
	ds_read_b128 v[156:159], v232 offset:3072
	ds_read_b128 v[160:163], v232 offset:4096
	ds_read_b128 v[164:167], v232 offset:5120
	ds_read_b128 v[168:171], v232 offset:6144
	ds_read_b128 v[172:175], v232 offset:7168
	global_load_lds_dwordx4 v[190:191], off
	v_lshl_add_u64 v[190:191], s[38:39], 0, v[186:187]
	s_add_i32 m0, s51, 0xe000
	s_nop 0
	global_load_lds_dwordx4 v[190:191], off
	s_waitcnt lgkmcnt(8)
	s_barrier
	s_waitcnt lgkmcnt(0)
	s_waitcnt lgkmcnt(0)
	v_mfma_f32_16x16x32_f16 v[144:147], v[72:75], v[136:139], v[144:147]
	v_mfma_f32_16x16x32_f16 v[140:143], v[88:91], v[136:139], v[140:143]
	v_mfma_f32_16x16x32_f16 v[124:127], v[72:75], v[152:155], v[124:127]
	v_mfma_f32_16x16x32_f16 v[120:123], v[88:91], v[152:155], v[120:123]
	v_mfma_f32_16x16x32_f16 v[108:111], v[72:75], v[160:163], v[108:111]
	v_mfma_f32_16x16x32_f16 v[104:107], v[88:91], v[160:163], v[104:107]
	v_mfma_f32_16x16x32_f16 v[84:87], v[72:75], v[168:171], v[84:87]
	v_mfma_f32_16x16x32_f16 v[76:79], v[88:91], v[168:171], v[76:79]
	v_mfma_f32_16x16x32_f16 v[144:147], v[80:83], v[148:151], v[144:147]
	v_mfma_f32_16x16x32_f16 v[140:143], v[92:95], v[148:151], v[140:143]
	v_mfma_f32_16x16x32_f16 v[124:127], v[80:83], v[156:159], v[124:127]
	v_mfma_f32_16x16x32_f16 v[120:123], v[92:95], v[156:159], v[120:123]
	v_mfma_f32_16x16x32_f16 v[108:111], v[80:83], v[164:167], v[108:111]
	v_mfma_f32_16x16x32_f16 v[104:107], v[92:95], v[164:167], v[104:107]
	v_mfma_f32_16x16x32_f16 v[84:87], v[80:83], v[172:175], v[84:87]
	v_mfma_f32_16x16x32_f16 v[76:79], v[92:95], v[172:175], v[76:79]
	s_barrier
	s_add_i32 s88, s69, s50
	v_lshl_add_u64 v[206:207], s[40:41], 0, v[178:179]
	s_mov_b32 m0, s88
	ds_read_b128 v[190:193], v233
	ds_read_b128 v[194:197], v233 offset:1024
	ds_read_b128 v[198:201], v233 offset:2048
	ds_read_b128 v[202:205], v233 offset:3072
	global_load_lds_dwordx4 v[206:207], off
	v_lshl_add_u64 v[208:209], s[40:41], 0, v[182:183]
	s_add_i32 m0, s88, 0x2000
	s_nop 0
	global_load_lds_dwordx4 v[208:209], off
	s_barrier
	s_waitcnt lgkmcnt(0)
	s_waitcnt lgkmcnt(0)
	v_mfma_f32_16x16x32_f16 v[132:135], v[190:193], v[136:139], v[132:135]
	v_mfma_f32_16x16x32_f16 v[128:131], v[198:201], v[136:139], v[128:131]
	v_mfma_f32_16x16x32_f16 v[116:119], v[190:193], v[152:155], v[116:119]
	v_mfma_f32_16x16x32_f16 v[112:115], v[198:201], v[152:155], v[112:115]
	v_mfma_f32_16x16x32_f16 v[100:103], v[190:193], v[160:163], v[100:103]
	v_mfma_f32_16x16x32_f16 v[96:99], v[198:201], v[160:163], v[96:99]
	v_mfma_f32_16x16x32_f16 v[68:71], v[190:193], v[168:171], v[68:71]
	v_mfma_f32_16x16x32_f16 v[64:67], v[198:201], v[168:171], v[64:67]
	v_mfma_f32_16x16x32_f16 v[132:135], v[194:197], v[148:151], v[132:135]
	v_mfma_f32_16x16x32_f16 v[128:131], v[202:205], v[148:151], v[128:131]
	v_mfma_f32_16x16x32_f16 v[116:119], v[194:197], v[156:159], v[116:119]
	v_mfma_f32_16x16x32_f16 v[112:115], v[202:205], v[156:159], v[112:115]
	v_mfma_f32_16x16x32_f16 v[100:103], v[194:197], v[164:167], v[100:103]
	v_mfma_f32_16x16x32_f16 v[96:99], v[202:205], v[164:167], v[96:99]
	v_mfma_f32_16x16x32_f16 v[68:71], v[194:197], v[172:175], v[68:71]
	v_mfma_f32_16x16x32_f16 v[64:67], v[202:205], v[172:175], v[64:67]
	s_mov_b32 m0, s51
	v_lshl_add_u64 v[210:211], s[42:43], 0, v[176:177]
	s_barrier
	ds_read_b128 v[136:139], v232 offset:16384
	ds_read_b128 v[148:151], v232 offset:17408
	ds_read_b128 v[152:155], v232 offset:18432
	ds_read_b128 v[156:159], v232 offset:19456
	ds_read_b128 v[160:163], v232 offset:20480
	ds_read_b128 v[164:167], v232 offset:21504
	ds_read_b128 v[168:171], v232 offset:22528
	ds_read_b128 v[172:175], v232 offset:23552
	global_load_lds_dwordx4 v[210:211], off
	v_lshl_add_u64 v[212:213], s[42:43], 0, v[180:181]
	s_mov_b32 m0, s52
	s_nop 0
	global_load_lds_dwordx4 v[212:213], off
	s_barrier
	s_waitcnt lgkmcnt(0)
	s_waitcnt lgkmcnt(0)
	v_mfma_f32_16x16x32_f16 v[60:63], v[72:75], v[136:139], v[60:63]
	v_mfma_f32_16x16x32_f16 v[56:59], v[88:91], v[136:139], v[56:59]
	v_mfma_f32_16x16x32_f16 v[44:47], v[72:75], v[152:155], v[44:47]
	v_mfma_f32_16x16x32_f16 v[40:43], v[88:91], v[152:155], v[40:43]
	v_mfma_f32_16x16x32_f16 v[28:31], v[72:75], v[160:163], v[28:31]
	v_mfma_f32_16x16x32_f16 v[24:27], v[88:91], v[160:163], v[24:27]
	v_mfma_f32_16x16x32_f16 v[12:15], v[72:75], v[168:171], v[12:15]
	v_mfma_f32_16x16x32_f16 v[8:11], v[88:91], v[168:171], v[8:11]
	v_mfma_f32_16x16x32_f16 v[60:63], v[80:83], v[148:151], v[60:63]
	v_mfma_f32_16x16x32_f16 v[56:59], v[92:95], v[148:151], v[56:59]
	v_mfma_f32_16x16x32_f16 v[44:47], v[80:83], v[156:159], v[44:47]
	v_mfma_f32_16x16x32_f16 v[40:43], v[92:95], v[156:159], v[40:43]
	v_mfma_f32_16x16x32_f16 v[28:31], v[80:83], v[164:167], v[28:31]
	v_mfma_f32_16x16x32_f16 v[24:27], v[92:95], v[164:167], v[24:27]
	v_mfma_f32_16x16x32_f16 v[12:15], v[80:83], v[172:175], v[12:15]
	v_mfma_f32_16x16x32_f16 v[8:11], v[92:95], v[172:175], v[8:11]
	s_barrier
	s_add_u32 s88, s40, 0x30000
	s_addc_u32 s89, s41, 0
	s_add_i32 s90, s70, s50
	v_lshl_add_u64 v[72:73], s[88:89], 0, v[178:179]
	s_mov_b32 m0, s90
	s_nop 0
	global_load_lds_dwordx4 v[72:73], off
	v_lshl_add_u64 v[72:73], s[88:89], 0, v[182:183]
	s_add_i32 m0, s90, 0x2000
	s_nop 0
	global_load_lds_dwordx4 v[72:73], off
	s_waitcnt vmcnt(6)
	s_barrier
	v_mfma_f32_16x16x32_f16 v[52:55], v[190:193], v[136:139], v[52:55]
	v_mfma_f32_16x16x32_f16 v[48:51], v[198:201], v[136:139], v[48:51]
	v_mfma_f32_16x16x32_f16 v[36:39], v[190:193], v[152:155], v[36:39]
	v_mfma_f32_16x16x32_f16 v[32:35], v[198:201], v[152:155], v[32:35]
	v_mfma_f32_16x16x32_f16 v[20:23], v[190:193], v[160:163], v[20:23]
	v_mfma_f32_16x16x32_f16 v[16:19], v[198:201], v[160:163], v[16:19]
	v_mfma_f32_16x16x32_f16 v[4:7], v[190:193], v[168:171], v[4:7]
	v_mfma_f32_16x16x32_f16 v[0:3], v[198:201], v[168:171], v[0:3]
	v_mfma_f32_16x16x32_f16 v[52:55], v[194:197], v[148:151], v[52:55]
	v_mfma_f32_16x16x32_f16 v[48:51], v[202:205], v[148:151], v[48:51]
	v_mfma_f32_16x16x32_f16 v[36:39], v[194:197], v[156:159], v[36:39]
	v_mfma_f32_16x16x32_f16 v[32:35], v[202:205], v[156:159], v[32:35]
	v_mfma_f32_16x16x32_f16 v[20:23], v[194:197], v[164:167], v[20:23]
	v_mfma_f32_16x16x32_f16 v[16:19], v[202:205], v[164:167], v[16:19]
	v_mfma_f32_16x16x32_f16 v[4:7], v[194:197], v[172:175], v[4:7]
	v_mfma_f32_16x16x32_f16 v[0:3], v[202:205], v[172:175], v[0:3]
	s_add_i32 s88, 0, 0x18000
	v_add_u32_e32 v92, s88, v228
	s_barrier
	ds_read_b128 v[72:75], v92
	ds_read_b128 v[80:83], v92 offset:1024
	ds_read_b128 v[88:91], v92 offset:2048
	ds_read_b128 v[92:95], v92 offset:3072
	s_add_u32 s42, s42, 0xc0000
	s_addc_u32 s43, s43, 0
	s_mov_b32 m0, s53
	v_lshl_add_u64 v[190:191], s[42:43], 0, v[176:177]
	ds_read_b128 v[136:139], v232 offset:32768
	ds_read_b128 v[148:151], v232 offset:33792
	ds_read_b128 v[152:155], v232 offset:34816
	ds_read_b128 v[156:159], v232 offset:35840
	ds_read_b128 v[160:163], v232 offset:36864
	ds_read_b128 v[164:167], v232 offset:37888
	ds_read_b128 v[168:171], v232 offset:38912
	ds_read_b128 v[172:175], v232 offset:39936
	global_load_lds_dwordx4 v[190:191], off
	v_lshl_add_u64 v[190:191], s[42:43], 0, v[180:181]
	s_mov_b32 m0, s54
	s_nop 0
	global_load_lds_dwordx4 v[190:191], off
	s_waitcnt lgkmcnt(8)
	s_barrier
	s_waitcnt lgkmcnt(0)
	s_waitcnt lgkmcnt(0)
	v_mfma_f32_16x16x32_f16 v[144:147], v[72:75], v[136:139], v[144:147]
	v_mfma_f32_16x16x32_f16 v[140:143], v[88:91], v[136:139], v[140:143]
	v_mfma_f32_16x16x32_f16 v[124:127], v[72:75], v[152:155], v[124:127]
	v_mfma_f32_16x16x32_f16 v[120:123], v[88:91], v[152:155], v[120:123]
	v_mfma_f32_16x16x32_f16 v[108:111], v[72:75], v[160:163], v[108:111]
	v_mfma_f32_16x16x32_f16 v[104:107], v[88:91], v[160:163], v[104:107]
	v_mfma_f32_16x16x32_f16 v[84:87], v[72:75], v[168:171], v[84:87]
	v_mfma_f32_16x16x32_f16 v[76:79], v[88:91], v[168:171], v[76:79]
	v_mfma_f32_16x16x32_f16 v[144:147], v[80:83], v[148:151], v[144:147]
	v_mfma_f32_16x16x32_f16 v[140:143], v[92:95], v[148:151], v[140:143]
	v_mfma_f32_16x16x32_f16 v[124:127], v[80:83], v[156:159], v[124:127]
	v_mfma_f32_16x16x32_f16 v[120:123], v[92:95], v[156:159], v[120:123]
	v_mfma_f32_16x16x32_f16 v[108:111], v[80:83], v[164:167], v[108:111]
	v_mfma_f32_16x16x32_f16 v[104:107], v[92:95], v[164:167], v[104:107]
	v_mfma_f32_16x16x32_f16 v[84:87], v[80:83], v[172:175], v[84:87]
	v_mfma_f32_16x16x32_f16 v[76:79], v[92:95], v[172:175], v[76:79]
	s_barrier
	s_add_i32 s42, 0, 0x1c000
	s_add_i32 s43, s88, s50
	v_add_u32_e32 v202, s42, v228
	v_lshl_add_u64 v[206:207], v[206:207], 0, s[36:37]
	s_mov_b32 m0, s43
	ds_read_b128 v[190:193], v202
	ds_read_b128 v[194:197], v202 offset:1024
	ds_read_b128 v[198:201], v202 offset:2048
	ds_read_b128 v[202:205], v202 offset:3072
	global_load_lds_dwordx4 v[206:207], off
	v_lshl_add_u64 v[206:207], v[208:209], 0, s[36:37]
	s_add_i32 m0, s43, 0x2000
	s_nop 0
	global_load_lds_dwordx4 v[206:207], off
	s_barrier
	s_waitcnt lgkmcnt(0)
	s_waitcnt lgkmcnt(0)
	v_mfma_f32_16x16x32_f16 v[132:135], v[190:193], v[136:139], v[132:135]
	v_mfma_f32_16x16x32_f16 v[128:131], v[198:201], v[136:139], v[128:131]
	v_mfma_f32_16x16x32_f16 v[116:119], v[190:193], v[152:155], v[116:119]
	v_mfma_f32_16x16x32_f16 v[112:115], v[198:201], v[152:155], v[112:115]
	v_mfma_f32_16x16x32_f16 v[100:103], v[190:193], v[160:163], v[100:103]
	v_mfma_f32_16x16x32_f16 v[96:99], v[198:201], v[160:163], v[96:99]
	v_mfma_f32_16x16x32_f16 v[68:71], v[190:193], v[168:171], v[68:71]
	v_mfma_f32_16x16x32_f16 v[64:67], v[198:201], v[168:171], v[64:67]
	v_mfma_f32_16x16x32_f16 v[132:135], v[194:197], v[148:151], v[132:135]
	v_mfma_f32_16x16x32_f16 v[128:131], v[202:205], v[148:151], v[128:131]
	v_mfma_f32_16x16x32_f16 v[116:119], v[194:197], v[156:159], v[116:119]
	v_mfma_f32_16x16x32_f16 v[112:115], v[202:205], v[156:159], v[112:115]
	v_mfma_f32_16x16x32_f16 v[100:103], v[194:197], v[164:167], v[100:103]
	v_mfma_f32_16x16x32_f16 v[96:99], v[202:205], v[164:167], v[96:99]
	v_mfma_f32_16x16x32_f16 v[68:71], v[194:197], v[172:175], v[68:71]
	v_mfma_f32_16x16x32_f16 v[64:67], v[202:205], v[172:175], v[64:67]
	s_mov_b32 m0, s58
	v_lshl_add_u64 v[206:207], v[210:211], 0, s[36:37]
	s_barrier
	ds_read_b128 v[136:139], v232 offset:49152
	ds_read_b128 v[148:151], v232 offset:50176
	ds_read_b128 v[152:155], v232 offset:51200
	ds_read_b128 v[156:159], v232 offset:52224
	ds_read_b128 v[160:163], v232 offset:53248
	ds_read_b128 v[164:167], v232 offset:54272
	ds_read_b128 v[168:171], v232 offset:55296
	ds_read_b128 v[172:175], v232 offset:56320
	global_load_lds_dwordx4 v[206:207], off
	v_lshl_add_u64 v[206:207], v[212:213], 0, s[36:37]
	s_mov_b32 m0, s59
	s_nop 0
	global_load_lds_dwordx4 v[206:207], off
	s_barrier
	s_waitcnt lgkmcnt(0)
	s_waitcnt lgkmcnt(0)
	v_mfma_f32_16x16x32_f16 v[60:63], v[72:75], v[136:139], v[60:63]
	v_mfma_f32_16x16x32_f16 v[56:59], v[88:91], v[136:139], v[56:59]
	v_mfma_f32_16x16x32_f16 v[44:47], v[72:75], v[152:155], v[44:47]
	v_mfma_f32_16x16x32_f16 v[40:43], v[88:91], v[152:155], v[40:43]
	v_mfma_f32_16x16x32_f16 v[28:31], v[72:75], v[160:163], v[28:31]
	v_mfma_f32_16x16x32_f16 v[24:27], v[88:91], v[160:163], v[24:27]
	v_mfma_f32_16x16x32_f16 v[12:15], v[72:75], v[168:171], v[12:15]
	v_mfma_f32_16x16x32_f16 v[8:11], v[88:91], v[168:171], v[8:11]
	v_mfma_f32_16x16x32_f16 v[60:63], v[80:83], v[148:151], v[60:63]
	v_mfma_f32_16x16x32_f16 v[56:59], v[92:95], v[148:151], v[56:59]
	v_mfma_f32_16x16x32_f16 v[44:47], v[80:83], v[156:159], v[44:47]
	v_mfma_f32_16x16x32_f16 v[40:43], v[92:95], v[156:159], v[40:43]
	v_mfma_f32_16x16x32_f16 v[28:31], v[80:83], v[164:167], v[28:31]
	v_mfma_f32_16x16x32_f16 v[24:27], v[92:95], v[164:167], v[24:27]
	v_mfma_f32_16x16x32_f16 v[12:15], v[80:83], v[172:175], v[12:15]
	v_mfma_f32_16x16x32_f16 v[8:11], v[92:95], v[172:175], v[8:11]
	s_barrier
	s_add_u32 s40, s40, 0x30080
	s_addc_u32 s41, s41, 0
	s_add_i32 s42, s42, s50
	v_lshl_add_u64 v[72:73], s[40:41], 0, v[178:179]
	s_mov_b32 m0, s42
	s_nop 0
	global_load_lds_dwordx4 v[72:73], off
	v_lshl_add_u64 v[72:73], s[40:41], 0, v[182:183]
	s_add_i32 m0, s42, 0x2000
	s_nop 0
	global_load_lds_dwordx4 v[72:73], off
	s_waitcnt vmcnt(6)
	s_barrier
	v_mfma_f32_16x16x32_f16 v[52:55], v[190:193], v[136:139], v[52:55]
	v_mfma_f32_16x16x32_f16 v[48:51], v[198:201], v[136:139], v[48:51]
	v_mfma_f32_16x16x32_f16 v[36:39], v[190:193], v[152:155], v[36:39]
	v_mfma_f32_16x16x32_f16 v[32:35], v[198:201], v[152:155], v[32:35]
	v_mfma_f32_16x16x32_f16 v[20:23], v[190:193], v[160:163], v[20:23]
	v_mfma_f32_16x16x32_f16 v[16:19], v[198:201], v[160:163], v[16:19]
	v_mfma_f32_16x16x32_f16 v[4:7], v[190:193], v[168:171], v[4:7]
	v_mfma_f32_16x16x32_f16 v[0:3], v[198:201], v[168:171], v[0:3]
	v_mfma_f32_16x16x32_f16 v[52:55], v[194:197], v[148:151], v[52:55]
	v_mfma_f32_16x16x32_f16 v[48:51], v[202:205], v[148:151], v[48:51]
	v_mfma_f32_16x16x32_f16 v[36:39], v[194:197], v[156:159], v[36:39]
	v_mfma_f32_16x16x32_f16 v[32:35], v[202:205], v[156:159], v[32:35]
	v_mfma_f32_16x16x32_f16 v[20:23], v[194:197], v[164:167], v[20:23]
	v_mfma_f32_16x16x32_f16 v[16:19], v[202:205], v[164:167], v[16:19]
	v_mfma_f32_16x16x32_f16 v[4:7], v[194:197], v[172:175], v[4:7]
	v_mfma_f32_16x16x32_f16 v[0:3], v[202:205], v[172:175], v[0:3]
	s_add_i32 s87, s87, 2
	s_add_u32 s38, s38, 0x100
	s_addc_u32 s39, s39, 0
	s_add_u32 s85, s85, 0x100
	s_addc_u32 s86, s86, 0
	s_cmp_gt_u32 s87, 45
	s_barrier
	s_cbranch_scc0 .LBB10_27
	s_lshl_b32 s92, s84, 8
	s_add_i32 s92, s92, s57
	s_lshl_b32 s93, s83, 8
	s_or_b32 s93, s93, s60
	v_lshlrev_b32_e32 v237, 2, v226
	s_lshl_b32 s96, s93, 2
	s_add_u32 s94, s16, s96
	s_addc_u32 s95, s17, 0
	global_load_dwordx4 v[72:75], v237, s[94:95] offset:0
	global_load_dwordx4 v[80:83], v237, s[94:95] offset:16
	global_load_dwordx4 v[88:91], v237, s[94:95] offset:128
	global_load_dwordx4 v[92:95], v237, s[94:95] offset:144
	s_add_u32 s94, s18, s96
	s_addc_u32 s95, s19, 0
	global_load_dwordx4 v[136:139], v237, s[94:95] offset:0
	global_load_dwordx4 v[148:151], v237, s[94:95] offset:16
	global_load_dwordx4 v[152:155], v237, s[94:95] offset:128
	global_load_dwordx4 v[156:159], v237, s[94:95] offset:144
	s_add_u32 s94, s14, s96
	s_addc_u32 s95, s15, 0
	global_load_dwordx4 v[160:163], v237, s[94:95] offset:0
	global_load_dwordx4 v[164:167], v237, s[94:95] offset:16
	global_load_dwordx4 v[168:171], v237, s[94:95] offset:128
	global_load_dwordx4 v[172:175], v237, s[94:95] offset:144
	v_lshlrev_b32_e32 v190, 3, v227
	s_lshl_b32 s96, s92, 3
	s_add_u32 s94, s12, s96
	s_addc_u32 s95, s13, 0
	global_load_dwordx2 v[238:239], v190, s[94:95] offset:0
	global_load_dwordx2 v[192:193], v190, s[94:95] offset:128
	global_load_dwordx2 v[194:195], v190, s[94:95] offset:256
	global_load_dwordx2 v[196:197], v190, s[94:95] offset:384
	global_load_dwordx2 v[198:199], v190, s[94:95] offset:1024
	global_load_dwordx2 v[200:201], v190, s[94:95] offset:1152
	global_load_dwordx2 v[202:203], v190, s[94:95] offset:1280
	global_load_dwordx2 v[204:205], v190, s[94:95] offset:1408
	v_mul_u32_u24_e32 v191, 0x600, v227
	v_lshl_add_u32 v191, v226, 1, v191
	s_mul_i32 s96, s92, 0x600
	s_lshl_b32 s97, s93, 1
	s_add_u32 s96, s96, s97
	s_add_u32 s98, s10, s96
	s_addc_u32 s99, s11, 0
	s_add_u32 s94, s98, 0x0
	s_addc_u32 s95, s99, 0
	global_load_dwordx4 v[208:211], v191, s[94:95] offset:0 nt
	global_load_dwordx4 v[212:215], v191, s[94:95] offset:64 nt
	s_add_u32 s94, s98, 0x6000
	s_addc_u32 s95, s99, 0
	global_load_dwordx4 v[216:219], v191, s[94:95] offset:0 nt
	global_load_dwordx4 v[220:223], v191, s[94:95] offset:64 nt
	v_add_u32_e32 v224, s92, v229
	v_mul_u32_u24_e32 v224, 0x600, v224
	s_lshl_b32 s97, s93, 1
	v_add3_u32 v224, v224, v230, s97
	s_lshl_b32 s96, s83, 2
	s_lshr_b32 s97, s60, 6
	s_add_u32 s96, s96, s97
	s_lshl_b32 s96, s96, 19
	s_lshl_b32 s97, s92, 3
	s_add_u32 s96, s96, s97
	s_add_u32 s100, s28, s96
	s_addc_u32 s101, s29, 0
	s_waitcnt vmcnt(19)
	v_pk_add_f32 v[72:73], v[72:73], v[136:137]
	v_pk_add_f32 v[74:75], v[74:75], v[138:139]
	s_waitcnt vmcnt(18)
	v_pk_add_f32 v[80:81], v[80:81], v[148:149]
	v_pk_add_f32 v[82:83], v[82:83], v[150:151]
	s_waitcnt vmcnt(17)
	v_pk_add_f32 v[88:89], v[88:89], v[152:153]
	v_pk_add_f32 v[90:91], v[90:91], v[154:155]
	s_waitcnt vmcnt(16)
	v_pk_add_f32 v[92:93], v[92:93], v[156:157]
	v_pk_add_f32 v[94:95], v[94:95], v[158:159]
	v_pk_add_f32 v[144:145], v[144:145], v[72:73]
	v_pk_add_f32 v[146:147], v[146:147], v[74:75]
	v_pk_add_f32 v[124:125], v[124:125], v[72:73]
	v_pk_add_f32 v[126:127], v[126:127], v[74:75]
	v_pk_add_f32 v[108:109], v[108:109], v[72:73]
	v_pk_add_f32 v[110:111], v[110:111], v[74:75]
	v_pk_add_f32 v[84:85], v[84:85], v[72:73]
	v_pk_add_f32 v[86:87], v[86:87], v[74:75]
	v_pk_add_f32 v[60:61], v[60:61], v[72:73]
	v_pk_add_f32 v[62:63], v[62:63], v[74:75]
	v_pk_add_f32 v[44:45], v[44:45], v[72:73]
	v_pk_add_f32 v[46:47], v[46:47], v[74:75]
	v_pk_add_f32 v[28:29], v[28:29], v[72:73]
	v_pk_add_f32 v[30:31], v[30:31], v[74:75]
	v_pk_add_f32 v[12:13], v[12:13], v[72:73]
	v_pk_add_f32 v[14:15], v[14:15], v[74:75]
	v_pk_add_f32 v[140:141], v[140:141], v[80:81]
	v_pk_add_f32 v[142:143], v[142:143], v[82:83]
	v_pk_add_f32 v[120:121], v[120:121], v[80:81]
	v_pk_add_f32 v[122:123], v[122:123], v[82:83]
	v_pk_add_f32 v[104:105], v[104:105], v[80:81]
	v_pk_add_f32 v[106:107], v[106:107], v[82:83]
	v_pk_add_f32 v[76:77], v[76:77], v[80:81]
	v_pk_add_f32 v[78:79], v[78:79], v[82:83]
	v_pk_add_f32 v[56:57], v[56:57], v[80:81]
	v_pk_add_f32 v[58:59], v[58:59], v[82:83]
	v_pk_add_f32 v[40:41], v[40:41], v[80:81]
	v_pk_add_f32 v[42:43], v[42:43], v[82:83]
	v_pk_add_f32 v[24:25], v[24:25], v[80:81]
	v_pk_add_f32 v[26:27], v[26:27], v[82:83]
	v_pk_add_f32 v[8:9], v[8:9], v[80:81]
	v_pk_add_f32 v[10:11], v[10:11], v[82:83]
	v_pk_add_f32 v[132:133], v[132:133], v[88:89]
	v_pk_add_f32 v[134:135], v[134:135], v[90:91]
	v_pk_add_f32 v[116:117], v[116:117], v[88:89]
	v_pk_add_f32 v[118:119], v[118:119], v[90:91]
	v_pk_add_f32 v[100:101], v[100:101], v[88:89]
	v_pk_add_f32 v[102:103], v[102:103], v[90:91]
	v_pk_add_f32 v[68:69], v[68:69], v[88:89]
	v_pk_add_f32 v[70:71], v[70:71], v[90:91]
	v_pk_add_f32 v[52:53], v[52:53], v[88:89]
	v_pk_add_f32 v[54:55], v[54:55], v[90:91]
	v_pk_add_f32 v[36:37], v[36:37], v[88:89]
	v_pk_add_f32 v[38:39], v[38:39], v[90:91]
	v_pk_add_f32 v[20:21], v[20:21], v[88:89]
	v_pk_add_f32 v[22:23], v[22:23], v[90:91]
	v_pk_add_f32 v[4:5], v[4:5], v[88:89]
	v_pk_add_f32 v[6:7], v[6:7], v[90:91]
	v_pk_add_f32 v[128:129], v[128:129], v[92:93]
	v_pk_add_f32 v[130:131], v[130:131], v[94:95]
	v_pk_add_f32 v[112:113], v[112:113], v[92:93]
	v_pk_add_f32 v[114:115], v[114:115], v[94:95]
	v_pk_add_f32 v[96:97], v[96:97], v[92:93]
	v_pk_add_f32 v[98:99], v[98:99], v[94:95]
	v_pk_add_f32 v[64:65], v[64:65], v[92:93]
	v_pk_add_f32 v[66:67], v[66:67], v[94:95]
	v_pk_add_f32 v[48:49], v[48:49], v[92:93]
	v_pk_add_f32 v[50:51], v[50:51], v[94:95]
	v_pk_add_f32 v[32:33], v[32:33], v[92:93]
	v_pk_add_f32 v[34:35], v[34:35], v[94:95]
	v_pk_add_f32 v[16:17], v[16:17], v[92:93]
	v_pk_add_f32 v[18:19], v[18:19], v[94:95]
	v_pk_add_f32 v[0:1], v[0:1], v[92:93]
	v_pk_add_f32 v[2:3], v[2:3], v[94:95]
	s_add_u32 s94, s98, 0xc000
	s_addc_u32 s95, s99, 0
	global_load_dwordx4 v[240:243], v191, s[94:95] offset:0 nt
	global_load_dwordx4 v[244:247], v191, s[94:95] offset:64 nt
	s_add_u32 s94, s98, 0x12000
	s_addc_u32 s95, s99, 0
	global_load_dwordx4 v[248:251], v191, s[94:95] offset:0 nt
	global_load_dwordx4 v[252:255], v191, s[94:95] offset:64 nt
	s_add_u32 s94, s98, 0x30000
	s_addc_u32 s95, s99, 0
	global_load_dwordx4 v[136:139], v191, s[94:95] offset:0 nt
	global_load_dwordx4 v[148:151], v191, s[94:95] offset:64 nt
	s_add_u32 s94, s98, 0x36000
	s_addc_u32 s95, s99, 0
	global_load_dwordx4 v[152:155], v191, s[94:95] offset:0 nt
	global_load_dwordx4 v[156:159], v191, s[94:95] offset:64 nt
	s_waitcnt vmcnt(19)
	s_waitcnt vmcnt(11)
	v_cvt_f32_f16_e32 v72, v208
	v_cvt_f32_f16_sdwa v73, v208 dst_sel:DWORD dst_unused:UNUSED_PAD src0_sel:WORD_1
	v_cvt_f32_f16_e32 v74, v209
	v_cvt_f32_f16_sdwa v75, v209 dst_sel:DWORD dst_unused:UNUSED_PAD src0_sel:WORD_1
	v_cvt_f32_f16_e32 v80, v210
	v_cvt_f32_f16_sdwa v81, v210 dst_sel:DWORD dst_unused:UNUSED_PAD src0_sel:WORD_1
	v_cvt_f32_f16_e32 v82, v211
	v_cvt_f32_f16_sdwa v83, v211 dst_sel:DWORD dst_unused:UNUSED_PAD src0_sel:WORD_1
	v_sub_f32_e32 v72, v72, v238
	v_sub_f32_e32 v73, v73, v238
	v_sub_f32_e32 v74, v74, v238
	v_sub_f32_e32 v75, v75, v238
	v_sub_f32_e32 v80, v80, v238
	v_sub_f32_e32 v81, v81, v238
	v_sub_f32_e32 v82, v82, v238
	v_sub_f32_e32 v83, v83, v238
	v_pk_mul_f32 v[72:73], v[238:239], v[72:73] op_sel:[1,0]
	v_pk_mul_f32 v[74:75], v[238:239], v[74:75] op_sel:[1,0]
	v_pk_mul_f32 v[80:81], v[238:239], v[80:81] op_sel:[1,0]
	v_pk_mul_f32 v[82:83], v[238:239], v[82:83] op_sel:[1,0]
	v_pk_fma_f32 v[144:145], v[72:73], v[160:161], v[144:145]
	v_pk_fma_f32 v[146:147], v[74:75], v[162:163], v[146:147]
	v_pk_fma_f32 v[140:141], v[80:81], v[164:165], v[140:141]
	v_pk_fma_f32 v[142:143], v[82:83], v[166:167], v[142:143]
	v_cvt_pk_f16_f32 v144, v144, v145
	v_cvt_pk_f16_f32 v145, v146, v147
	v_cvt_pk_f16_f32 v146, v140, v141
	v_cvt_pk_f16_f32 v147, v142, v143
	ds_write_b128 v235, v[144:147]
	v_fma_mix_f32 v206, v144, 1.0, 0 op_sel_hi:[1,0,0]
	v_fma_mix_f32 v207, v144, v144, 0 op_sel_hi:[1,1,0]
	v_fma_mix_f32 v206, v144, 1.0, v206 op_sel:[1,0,0] op_sel_hi:[1,0,0]
	v_fma_mix_f32 v207, v144, v144, v207 op_sel:[1,1,0] op_sel_hi:[1,1,0]
	v_fma_mix_f32 v206, v145, 1.0, v206 op_sel_hi:[1,0,0]
	v_fma_mix_f32 v207, v145, v145, v207 op_sel_hi:[1,1,0]
	v_fma_mix_f32 v206, v145, 1.0, v206 op_sel:[1,0,0] op_sel_hi:[1,0,0]
	v_fma_mix_f32 v207, v145, v145, v207 op_sel:[1,1,0] op_sel_hi:[1,1,0]
	v_fma_mix_f32 v206, v146, 1.0, v206 op_sel_hi:[1,0,0]
	v_fma_mix_f32 v207, v146, v146, v207 op_sel_hi:[1,1,0]
	v_fma_mix_f32 v206, v146, 1.0, v206 op_sel:[1,0,0] op_sel_hi:[1,0,0]
	v_fma_mix_f32 v207, v146, v146, v207 op_sel:[1,1,0] op_sel_hi:[1,1,0]
	v_fma_mix_f32 v206, v147, 1.0, v206 op_sel_hi:[1,0,0]
	v_fma_mix_f32 v207, v147, v147, v207 op_sel_hi:[1,1,0]
	v_fma_mix_f32 v206, v147, 1.0, v206 op_sel:[1,0,0] op_sel_hi:[1,0,0]
	v_fma_mix_f32 v207, v147, v147, v207 op_sel:[1,1,0] op_sel_hi:[1,1,0]
	s_waitcnt vmcnt(10)
	v_cvt_f32_f16_e32 v72, v212
	v_cvt_f32_f16_sdwa v73, v212 dst_sel:DWORD dst_unused:UNUSED_PAD src0_sel:WORD_1
	v_cvt_f32_f16_e32 v74, v213
	v_cvt_f32_f16_sdwa v75, v213 dst_sel:DWORD dst_unused:UNUSED_PAD src0_sel:WORD_1
	v_cvt_f32_f16_e32 v80, v214
	v_cvt_f32_f16_sdwa v81, v214 dst_sel:DWORD dst_unused:UNUSED_PAD src0_sel:WORD_1
	v_cvt_f32_f16_e32 v82, v215
	v_cvt_f32_f16_sdwa v83, v215 dst_sel:DWORD dst_unused:UNUSED_PAD src0_sel:WORD_1
	v_sub_f32_e32 v72, v72, v238
	v_sub_f32_e32 v73, v73, v238
	v_sub_f32_e32 v74, v74, v238
	v_sub_f32_e32 v75, v75, v238
	v_sub_f32_e32 v80, v80, v238
	v_sub_f32_e32 v81, v81, v238
	v_sub_f32_e32 v82, v82, v238
	v_sub_f32_e32 v83, v83, v238
	v_pk_mul_f32 v[72:73], v[238:239], v[72:73] op_sel:[1,0]
	v_pk_mul_f32 v[74:75], v[238:239], v[74:75] op_sel:[1,0]
	v_pk_mul_f32 v[80:81], v[238:239], v[80:81] op_sel:[1,0]
	v_pk_mul_f32 v[82:83], v[238:239], v[82:83] op_sel:[1,0]
	v_pk_fma_f32 v[132:133], v[72:73], v[168:169], v[132:133]
	v_pk_fma_f32 v[134:135], v[74:75], v[170:171], v[134:135]
	v_pk_fma_f32 v[128:129], v[80:81], v[172:173], v[128:129]
	v_pk_fma_f32 v[130:131], v[82:83], v[174:175], v[130:131]
	v_cvt_pk_f16_f32 v132, v132, v133
	v_cvt_pk_f16_f32 v133, v134, v135
	v_cvt_pk_f16_f32 v134, v128, v129
	v_cvt_pk_f16_f32 v135, v130, v131
	ds_write_b128 v235, v[132:135] offset:64
	v_fma_mix_f32 v206, v132, 1.0, v206 op_sel_hi:[1,0,0]
	v_fma_mix_f32 v207, v132, v132, v207 op_sel_hi:[1,1,0]
	v_fma_mix_f32 v206, v132, 1.0, v206 op_sel:[1,0,0] op_sel_hi:[1,0,0]
	v_fma_mix_f32 v207, v132, v132, v207 op_sel:[1,1,0] op_sel_hi:[1,1,0]
	v_fma_mix_f32 v206, v133, 1.0, v206 op_sel_hi:[1,0,0]
	v_fma_mix_f32 v207, v133, v133, v207 op_sel_hi:[1,1,0]
	v_fma_mix_f32 v206, v133, 1.0, v206 op_sel:[1,0,0] op_sel_hi:[1,0,0]
	v_fma_mix_f32 v207, v133, v133, v207 op_sel:[1,1,0] op_sel_hi:[1,1,0]
	v_fma_mix_f32 v206, v134, 1.0, v206 op_sel_hi:[1,0,0]
	v_fma_mix_f32 v207, v134, v134, v207 op_sel_hi:[1,1,0]
	v_fma_mix_f32 v206, v134, 1.0, v206 op_sel:[1,0,0] op_sel_hi:[1,0,0]
	v_fma_mix_f32 v207, v134, v134, v207 op_sel:[1,1,0] op_sel_hi:[1,1,0]
	v_fma_mix_f32 v206, v135, 1.0, v206 op_sel_hi:[1,0,0]
	v_fma_mix_f32 v207, v135, v135, v207 op_sel_hi:[1,1,0]
	v_fma_mix_f32 v206, v135, 1.0, v206 op_sel:[1,0,0] op_sel_hi:[1,0,0]
	v_fma_mix_f32 v207, v135, v135, v207 op_sel:[1,1,0] op_sel_hi:[1,1,0]
	ds_read_b128 v[88:91], v236
	ds_read_b128 v[92:95], v236 offset:1152
	s_waitcnt vmcnt(9)
	v_cvt_f32_f16_e32 v72, v216
	v_cvt_f32_f16_sdwa v73, v216 dst_sel:DWORD dst_unused:UNUSED_PAD src0_sel:WORD_1
	v_cvt_f32_f16_e32 v74, v217
	v_cvt_f32_f16_sdwa v75, v217 dst_sel:DWORD dst_unused:UNUSED_PAD src0_sel:WORD_1
	v_cvt_f32_f16_e32 v80, v218
	v_cvt_f32_f16_sdwa v81, v218 dst_sel:DWORD dst_unused:UNUSED_PAD src0_sel:WORD_1
	v_cvt_f32_f16_e32 v82, v219
	v_cvt_f32_f16_sdwa v83, v219 dst_sel:DWORD dst_unused:UNUSED_PAD src0_sel:WORD_1
	v_sub_f32_e32 v72, v72, v192
	v_sub_f32_e32 v73, v73, v192
	v_sub_f32_e32 v74, v74, v192
	v_sub_f32_e32 v75, v75, v192
	v_sub_f32_e32 v80, v80, v192
	v_sub_f32_e32 v81, v81, v192
	v_sub_f32_e32 v82, v82, v192
	v_sub_f32_e32 v83, v83, v192
	v_pk_mul_f32 v[72:73], v[192:193], v[72:73] op_sel:[1,0]
	v_pk_mul_f32 v[74:75], v[192:193], v[74:75] op_sel:[1,0]
	v_pk_mul_f32 v[80:81], v[192:193], v[80:81] op_sel:[1,0]
	v_pk_mul_f32 v[82:83], v[192:193], v[82:83] op_sel:[1,0]
	v_pk_fma_f32 v[124:125], v[72:73], v[160:161], v[124:125]
	v_pk_fma_f32 v[126:127], v[74:75], v[162:163], v[126:127]
	v_pk_fma_f32 v[120:121], v[80:81], v[164:165], v[120:121]
	v_pk_fma_f32 v[122:123], v[82:83], v[166:167], v[122:123]
	v_cvt_pk_f16_f32 v124, v124, v125
	v_cvt_pk_f16_f32 v125, v126, v127
	v_cvt_pk_f16_f32 v126, v120, v121
	v_cvt_pk_f16_f32 v127, v122, v123
	s_waitcnt lgkmcnt(0)
	buffer_store_dwordx4 v[88:91], v224, s[24:27], 0 offen nt
	v_add_u32_e32 v82, 0x3000, v224
	buffer_store_dwordx4 v[92:95], v82, s[24:27], 0 offen nt
	ds_write_b128 v235, v[124:127]
	v_fma_mix_f32 v140, v124, 1.0, 0 op_sel_hi:[1,0,0]
	v_fma_mix_f32 v141, v124, v124, 0 op_sel_hi:[1,1,0]
	v_fma_mix_f32 v140, v124, 1.0, v140 op_sel:[1,0,0] op_sel_hi:[1,0,0]
	v_fma_mix_f32 v141, v124, v124, v141 op_sel:[1,1,0] op_sel_hi:[1,1,0]
	v_fma_mix_f32 v140, v125, 1.0, v140 op_sel_hi:[1,0,0]
	v_fma_mix_f32 v141, v125, v125, v141 op_sel_hi:[1,1,0]
	v_fma_mix_f32 v140, v125, 1.0, v140 op_sel:[1,0,0] op_sel_hi:[1,0,0]
	v_fma_mix_f32 v141, v125, v125, v141 op_sel:[1,1,0] op_sel_hi:[1,1,0]
	v_fma_mix_f32 v140, v126, 1.0, v140 op_sel_hi:[1,0,0]
	v_fma_mix_f32 v141, v126, v126, v141 op_sel_hi:[1,1,0]
	v_fma_mix_f32 v140, v126, 1.0, v140 op_sel:[1,0,0] op_sel_hi:[1,0,0]
	v_fma_mix_f32 v141, v126, v126, v141 op_sel:[1,1,0] op_sel_hi:[1,1,0]
	v_fma_mix_f32 v140, v127, 1.0, v140 op_sel_hi:[1,0,0]
	v_fma_mix_f32 v141, v127, v127, v141 op_sel_hi:[1,1,0]
	v_fma_mix_f32 v140, v127, 1.0, v140 op_sel:[1,0,0] op_sel_hi:[1,0,0]
	v_fma_mix_f32 v141, v127, v127, v141 op_sel:[1,1,0] op_sel_hi:[1,1,0]
	s_waitcnt vmcnt(10)
	v_cvt_f32_f16_e32 v72, v220
	v_cvt_f32_f16_sdwa v73, v220 dst_sel:DWORD dst_unused:UNUSED_PAD src0_sel:WORD_1
	v_cvt_f32_f16_e32 v74, v221
	v_cvt_f32_f16_sdwa v75, v221 dst_sel:DWORD dst_unused:UNUSED_PAD src0_sel:WORD_1
	v_cvt_f32_f16_e32 v80, v222
	v_cvt_f32_f16_sdwa v81, v222 dst_sel:DWORD dst_unused:UNUSED_PAD src0_sel:WORD_1
	v_cvt_f32_f16_e32 v82, v223
	v_cvt_f32_f16_sdwa v83, v223 dst_sel:DWORD dst_unused:UNUSED_PAD src0_sel:WORD_1
	v_sub_f32_e32 v72, v72, v192
	v_sub_f32_e32 v73, v73, v192
	v_sub_f32_e32 v74, v74, v192
	v_sub_f32_e32 v75, v75, v192
	v_sub_f32_e32 v80, v80, v192
	v_sub_f32_e32 v81, v81, v192
	v_sub_f32_e32 v82, v82, v192
	v_sub_f32_e32 v83, v83, v192
	v_pk_mul_f32 v[72:73], v[192:193], v[72:73] op_sel:[1,0]
	v_pk_mul_f32 v[74:75], v[192:193], v[74:75] op_sel:[1,0]
	v_pk_mul_f32 v[80:81], v[192:193], v[80:81] op_sel:[1,0]
	v_pk_mul_f32 v[82:83], v[192:193], v[82:83] op_sel:[1,0]
	v_pk_fma_f32 v[116:117], v[72:73], v[168:169], v[116:117]
	v_pk_fma_f32 v[118:119], v[74:75], v[170:171], v[118:119]
	v_pk_fma_f32 v[112:113], v[80:81], v[172:173], v[112:113]
	v_pk_fma_f32 v[114:115], v[82:83], v[174:175], v[114:115]
	v_cvt_pk_f16_f32 v116, v116, v117
	v_cvt_pk_f16_f32 v117, v118, v119
	v_cvt_pk_f16_f32 v118, v112, v113
	v_cvt_pk_f16_f32 v119, v114, v115
	ds_write_b128 v235, v[116:119] offset:64
	v_fma_mix_f32 v140, v116, 1.0, v140 op_sel_hi:[1,0,0]
	v_fma_mix_f32 v141, v116, v116, v141 op_sel_hi:[1,1,0]
	v_fma_mix_f32 v140, v116, 1.0, v140 op_sel:[1,0,0] op_sel_hi:[1,0,0]
	v_fma_mix_f32 v141, v116, v116, v141 op_sel:[1,1,0] op_sel_hi:[1,1,0]
	v_fma_mix_f32 v140, v117, 1.0, v140 op_sel_hi:[1,0,0]
	v_fma_mix_f32 v141, v117, v117, v141 op_sel_hi:[1,1,0]
	v_fma_mix_f32 v140, v117, 1.0, v140 op_sel:[1,0,0] op_sel_hi:[1,0,0]
	v_fma_mix_f32 v141, v117, v117, v141 op_sel:[1,1,0] op_sel_hi:[1,1,0]
	v_fma_mix_f32 v140, v118, 1.0, v140 op_sel_hi:[1,0,0]
	v_fma_mix_f32 v141, v118, v118, v141 op_sel_hi:[1,1,0]
	v_fma_mix_f32 v140, v118, 1.0, v140 op_sel:[1,0,0] op_sel_hi:[1,0,0]
	v_fma_mix_f32 v141, v118, v118, v141 op_sel:[1,1,0] op_sel_hi:[1,1,0]
	v_fma_mix_f32 v140, v119, 1.0, v140 op_sel_hi:[1,0,0]
	v_fma_mix_f32 v141, v119, v119, v141 op_sel_hi:[1,1,0]
	v_fma_mix_f32 v140, v119, 1.0, v140 op_sel:[1,0,0] op_sel_hi:[1,0,0]
	v_fma_mix_f32 v141, v119, v119, v141 op_sel:[1,1,0] op_sel_hi:[1,1,0]
	ds_read_b128 v[208:211], v236
	ds_read_b128 v[128:131], v236 offset:1152
	s_add_u32 s94, s98, 0x3c000
	s_addc_u32 s95, s99, 0
	global_load_dwordx4 v[212:215], v191, s[94:95] offset:0 nt
	global_load_dwordx4 v[144:147], v191, s[94:95] offset:64 nt
	s_add_u32 s94, s98, 0x42000
	s_addc_u32 s95, s99, 0
	global_load_dwordx4 v[132:135], v191, s[94:95] offset:0 nt
	global_load_dwordx4 v[88:91], v191, s[94:95] offset:64 nt
	s_waitcnt vmcnt(13)
	v_cvt_f32_f16_e32 v72, v240
	v_cvt_f32_f16_sdwa v73, v240 dst_sel:DWORD dst_unused:UNUSED_PAD src0_sel:WORD_1
	v_cvt_f32_f16_e32 v74, v241
	v_cvt_f32_f16_sdwa v75, v241 dst_sel:DWORD dst_unused:UNUSED_PAD src0_sel:WORD_1
	v_cvt_f32_f16_e32 v80, v242
	v_cvt_f32_f16_sdwa v81, v242 dst_sel:DWORD dst_unused:UNUSED_PAD src0_sel:WORD_1
	v_cvt_f32_f16_e32 v82, v243
	v_cvt_f32_f16_sdwa v83, v243 dst_sel:DWORD dst_unused:UNUSED_PAD src0_sel:WORD_1
	v_sub_f32_e32 v72, v72, v194
	v_sub_f32_e32 v73, v73, v194
	v_sub_f32_e32 v74, v74, v194
	v_sub_f32_e32 v75, v75, v194
	v_sub_f32_e32 v80, v80, v194
	v_sub_f32_e32 v81, v81, v194
	v_sub_f32_e32 v82, v82, v194
	v_sub_f32_e32 v83, v83, v194
	v_pk_mul_f32 v[72:73], v[194:195], v[72:73] op_sel:[1,0]
	v_pk_mul_f32 v[74:75], v[194:195], v[74:75] op_sel:[1,0]
	v_pk_mul_f32 v[80:81], v[194:195], v[80:81] op_sel:[1,0]
	v_pk_mul_f32 v[82:83], v[194:195], v[82:83] op_sel:[1,0]
	v_pk_fma_f32 v[108:109], v[72:73], v[160:161], v[108:109]
	v_pk_fma_f32 v[110:111], v[74:75], v[162:163], v[110:111]
	v_pk_fma_f32 v[104:105], v[80:81], v[164:165], v[104:105]
	v_pk_fma_f32 v[106:107], v[82:83], v[166:167], v[106:107]
	v_cvt_pk_f16_f32 v108, v108, v109
	v_cvt_pk_f16_f32 v109, v110, v111
	v_cvt_pk_f16_f32 v110, v104, v105
	v_cvt_pk_f16_f32 v111, v106, v107
	s_waitcnt lgkmcnt(0)
	v_add_u32_e32 v83, 0x6000, v224
	buffer_store_dwordx4 v[208:211], v83, s[24:27], 0 offen nt
	v_add_u32_e32 v82, 0x9000, v224
	buffer_store_dwordx4 v[128:131], v82, s[24:27], 0 offen nt
	ds_write_b128 v235, v[108:111]
	v_fma_mix_f32 v142, v108, 1.0, 0 op_sel_hi:[1,0,0]
	v_fma_mix_f32 v143, v108, v108, 0 op_sel_hi:[1,1,0]
	v_fma_mix_f32 v142, v108, 1.0, v142 op_sel:[1,0,0] op_sel_hi:[1,0,0]
	v_fma_mix_f32 v143, v108, v108, v143 op_sel:[1,1,0] op_sel_hi:[1,1,0]
	v_fma_mix_f32 v142, v109, 1.0, v142 op_sel_hi:[1,0,0]
	v_fma_mix_f32 v143, v109, v109, v143 op_sel_hi:[1,1,0]
	v_fma_mix_f32 v142, v109, 1.0, v142 op_sel:[1,0,0] op_sel_hi:[1,0,0]
	v_fma_mix_f32 v143, v109, v109, v143 op_sel:[1,1,0] op_sel_hi:[1,1,0]
	v_fma_mix_f32 v142, v110, 1.0, v142 op_sel_hi:[1,0,0]
	v_fma_mix_f32 v143, v110, v110, v143 op_sel_hi:[1,1,0]
	v_fma_mix_f32 v142, v110, 1.0, v142 op_sel:[1,0,0] op_sel_hi:[1,0,0]
	v_fma_mix_f32 v143, v110, v110, v143 op_sel:[1,1,0] op_sel_hi:[1,1,0]
	v_fma_mix_f32 v142, v111, 1.0, v142 op_sel_hi:[1,0,0]
	v_fma_mix_f32 v143, v111, v111, v143 op_sel_hi:[1,1,0]
	v_fma_mix_f32 v142, v111, 1.0, v142 op_sel:[1,0,0] op_sel_hi:[1,0,0]
	v_fma_mix_f32 v143, v111, v111, v143 op_sel:[1,1,0] op_sel_hi:[1,1,0]
	s_waitcnt vmcnt(14)
	v_cvt_f32_f16_e32 v72, v244
	v_cvt_f32_f16_sdwa v73, v244 dst_sel:DWORD dst_unused:UNUSED_PAD src0_sel:WORD_1
	v_cvt_f32_f16_e32 v74, v245
	v_cvt_f32_f16_sdwa v75, v245 dst_sel:DWORD dst_unused:UNUSED_PAD src0_sel:WORD_1
	v_cvt_f32_f16_e32 v80, v246
	v_cvt_f32_f16_sdwa v81, v246 dst_sel:DWORD dst_unused:UNUSED_PAD src0_sel:WORD_1
	v_cvt_f32_f16_e32 v82, v247
	v_cvt_f32_f16_sdwa v83, v247 dst_sel:DWORD dst_unused:UNUSED_PAD src0_sel:WORD_1
	v_sub_f32_e32 v72, v72, v194
	v_sub_f32_e32 v73, v73, v194
	v_sub_f32_e32 v74, v74, v194
	v_sub_f32_e32 v75, v75, v194
	v_sub_f32_e32 v80, v80, v194
	v_sub_f32_e32 v81, v81, v194
	v_sub_f32_e32 v82, v82, v194
	v_sub_f32_e32 v83, v83, v194
	v_pk_mul_f32 v[72:73], v[194:195], v[72:73] op_sel:[1,0]
	v_pk_mul_f32 v[74:75], v[194:195], v[74:75] op_sel:[1,0]
	v_pk_mul_f32 v[80:81], v[194:195], v[80:81] op_sel:[1,0]
	v_pk_mul_f32 v[82:83], v[194:195], v[82:83] op_sel:[1,0]
	v_pk_fma_f32 v[100:101], v[72:73], v[168:169], v[100:101]
	v_pk_fma_f32 v[102:103], v[74:75], v[170:171], v[102:103]
	v_pk_fma_f32 v[96:97], v[80:81], v[172:173], v[96:97]
	v_pk_fma_f32 v[98:99], v[82:83], v[174:175], v[98:99]
	v_cvt_pk_f16_f32 v100, v100, v101
	v_cvt_pk_f16_f32 v101, v102, v103
	v_cvt_pk_f16_f32 v102, v96, v97
	v_cvt_pk_f16_f32 v103, v98, v99
	ds_write_b128 v235, v[100:103] offset:64
	v_fma_mix_f32 v142, v100, 1.0, v142 op_sel_hi:[1,0,0]
	v_fma_mix_f32 v143, v100, v100, v143 op_sel_hi:[1,1,0]
	v_fma_mix_f32 v142, v100, 1.0, v142 op_sel:[1,0,0] op_sel_hi:[1,0,0]
	v_fma_mix_f32 v143, v100, v100, v143 op_sel:[1,1,0] op_sel_hi:[1,1,0]
	v_fma_mix_f32 v142, v101, 1.0, v142 op_sel_hi:[1,0,0]
	v_fma_mix_f32 v143, v101, v101, v143 op_sel_hi:[1,1,0]
	v_fma_mix_f32 v142, v101, 1.0, v142 op_sel:[1,0,0] op_sel_hi:[1,0,0]
	v_fma_mix_f32 v143, v101, v101, v143 op_sel:[1,1,0] op_sel_hi:[1,1,0]
	v_fma_mix_f32 v142, v102, 1.0, v142 op_sel_hi:[1,0,0]
	v_fma_mix_f32 v143, v102, v102, v143 op_sel_hi:[1,1,0]
	v_fma_mix_f32 v142, v102, 1.0, v142 op_sel:[1,0,0] op_sel_hi:[1,0,0]
	v_fma_mix_f32 v143, v102, v102, v143 op_sel:[1,1,0] op_sel_hi:[1,1,0]
	v_fma_mix_f32 v142, v103, 1.0, v142 op_sel_hi:[1,0,0]
	v_fma_mix_f32 v143, v103, v103, v143 op_sel_hi:[1,1,0]
	v_fma_mix_f32 v142, v103, 1.0, v142 op_sel:[1,0,0] op_sel_hi:[1,0,0]
	v_fma_mix_f32 v143, v103, v103, v143 op_sel:[1,1,0] op_sel_hi:[1,1,0]
	ds_read_b128 v[92:95], v236
	ds_read_b128 v[120:123], v236 offset:1152
	s_waitcnt vmcnt(13)
	v_cvt_f32_f16_e32 v72, v248
	v_cvt_f32_f16_sdwa v73, v248 dst_sel:DWORD dst_unused:UNUSED_PAD src0_sel:WORD_1
	v_cvt_f32_f16_e32 v74, v249
	v_cvt_f32_f16_sdwa v75, v249 dst_sel:DWORD dst_unused:UNUSED_PAD src0_sel:WORD_1
	v_cvt_f32_f16_e32 v80, v250
	v_cvt_f32_f16_sdwa v81, v250 dst_sel:DWORD dst_unused:UNUSED_PAD src0_sel:WORD_1
	v_cvt_f32_f16_e32 v82, v251
	v_cvt_f32_f16_sdwa v83, v251 dst_sel:DWORD dst_unused:UNUSED_PAD src0_sel:WORD_1
	v_sub_f32_e32 v72, v72, v196
	v_sub_f32_e32 v73, v73, v196
	v_sub_f32_e32 v74, v74, v196
	v_sub_f32_e32 v75, v75, v196
	v_sub_f32_e32 v80, v80, v196
	v_sub_f32_e32 v81, v81, v196
	v_sub_f32_e32 v82, v82, v196
	v_sub_f32_e32 v83, v83, v196
	v_pk_mul_f32 v[72:73], v[196:197], v[72:73] op_sel:[1,0]
	v_pk_mul_f32 v[74:75], v[196:197], v[74:75] op_sel:[1,0]
	v_pk_mul_f32 v[80:81], v[196:197], v[80:81] op_sel:[1,0]
	v_pk_mul_f32 v[82:83], v[196:197], v[82:83] op_sel:[1,0]
	v_pk_fma_f32 v[84:85], v[72:73], v[160:161], v[84:85]
	v_pk_fma_f32 v[86:87], v[74:75], v[162:163], v[86:87]
	v_pk_fma_f32 v[76:77], v[80:81], v[164:165], v[76:77]
	v_pk_fma_f32 v[78:79], v[82:83], v[166:167], v[78:79]
	v_cvt_pk_f16_f32 v84, v84, v85
	v_cvt_pk_f16_f32 v85, v86, v87
	v_cvt_pk_f16_f32 v86, v76, v77
	v_cvt_pk_f16_f32 v87, v78, v79
	s_waitcnt lgkmcnt(0)
	v_add_u32_e32 v83, 0xc000, v224
	buffer_store_dwordx4 v[92:95], v83, s[24:27], 0 offen nt
	v_add_u32_e32 v82, 0xf000, v224
	buffer_store_dwordx4 v[120:123], v82, s[24:27], 0 offen nt
	ds_write_b128 v235, v[84:87]
	v_fma_mix_f32 v216, v84, 1.0, 0 op_sel_hi:[1,0,0]
	v_fma_mix_f32 v217, v84, v84, 0 op_sel_hi:[1,1,0]
	v_fma_mix_f32 v216, v84, 1.0, v216 op_sel:[1,0,0] op_sel_hi:[1,0,0]
	v_fma_mix_f32 v217, v84, v84, v217 op_sel:[1,1,0] op_sel_hi:[1,1,0]
	v_fma_mix_f32 v216, v85, 1.0, v216 op_sel_hi:[1,0,0]
	v_fma_mix_f32 v217, v85, v85, v217 op_sel_hi:[1,1,0]
	v_fma_mix_f32 v216, v85, 1.0, v216 op_sel:[1,0,0] op_sel_hi:[1,0,0]
	v_fma_mix_f32 v217, v85, v85, v217 op_sel:[1,1,0] op_sel_hi:[1,1,0]
	v_fma_mix_f32 v216, v86, 1.0, v216 op_sel_hi:[1,0,0]
	v_fma_mix_f32 v217, v86, v86, v217 op_sel_hi:[1,1,0]
	v_fma_mix_f32 v216, v86, 1.0, v216 op_sel:[1,0,0] op_sel_hi:[1,0,0]
	v_fma_mix_f32 v217, v86, v86, v217 op_sel:[1,1,0] op_sel_hi:[1,1,0]
	v_fma_mix_f32 v216, v87, 1.0, v216 op_sel_hi:[1,0,0]
	v_fma_mix_f32 v217, v87, v87, v217 op_sel_hi:[1,1,0]
	v_fma_mix_f32 v216, v87, 1.0, v216 op_sel:[1,0,0] op_sel_hi:[1,0,0]
	v_fma_mix_f32 v217, v87, v87, v217 op_sel:[1,1,0] op_sel_hi:[1,1,0]
	s_waitcnt vmcnt(14)
	v_cvt_f32_f16_e32 v72, v252
	v_cvt_f32_f16_sdwa v73, v252 dst_sel:DWORD dst_unused:UNUSED_PAD src0_sel:WORD_1
	v_cvt_f32_f16_e32 v74, v253
	v_cvt_f32_f16_sdwa v75, v253 dst_sel:DWORD dst_unused:UNUSED_PAD src0_sel:WORD_1
	v_cvt_f32_f16_e32 v80, v254
	v_cvt_f32_f16_sdwa v81, v254 dst_sel:DWORD dst_unused:UNUSED_PAD src0_sel:WORD_1
	v_cvt_f32_f16_e32 v82, v255
	v_cvt_f32_f16_sdwa v83, v255 dst_sel:DWORD dst_unused:UNUSED_PAD src0_sel:WORD_1
	v_sub_f32_e32 v72, v72, v196
	v_sub_f32_e32 v73, v73, v196
	v_sub_f32_e32 v74, v74, v196
	v_sub_f32_e32 v75, v75, v196
	v_sub_f32_e32 v80, v80, v196
	v_sub_f32_e32 v81, v81, v196
	v_sub_f32_e32 v82, v82, v196
	v_sub_f32_e32 v83, v83, v196
	v_pk_mul_f32 v[72:73], v[196:197], v[72:73] op_sel:[1,0]
	v_pk_mul_f32 v[74:75], v[196:197], v[74:75] op_sel:[1,0]
	v_pk_mul_f32 v[80:81], v[196:197], v[80:81] op_sel:[1,0]
	v_pk_mul_f32 v[82:83], v[196:197], v[82:83] op_sel:[1,0]
	v_pk_fma_f32 v[68:69], v[72:73], v[168:169], v[68:69]
	v_pk_fma_f32 v[70:71], v[74:75], v[170:171], v[70:71]
	v_pk_fma_f32 v[64:65], v[80:81], v[172:173], v[64:65]
	v_pk_fma_f32 v[66:67], v[82:83], v[174:175], v[66:67]
	v_cvt_pk_f16_f32 v68, v68, v69
	v_cvt_pk_f16_f32 v69, v70, v71
	v_cvt_pk_f16_f32 v70, v64, v65
	v_cvt_pk_f16_f32 v71, v66, v67
	ds_write_b128 v235, v[68:71] offset:64
	v_fma_mix_f32 v216, v68, 1.0, v216 op_sel_hi:[1,0,0]
	v_fma_mix_f32 v217, v68, v68, v217 op_sel_hi:[1,1,0]
	v_fma_mix_f32 v216, v68, 1.0, v216 op_sel:[1,0,0] op_sel_hi:[1,0,0]
	v_fma_mix_f32 v217, v68, v68, v217 op_sel:[1,1,0] op_sel_hi:[1,1,0]
	v_fma_mix_f32 v216, v69, 1.0, v216 op_sel_hi:[1,0,0]
	v_fma_mix_f32 v217, v69, v69, v217 op_sel_hi:[1,1,0]
	v_fma_mix_f32 v216, v69, 1.0, v216 op_sel:[1,0,0] op_sel_hi:[1,0,0]
	v_fma_mix_f32 v217, v69, v69, v217 op_sel:[1,1,0] op_sel_hi:[1,1,0]
	v_fma_mix_f32 v216, v70, 1.0, v216 op_sel_hi:[1,0,0]
	v_fma_mix_f32 v217, v70, v70, v217 op_sel_hi:[1,1,0]
	v_fma_mix_f32 v216, v70, 1.0, v216 op_sel:[1,0,0] op_sel_hi:[1,0,0]
	v_fma_mix_f32 v217, v70, v70, v217 op_sel:[1,1,0] op_sel_hi:[1,1,0]
	v_fma_mix_f32 v216, v71, 1.0, v216 op_sel_hi:[1,0,0]
	v_fma_mix_f32 v217, v71, v71, v217 op_sel_hi:[1,1,0]
	v_fma_mix_f32 v216, v71, 1.0, v216 op_sel:[1,0,0] op_sel_hi:[1,0,0]
	v_fma_mix_f32 v217, v71, v71, v217 op_sel:[1,1,0] op_sel_hi:[1,1,0]
	ds_read_b128 v[112:115], v236
	ds_read_b128 v[220:223], v236 offset:1152
	s_waitcnt vmcnt(13)
	v_cvt_f32_f16_e32 v72, v136
	v_cvt_f32_f16_sdwa v73, v136 dst_sel:DWORD dst_unused:UNUSED_PAD src0_sel:WORD_1
	v_cvt_f32_f16_e32 v74, v137
	v_cvt_f32_f16_sdwa v75, v137 dst_sel:DWORD dst_unused:UNUSED_PAD src0_sel:WORD_1
	v_cvt_f32_f16_e32 v80, v138
	v_cvt_f32_f16_sdwa v81, v138 dst_sel:DWORD dst_unused:UNUSED_PAD src0_sel:WORD_1
	v_cvt_f32_f16_e32 v82, v139
	v_cvt_f32_f16_sdwa v83, v139 dst_sel:DWORD dst_unused:UNUSED_PAD src0_sel:WORD_1
	v_sub_f32_e32 v72, v72, v198
	v_sub_f32_e32 v73, v73, v198
	v_sub_f32_e32 v74, v74, v198
	v_sub_f32_e32 v75, v75, v198
	v_sub_f32_e32 v80, v80, v198
	v_sub_f32_e32 v81, v81, v198
	v_sub_f32_e32 v82, v82, v198
	v_sub_f32_e32 v83, v83, v198
	v_pk_mul_f32 v[72:73], v[198:199], v[72:73] op_sel:[1,0]
	v_pk_mul_f32 v[74:75], v[198:199], v[74:75] op_sel:[1,0]
	v_pk_mul_f32 v[80:81], v[198:199], v[80:81] op_sel:[1,0]
	v_pk_mul_f32 v[82:83], v[198:199], v[82:83] op_sel:[1,0]
	v_pk_fma_f32 v[60:61], v[72:73], v[160:161], v[60:61]
	v_pk_fma_f32 v[62:63], v[74:75], v[162:163], v[62:63]
	v_pk_fma_f32 v[56:57], v[80:81], v[164:165], v[56:57]
	v_pk_fma_f32 v[58:59], v[82:83], v[166:167], v[58:59]
	v_cvt_pk_f16_f32 v60, v60, v61
	v_cvt_pk_f16_f32 v61, v62, v63
	v_cvt_pk_f16_f32 v62, v56, v57
	v_cvt_pk_f16_f32 v63, v58, v59
	s_waitcnt lgkmcnt(0)
	v_add_u32_e32 v83, 0x12000, v224
	buffer_store_dwordx4 v[112:115], v83, s[24:27], 0 offen nt
	v_add_u32_e32 v82, 0x15000, v224
	buffer_store_dwordx4 v[220:223], v82, s[24:27], 0 offen nt
	ds_write_b128 v235, v[60:63]
	v_fma_mix_f32 v218, v60, 1.0, 0 op_sel_hi:[1,0,0]
	v_fma_mix_f32 v219, v60, v60, 0 op_sel_hi:[1,1,0]
	v_fma_mix_f32 v218, v60, 1.0, v218 op_sel:[1,0,0] op_sel_hi:[1,0,0]
	v_fma_mix_f32 v219, v60, v60, v219 op_sel:[1,1,0] op_sel_hi:[1,1,0]
	v_fma_mix_f32 v218, v61, 1.0, v218 op_sel_hi:[1,0,0]
	v_fma_mix_f32 v219, v61, v61, v219 op_sel_hi:[1,1,0]
	v_fma_mix_f32 v218, v61, 1.0, v218 op_sel:[1,0,0] op_sel_hi:[1,0,0]
	v_fma_mix_f32 v219, v61, v61, v219 op_sel:[1,1,0] op_sel_hi:[1,1,0]
	v_fma_mix_f32 v218, v62, 1.0, v218 op_sel_hi:[1,0,0]
	v_fma_mix_f32 v219, v62, v62, v219 op_sel_hi:[1,1,0]
	v_fma_mix_f32 v218, v62, 1.0, v218 op_sel:[1,0,0] op_sel_hi:[1,0,0]
	v_fma_mix_f32 v219, v62, v62, v219 op_sel:[1,1,0] op_sel_hi:[1,1,0]
	v_fma_mix_f32 v218, v63, 1.0, v218 op_sel_hi:[1,0,0]
	v_fma_mix_f32 v219, v63, v63, v219 op_sel_hi:[1,1,0]
	v_fma_mix_f32 v218, v63, 1.0, v218 op_sel:[1,0,0] op_sel_hi:[1,0,0]
	v_fma_mix_f32 v219, v63, v63, v219 op_sel:[1,1,0] op_sel_hi:[1,1,0]
	s_waitcnt vmcnt(14)
	v_cvt_f32_f16_e32 v72, v148
	v_cvt_f32_f16_sdwa v73, v148 dst_sel:DWORD dst_unused:UNUSED_PAD src0_sel:WORD_1
	v_cvt_f32_f16_e32 v74, v149
	v_cvt_f32_f16_sdwa v75, v149 dst_sel:DWORD dst_unused:UNUSED_PAD src0_sel:WORD_1
	v_cvt_f32_f16_e32 v80, v150
	v_cvt_f32_f16_sdwa v81, v150 dst_sel:DWORD dst_unused:UNUSED_PAD src0_sel:WORD_1
	v_cvt_f32_f16_e32 v82, v151
	v_cvt_f32_f16_sdwa v83, v151 dst_sel:DWORD dst_unused:UNUSED_PAD src0_sel:WORD_1
	v_sub_f32_e32 v72, v72, v198
	v_sub_f32_e32 v73, v73, v198
	v_sub_f32_e32 v74, v74, v198
	v_sub_f32_e32 v75, v75, v198
	v_sub_f32_e32 v80, v80, v198
	v_sub_f32_e32 v81, v81, v198
	v_sub_f32_e32 v82, v82, v198
	v_sub_f32_e32 v83, v83, v198
	v_pk_mul_f32 v[72:73], v[198:199], v[72:73] op_sel:[1,0]
	v_pk_mul_f32 v[74:75], v[198:199], v[74:75] op_sel:[1,0]
	v_pk_mul_f32 v[80:81], v[198:199], v[80:81] op_sel:[1,0]
	v_pk_mul_f32 v[82:83], v[198:199], v[82:83] op_sel:[1,0]
	v_pk_fma_f32 v[52:53], v[72:73], v[168:169], v[52:53]
	v_pk_fma_f32 v[54:55], v[74:75], v[170:171], v[54:55]
	v_pk_fma_f32 v[48:49], v[80:81], v[172:173], v[48:49]
	v_pk_fma_f32 v[50:51], v[82:83], v[174:175], v[50:51]
	v_cvt_pk_f16_f32 v52, v52, v53
	v_cvt_pk_f16_f32 v53, v54, v55
	v_cvt_pk_f16_f32 v54, v48, v49
	v_cvt_pk_f16_f32 v55, v50, v51
	ds_write_b128 v235, v[52:55] offset:64
	v_fma_mix_f32 v218, v52, 1.0, v218 op_sel_hi:[1,0,0]
	v_fma_mix_f32 v219, v52, v52, v219 op_sel_hi:[1,1,0]
	v_fma_mix_f32 v218, v52, 1.0, v218 op_sel:[1,0,0] op_sel_hi:[1,0,0]
	v_fma_mix_f32 v219, v52, v52, v219 op_sel:[1,1,0] op_sel_hi:[1,1,0]
	v_fma_mix_f32 v218, v53, 1.0, v218 op_sel_hi:[1,0,0]
	v_fma_mix_f32 v219, v53, v53, v219 op_sel_hi:[1,1,0]
	v_fma_mix_f32 v218, v53, 1.0, v218 op_sel:[1,0,0] op_sel_hi:[1,0,0]
	v_fma_mix_f32 v219, v53, v53, v219 op_sel:[1,1,0] op_sel_hi:[1,1,0]
	v_fma_mix_f32 v218, v54, 1.0, v218 op_sel_hi:[1,0,0]
	v_fma_mix_f32 v219, v54, v54, v219 op_sel_hi:[1,1,0]
	v_fma_mix_f32 v218, v54, 1.0, v218 op_sel:[1,0,0] op_sel_hi:[1,0,0]
	v_fma_mix_f32 v219, v54, v54, v219 op_sel:[1,1,0] op_sel_hi:[1,1,0]
	v_fma_mix_f32 v218, v55, 1.0, v218 op_sel_hi:[1,0,0]
	v_fma_mix_f32 v219, v55, v55, v219 op_sel_hi:[1,1,0]
	v_fma_mix_f32 v218, v55, 1.0, v218 op_sel:[1,0,0] op_sel_hi:[1,0,0]
	v_fma_mix_f32 v219, v55, v55, v219 op_sel:[1,1,0] op_sel_hi:[1,1,0]
	ds_read_b128 v[124:127], v236
	ds_read_b128 v[116:119], v236 offset:1152
	s_waitcnt vmcnt(13)
	v_cvt_f32_f16_e32 v72, v152
	v_cvt_f32_f16_sdwa v73, v152 dst_sel:DWORD dst_unused:UNUSED_PAD src0_sel:WORD_1
	v_cvt_f32_f16_e32 v74, v153
	v_cvt_f32_f16_sdwa v75, v153 dst_sel:DWORD dst_unused:UNUSED_PAD src0_sel:WORD_1
	v_cvt_f32_f16_e32 v80, v154
	v_cvt_f32_f16_sdwa v81, v154 dst_sel:DWORD dst_unused:UNUSED_PAD src0_sel:WORD_1
	v_cvt_f32_f16_e32 v82, v155
	v_cvt_f32_f16_sdwa v83, v155 dst_sel:DWORD dst_unused:UNUSED_PAD src0_sel:WORD_1
	v_sub_f32_e32 v72, v72, v200
	v_sub_f32_e32 v73, v73, v200
	v_sub_f32_e32 v74, v74, v200
	v_sub_f32_e32 v75, v75, v200
	v_sub_f32_e32 v80, v80, v200
	v_sub_f32_e32 v81, v81, v200
	v_sub_f32_e32 v82, v82, v200
	v_sub_f32_e32 v83, v83, v200
	v_pk_mul_f32 v[72:73], v[200:201], v[72:73] op_sel:[1,0]
	v_pk_mul_f32 v[74:75], v[200:201], v[74:75] op_sel:[1,0]
	v_pk_mul_f32 v[80:81], v[200:201], v[80:81] op_sel:[1,0]
	v_pk_mul_f32 v[82:83], v[200:201], v[82:83] op_sel:[1,0]
	v_pk_fma_f32 v[44:45], v[72:73], v[160:161], v[44:45]
	v_pk_fma_f32 v[46:47], v[74:75], v[162:163], v[46:47]
	v_pk_fma_f32 v[40:41], v[80:81], v[164:165], v[40:41]
	v_pk_fma_f32 v[42:43], v[82:83], v[166:167], v[42:43]
	v_cvt_pk_f16_f32 v44, v44, v45
	v_cvt_pk_f16_f32 v45, v46, v47
	v_cvt_pk_f16_f32 v46, v40, v41
	v_cvt_pk_f16_f32 v47, v42, v43
	s_waitcnt lgkmcnt(0)
	v_add_u32_e32 v83, 0x30000, v224
	buffer_store_dwordx4 v[124:127], v83, s[24:27], 0 offen nt
	v_add_u32_e32 v82, 0x33000, v224
	buffer_store_dwordx4 v[116:119], v82, s[24:27], 0 offen nt
	ds_write_b128 v235, v[44:47]
	v_fma_mix_f32 v208, v44, 1.0, 0 op_sel_hi:[1,0,0]
	v_fma_mix_f32 v209, v44, v44, 0 op_sel_hi:[1,1,0]
	v_fma_mix_f32 v208, v44, 1.0, v208 op_sel:[1,0,0] op_sel_hi:[1,0,0]
	v_fma_mix_f32 v209, v44, v44, v209 op_sel:[1,1,0] op_sel_hi:[1,1,0]
	v_fma_mix_f32 v208, v45, 1.0, v208 op_sel_hi:[1,0,0]
	v_fma_mix_f32 v209, v45, v45, v209 op_sel_hi:[1,1,0]
	v_fma_mix_f32 v208, v45, 1.0, v208 op_sel:[1,0,0] op_sel_hi:[1,0,0]
	v_fma_mix_f32 v209, v45, v45, v209 op_sel:[1,1,0] op_sel_hi:[1,1,0]
	v_fma_mix_f32 v208, v46, 1.0, v208 op_sel_hi:[1,0,0]
	v_fma_mix_f32 v209, v46, v46, v209 op_sel_hi:[1,1,0]
	v_fma_mix_f32 v208, v46, 1.0, v208 op_sel:[1,0,0] op_sel_hi:[1,0,0]
	v_fma_mix_f32 v209, v46, v46, v209 op_sel:[1,1,0] op_sel_hi:[1,1,0]
	v_fma_mix_f32 v208, v47, 1.0, v208 op_sel_hi:[1,0,0]
	v_fma_mix_f32 v209, v47, v47, v209 op_sel_hi:[1,1,0]
	v_fma_mix_f32 v208, v47, 1.0, v208 op_sel:[1,0,0] op_sel_hi:[1,0,0]
	v_fma_mix_f32 v209, v47, v47, v209 op_sel:[1,1,0] op_sel_hi:[1,1,0]
	s_waitcnt vmcnt(14)
	v_cvt_f32_f16_e32 v72, v156
	v_cvt_f32_f16_sdwa v73, v156 dst_sel:DWORD dst_unused:UNUSED_PAD src0_sel:WORD_1
	v_cvt_f32_f16_e32 v74, v157
	v_cvt_f32_f16_sdwa v75, v157 dst_sel:DWORD dst_unused:UNUSED_PAD src0_sel:WORD_1
	v_cvt_f32_f16_e32 v80, v158
	v_cvt_f32_f16_sdwa v81, v158 dst_sel:DWORD dst_unused:UNUSED_PAD src0_sel:WORD_1
	v_cvt_f32_f16_e32 v82, v159
	v_cvt_f32_f16_sdwa v83, v159 dst_sel:DWORD dst_unused:UNUSED_PAD src0_sel:WORD_1
	v_sub_f32_e32 v72, v72, v200
	v_sub_f32_e32 v73, v73, v200
	v_sub_f32_e32 v74, v74, v200
	v_sub_f32_e32 v75, v75, v200
	v_sub_f32_e32 v80, v80, v200
	v_sub_f32_e32 v81, v81, v200
	v_sub_f32_e32 v82, v82, v200
	v_sub_f32_e32 v83, v83, v200
	v_pk_mul_f32 v[72:73], v[200:201], v[72:73] op_sel:[1,0]
	v_pk_mul_f32 v[74:75], v[200:201], v[74:75] op_sel:[1,0]
	v_pk_mul_f32 v[80:81], v[200:201], v[80:81] op_sel:[1,0]
	v_pk_mul_f32 v[82:83], v[200:201], v[82:83] op_sel:[1,0]
	v_pk_fma_f32 v[36:37], v[72:73], v[168:169], v[36:37]
	v_pk_fma_f32 v[38:39], v[74:75], v[170:171], v[38:39]
	v_pk_fma_f32 v[32:33], v[80:81], v[172:173], v[32:33]
	v_pk_fma_f32 v[34:35], v[82:83], v[174:175], v[34:35]
	v_cvt_pk_f16_f32 v36, v36, v37
	v_cvt_pk_f16_f32 v37, v38, v39
	v_cvt_pk_f16_f32 v38, v32, v33
	v_cvt_pk_f16_f32 v39, v34, v35
	ds_write_b128 v235, v[36:39] offset:64
	v_fma_mix_f32 v208, v36, 1.0, v208 op_sel_hi:[1,0,0]
	v_fma_mix_f32 v209, v36, v36, v209 op_sel_hi:[1,1,0]
	v_fma_mix_f32 v208, v36, 1.0, v208 op_sel:[1,0,0] op_sel_hi:[1,0,0]
	v_fma_mix_f32 v209, v36, v36, v209 op_sel:[1,1,0] op_sel_hi:[1,1,0]
	v_fma_mix_f32 v208, v37, 1.0, v208 op_sel_hi:[1,0,0]
	v_fma_mix_f32 v209, v37, v37, v209 op_sel_hi:[1,1,0]
	v_fma_mix_f32 v208, v37, 1.0, v208 op_sel:[1,0,0] op_sel_hi:[1,0,0]
	v_fma_mix_f32 v209, v37, v37, v209 op_sel:[1,1,0] op_sel_hi:[1,1,0]
	v_fma_mix_f32 v208, v38, 1.0, v208 op_sel_hi:[1,0,0]
	v_fma_mix_f32 v209, v38, v38, v209 op_sel_hi:[1,1,0]
	v_fma_mix_f32 v208, v38, 1.0, v208 op_sel:[1,0,0] op_sel_hi:[1,0,0]
	v_fma_mix_f32 v209, v38, v38, v209 op_sel:[1,1,0] op_sel_hi:[1,1,0]
	v_fma_mix_f32 v208, v39, 1.0, v208 op_sel_hi:[1,0,0]
	v_fma_mix_f32 v209, v39, v39, v209 op_sel_hi:[1,1,0]
	v_fma_mix_f32 v208, v39, 1.0, v208 op_sel:[1,0,0] op_sel_hi:[1,0,0]
	v_fma_mix_f32 v209, v39, v39, v209 op_sel:[1,1,0] op_sel_hi:[1,1,0]
	ds_read_b128 v[128:131], v236
	ds_read_b128 v[104:107], v236 offset:1152
	s_waitcnt vmcnt(11)
	v_cvt_f32_f16_e32 v72, v212
	v_cvt_f32_f16_sdwa v73, v212 dst_sel:DWORD dst_unused:UNUSED_PAD src0_sel:WORD_1
	v_cvt_f32_f16_e32 v74, v213
	v_cvt_f32_f16_sdwa v75, v213 dst_sel:DWORD dst_unused:UNUSED_PAD src0_sel:WORD_1
	v_cvt_f32_f16_e32 v80, v214
	v_cvt_f32_f16_sdwa v81, v214 dst_sel:DWORD dst_unused:UNUSED_PAD src0_sel:WORD_1
	v_cvt_f32_f16_e32 v82, v215
	v_cvt_f32_f16_sdwa v83, v215 dst_sel:DWORD dst_unused:UNUSED_PAD src0_sel:WORD_1
	v_sub_f32_e32 v72, v72, v202
	v_sub_f32_e32 v73, v73, v202
	v_sub_f32_e32 v74, v74, v202
	v_sub_f32_e32 v75, v75, v202
	v_sub_f32_e32 v80, v80, v202
	v_sub_f32_e32 v81, v81, v202
	v_sub_f32_e32 v82, v82, v202
	v_sub_f32_e32 v83, v83, v202
	v_pk_mul_f32 v[72:73], v[202:203], v[72:73] op_sel:[1,0]
	v_pk_mul_f32 v[74:75], v[202:203], v[74:75] op_sel:[1,0]
	v_pk_mul_f32 v[80:81], v[202:203], v[80:81] op_sel:[1,0]
	v_pk_mul_f32 v[82:83], v[202:203], v[82:83] op_sel:[1,0]
	v_pk_fma_f32 v[28:29], v[72:73], v[160:161], v[28:29]
	v_pk_fma_f32 v[30:31], v[74:75], v[162:163], v[30:31]
	v_pk_fma_f32 v[24:25], v[80:81], v[164:165], v[24:25]
	v_pk_fma_f32 v[26:27], v[82:83], v[166:167], v[26:27]
	v_cvt_pk_f16_f32 v28, v28, v29
	v_cvt_pk_f16_f32 v29, v30, v31
	v_cvt_pk_f16_f32 v30, v24, v25
	v_cvt_pk_f16_f32 v31, v26, v27
	s_waitcnt lgkmcnt(0)
	v_add_u32_e32 v83, 0x36000, v224
	buffer_store_dwordx4 v[128:131], v83, s[24:27], 0 offen nt
	v_add_u32_e32 v82, 0x39000, v224
	buffer_store_dwordx4 v[104:107], v82, s[24:27], 0 offen nt
	ds_write_b128 v235, v[28:31]
	v_fma_mix_f32 v210, v28, 1.0, 0 op_sel_hi:[1,0,0]
	v_fma_mix_f32 v211, v28, v28, 0 op_sel_hi:[1,1,0]
	v_fma_mix_f32 v210, v28, 1.0, v210 op_sel:[1,0,0] op_sel_hi:[1,0,0]
	v_fma_mix_f32 v211, v28, v28, v211 op_sel:[1,1,0] op_sel_hi:[1,1,0]
	v_fma_mix_f32 v210, v29, 1.0, v210 op_sel_hi:[1,0,0]
	v_fma_mix_f32 v211, v29, v29, v211 op_sel_hi:[1,1,0]
	v_fma_mix_f32 v210, v29, 1.0, v210 op_sel:[1,0,0] op_sel_hi:[1,0,0]
	v_fma_mix_f32 v211, v29, v29, v211 op_sel:[1,1,0] op_sel_hi:[1,1,0]
	v_fma_mix_f32 v210, v30, 1.0, v210 op_sel_hi:[1,0,0]
	v_fma_mix_f32 v211, v30, v30, v211 op_sel_hi:[1,1,0]
	v_fma_mix_f32 v210, v30, 1.0, v210 op_sel:[1,0,0] op_sel_hi:[1,0,0]
	v_fma_mix_f32 v211, v30, v30, v211 op_sel:[1,1,0] op_sel_hi:[1,1,0]
	v_fma_mix_f32 v210, v31, 1.0, v210 op_sel_hi:[1,0,0]
	v_fma_mix_f32 v211, v31, v31, v211 op_sel_hi:[1,1,0]
	v_fma_mix_f32 v210, v31, 1.0, v210 op_sel:[1,0,0] op_sel_hi:[1,0,0]
	v_fma_mix_f32 v211, v31, v31, v211 op_sel:[1,1,0] op_sel_hi:[1,1,0]
	s_waitcnt vmcnt(12)
	v_cvt_f32_f16_e32 v72, v144
	v_cvt_f32_f16_sdwa v73, v144 dst_sel:DWORD dst_unused:UNUSED_PAD src0_sel:WORD_1
	v_cvt_f32_f16_e32 v74, v145
	v_cvt_f32_f16_sdwa v75, v145 dst_sel:DWORD dst_unused:UNUSED_PAD src0_sel:WORD_1
	v_cvt_f32_f16_e32 v80, v146
	v_cvt_f32_f16_sdwa v81, v146 dst_sel:DWORD dst_unused:UNUSED_PAD src0_sel:WORD_1
	v_cvt_f32_f16_e32 v82, v147
	v_cvt_f32_f16_sdwa v83, v147 dst_sel:DWORD dst_unused:UNUSED_PAD src0_sel:WORD_1
	v_sub_f32_e32 v72, v72, v202
	v_sub_f32_e32 v73, v73, v202
	v_sub_f32_e32 v74, v74, v202
	v_sub_f32_e32 v75, v75, v202
	v_sub_f32_e32 v80, v80, v202
	v_sub_f32_e32 v81, v81, v202
	v_sub_f32_e32 v82, v82, v202
	v_sub_f32_e32 v83, v83, v202
	v_pk_mul_f32 v[72:73], v[202:203], v[72:73] op_sel:[1,0]
	v_pk_mul_f32 v[74:75], v[202:203], v[74:75] op_sel:[1,0]
	v_pk_mul_f32 v[80:81], v[202:203], v[80:81] op_sel:[1,0]
	v_pk_mul_f32 v[82:83], v[202:203], v[82:83] op_sel:[1,0]
	v_pk_fma_f32 v[20:21], v[72:73], v[168:169], v[20:21]
	v_pk_fma_f32 v[22:23], v[74:75], v[170:171], v[22:23]
	v_pk_fma_f32 v[16:17], v[80:81], v[172:173], v[16:17]
	v_pk_fma_f32 v[18:19], v[82:83], v[174:175], v[18:19]
	v_cvt_pk_f16_f32 v20, v20, v21
	v_cvt_pk_f16_f32 v21, v22, v23
	v_cvt_pk_f16_f32 v22, v16, v17
	v_cvt_pk_f16_f32 v23, v18, v19
	ds_write_b128 v235, v[20:23] offset:64
	v_fma_mix_f32 v210, v20, 1.0, v210 op_sel_hi:[1,0,0]
	v_fma_mix_f32 v211, v20, v20, v211 op_sel_hi:[1,1,0]
	v_fma_mix_f32 v210, v20, 1.0, v210 op_sel:[1,0,0] op_sel_hi:[1,0,0]
	v_fma_mix_f32 v211, v20, v20, v211 op_sel:[1,1,0] op_sel_hi:[1,1,0]
	v_fma_mix_f32 v210, v21, 1.0, v210 op_sel_hi:[1,0,0]
	v_fma_mix_f32 v211, v21, v21, v211 op_sel_hi:[1,1,0]
	v_fma_mix_f32 v210, v21, 1.0, v210 op_sel:[1,0,0] op_sel_hi:[1,0,0]
	v_fma_mix_f32 v211, v21, v21, v211 op_sel:[1,1,0] op_sel_hi:[1,1,0]
	v_fma_mix_f32 v210, v22, 1.0, v210 op_sel_hi:[1,0,0]
	v_fma_mix_f32 v211, v22, v22, v211 op_sel_hi:[1,1,0]
	v_fma_mix_f32 v210, v22, 1.0, v210 op_sel:[1,0,0] op_sel_hi:[1,0,0]
	v_fma_mix_f32 v211, v22, v22, v211 op_sel:[1,1,0] op_sel_hi:[1,1,0]
	v_fma_mix_f32 v210, v23, 1.0, v210 op_sel_hi:[1,0,0]
	v_fma_mix_f32 v211, v23, v23, v211 op_sel_hi:[1,1,0]
	v_fma_mix_f32 v210, v23, 1.0, v210 op_sel:[1,0,0] op_sel_hi:[1,0,0]
	v_fma_mix_f32 v211, v23, v23, v211 op_sel:[1,1,0] op_sel_hi:[1,1,0]
	ds_read_b128 v[240:243], v236
	ds_read_b128 v[96:99], v236 offset:1152
	s_waitcnt vmcnt(11)
	v_cvt_f32_f16_e32 v72, v132
	v_cvt_f32_f16_sdwa v73, v132 dst_sel:DWORD dst_unused:UNUSED_PAD src0_sel:WORD_1
	v_cvt_f32_f16_e32 v74, v133
	v_cvt_f32_f16_sdwa v75, v133 dst_sel:DWORD dst_unused:UNUSED_PAD src0_sel:WORD_1
	v_cvt_f32_f16_e32 v80, v134
	v_cvt_f32_f16_sdwa v81, v134 dst_sel:DWORD dst_unused:UNUSED_PAD src0_sel:WORD_1
	v_cvt_f32_f16_e32 v82, v135
	v_cvt_f32_f16_sdwa v83, v135 dst_sel:DWORD dst_unused:UNUSED_PAD src0_sel:WORD_1
	v_sub_f32_e32 v72, v72, v204
	v_sub_f32_e32 v73, v73, v204
	v_sub_f32_e32 v74, v74, v204
	v_sub_f32_e32 v75, v75, v204
	v_sub_f32_e32 v80, v80, v204
	v_sub_f32_e32 v81, v81, v204
	v_sub_f32_e32 v82, v82, v204
	v_sub_f32_e32 v83, v83, v204
	v_pk_mul_f32 v[72:73], v[204:205], v[72:73] op_sel:[1,0]
	v_pk_mul_f32 v[74:75], v[204:205], v[74:75] op_sel:[1,0]
	v_pk_mul_f32 v[80:81], v[204:205], v[80:81] op_sel:[1,0]
	v_pk_mul_f32 v[82:83], v[204:205], v[82:83] op_sel:[1,0]
	v_pk_fma_f32 v[12:13], v[72:73], v[160:161], v[12:13]
	v_pk_fma_f32 v[14:15], v[74:75], v[162:163], v[14:15]
	v_pk_fma_f32 v[8:9], v[80:81], v[164:165], v[8:9]
	v_pk_fma_f32 v[10:11], v[82:83], v[166:167], v[10:11]
	v_cvt_pk_f16_f32 v12, v12, v13
	v_cvt_pk_f16_f32 v13, v14, v15
	v_cvt_pk_f16_f32 v14, v8, v9
	v_cvt_pk_f16_f32 v15, v10, v11
	s_waitcnt lgkmcnt(0)
	v_add_u32_e32 v83, 0x3c000, v224
	buffer_store_dwordx4 v[240:243], v83, s[24:27], 0 offen nt
	v_add_u32_e32 v82, 0x3f000, v224
	buffer_store_dwordx4 v[96:99], v82, s[24:27], 0 offen nt
	ds_write_b128 v235, v[12:15]
	v_fma_mix_f32 v244, v12, 1.0, 0 op_sel_hi:[1,0,0]
	v_fma_mix_f32 v245, v12, v12, 0 op_sel_hi:[1,1,0]
	v_fma_mix_f32 v244, v12, 1.0, v244 op_sel:[1,0,0] op_sel_hi:[1,0,0]
	v_fma_mix_f32 v245, v12, v12, v245 op_sel:[1,1,0] op_sel_hi:[1,1,0]
	v_fma_mix_f32 v244, v13, 1.0, v244 op_sel_hi:[1,0,0]
	v_fma_mix_f32 v245, v13, v13, v245 op_sel_hi:[1,1,0]
	v_fma_mix_f32 v244, v13, 1.0, v244 op_sel:[1,0,0] op_sel_hi:[1,0,0]
	v_fma_mix_f32 v245, v13, v13, v245 op_sel:[1,1,0] op_sel_hi:[1,1,0]
	v_fma_mix_f32 v244, v14, 1.0, v244 op_sel_hi:[1,0,0]
	v_fma_mix_f32 v245, v14, v14, v245 op_sel_hi:[1,1,0]
	v_fma_mix_f32 v244, v14, 1.0, v244 op_sel:[1,0,0] op_sel_hi:[1,0,0]
	v_fma_mix_f32 v245, v14, v14, v245 op_sel:[1,1,0] op_sel_hi:[1,1,0]
	v_fma_mix_f32 v244, v15, 1.0, v244 op_sel_hi:[1,0,0]
	v_fma_mix_f32 v245, v15, v15, v245 op_sel_hi:[1,1,0]
	v_fma_mix_f32 v244, v15, 1.0, v244 op_sel:[1,0,0] op_sel_hi:[1,0,0]
	v_fma_mix_f32 v245, v15, v15, v245 op_sel:[1,1,0] op_sel_hi:[1,1,0]
	s_waitcnt vmcnt(12)
	v_cvt_f32_f16_e32 v72, v88
	v_cvt_f32_f16_sdwa v73, v88 dst_sel:DWORD dst_unused:UNUSED_PAD src0_sel:WORD_1
	v_cvt_f32_f16_e32 v74, v89
	v_cvt_f32_f16_sdwa v75, v89 dst_sel:DWORD dst_unused:UNUSED_PAD src0_sel:WORD_1
	v_cvt_f32_f16_e32 v80, v90
	v_cvt_f32_f16_sdwa v81, v90 dst_sel:DWORD dst_unused:UNUSED_PAD src0_sel:WORD_1
	v_cvt_f32_f16_e32 v82, v91
	v_cvt_f32_f16_sdwa v83, v91 dst_sel:DWORD dst_unused:UNUSED_PAD src0_sel:WORD_1
	v_sub_f32_e32 v72, v72, v204
	v_sub_f32_e32 v73, v73, v204
	v_sub_f32_e32 v74, v74, v204
	v_sub_f32_e32 v75, v75, v204
	v_sub_f32_e32 v80, v80, v204
	v_sub_f32_e32 v81, v81, v204
	v_sub_f32_e32 v82, v82, v204
	v_sub_f32_e32 v83, v83, v204
	v_pk_mul_f32 v[72:73], v[204:205], v[72:73] op_sel:[1,0]
	v_pk_mul_f32 v[74:75], v[204:205], v[74:75] op_sel:[1,0]
	v_pk_mul_f32 v[80:81], v[204:205], v[80:81] op_sel:[1,0]
	v_pk_mul_f32 v[82:83], v[204:205], v[82:83] op_sel:[1,0]
	v_pk_fma_f32 v[4:5], v[72:73], v[168:169], v[4:5]
	v_pk_fma_f32 v[6:7], v[74:75], v[170:171], v[6:7]
	v_pk_fma_f32 v[0:1], v[80:81], v[172:173], v[0:1]
	v_pk_fma_f32 v[2:3], v[82:83], v[174:175], v[2:3]
	v_cvt_pk_f16_f32 v4, v4, v5
	v_cvt_pk_f16_f32 v5, v6, v7
	v_cvt_pk_f16_f32 v6, v0, v1
	v_cvt_pk_f16_f32 v7, v2, v3
	ds_write_b128 v235, v[4:7] offset:64
	v_fma_mix_f32 v244, v4, 1.0, v244 op_sel_hi:[1,0,0]
	v_fma_mix_f32 v245, v4, v4, v245 op_sel_hi:[1,1,0]
	v_fma_mix_f32 v244, v4, 1.0, v244 op_sel:[1,0,0] op_sel_hi:[1,0,0]
	v_fma_mix_f32 v245, v4, v4, v245 op_sel:[1,1,0] op_sel_hi:[1,1,0]
	v_fma_mix_f32 v244, v5, 1.0, v244 op_sel_hi:[1,0,0]
	v_fma_mix_f32 v245, v5, v5, v245 op_sel_hi:[1,1,0]
	v_fma_mix_f32 v244, v5, 1.0, v244 op_sel:[1,0,0] op_sel_hi:[1,0,0]
	v_fma_mix_f32 v245, v5, v5, v245 op_sel:[1,1,0] op_sel_hi:[1,1,0]
	v_fma_mix_f32 v244, v6, 1.0, v244 op_sel_hi:[1,0,0]
	v_fma_mix_f32 v245, v6, v6, v245 op_sel_hi:[1,1,0]
	v_fma_mix_f32 v244, v6, 1.0, v244 op_sel:[1,0,0] op_sel_hi:[1,0,0]
	v_fma_mix_f32 v245, v6, v6, v245 op_sel:[1,1,0] op_sel_hi:[1,1,0]
	v_fma_mix_f32 v244, v7, 1.0, v244 op_sel_hi:[1,0,0]
	v_fma_mix_f32 v245, v7, v7, v245 op_sel_hi:[1,1,0]
	v_fma_mix_f32 v244, v7, 1.0, v244 op_sel:[1,0,0] op_sel_hi:[1,0,0]
	v_fma_mix_f32 v245, v7, v7, v245 op_sel:[1,1,0] op_sel_hi:[1,1,0]
	ds_read_b128 v[108:111], v236
	ds_read_b128 v[100:103], v236 offset:1152
	s_waitcnt lgkmcnt(0)
	v_add_u32_e32 v83, 0x42000, v224
	buffer_store_dwordx4 v[108:111], v83, s[24:27], 0 offen nt
	v_add_u32_e32 v82, 0x45000, v224
	buffer_store_dwordx4 v[100:103], v82, s[24:27], 0 offen nt
	v_xor_b32_e32 v225, 16, v234
	v_lshlrev_b32_e32 v225, 2, v225
	v_xor_b32_e32 v246, 32, v234
	v_lshlrev_b32_e32 v246, 2, v246
	ds_bpermute_b32 v92, v225, v206
	ds_bpermute_b32 v93, v225, v207
	ds_bpermute_b32 v94, v225, v140
	ds_bpermute_b32 v95, v225, v141
	ds_bpermute_b32 v120, v225, v142
	ds_bpermute_b32 v121, v225, v143
	ds_bpermute_b32 v122, v225, v216
	ds_bpermute_b32 v123, v225, v217
	s_waitcnt lgkmcnt(0)
	v_pk_add_f32 v[206:207], v[206:207], v[92:93]
	v_pk_add_f32 v[140:141], v[140:141], v[94:95]
	v_pk_add_f32 v[142:143], v[142:143], v[120:121]
	v_pk_add_f32 v[216:217], v[216:217], v[122:123]
	ds_bpermute_b32 v92, v225, v218
	ds_bpermute_b32 v93, v225, v219
	ds_bpermute_b32 v94, v225, v208
	ds_bpermute_b32 v95, v225, v209
	ds_bpermute_b32 v120, v225, v210
	ds_bpermute_b32 v121, v225, v211
	ds_bpermute_b32 v122, v225, v244
	ds_bpermute_b32 v123, v225, v245
	s_waitcnt lgkmcnt(0)
	v_pk_add_f32 v[218:219], v[218:219], v[92:93]
	v_pk_add_f32 v[208:209], v[208:209], v[94:95]
	v_pk_add_f32 v[210:211], v[210:211], v[120:121]
	v_pk_add_f32 v[244:245], v[244:245], v[122:123]
	ds_bpermute_b32 v92, v246, v206
	ds_bpermute_b32 v93, v246, v207
	ds_bpermute_b32 v94, v246, v140
	ds_bpermute_b32 v95, v246, v141
	ds_bpermute_b32 v120, v246, v142
	ds_bpermute_b32 v121, v246, v143
	ds_bpermute_b32 v122, v246, v216
	ds_bpermute_b32 v123, v246, v217
	s_waitcnt lgkmcnt(0)
	v_pk_add_f32 v[206:207], v[206:207], v[92:93]
	v_pk_add_f32 v[140:141], v[140:141], v[94:95]
	v_pk_add_f32 v[142:143], v[142:143], v[120:121]
	v_pk_add_f32 v[216:217], v[216:217], v[122:123]
	ds_bpermute_b32 v92, v246, v218
	ds_bpermute_b32 v93, v246, v219
	ds_bpermute_b32 v94, v246, v208
	ds_bpermute_b32 v95, v246, v209
	ds_bpermute_b32 v120, v246, v210
	ds_bpermute_b32 v121, v246, v211
	ds_bpermute_b32 v122, v246, v244
	ds_bpermute_b32 v123, v246, v245
	s_waitcnt lgkmcnt(0)
	v_pk_add_f32 v[218:219], v[218:219], v[92:93]
	v_pk_add_f32 v[208:209], v[208:209], v[94:95]
	v_pk_add_f32 v[210:211], v[210:211], v[120:121]
	v_pk_add_f32 v[244:245], v[244:245], v[122:123]
	s_mov_b64 exec, 0xffff
	global_store_dwordx2 v190, v[206:207], s[100:101] offset:0
	global_store_dwordx2 v190, v[140:141], s[100:101] offset:128
	global_store_dwordx2 v190, v[142:143], s[100:101] offset:256
	global_store_dwordx2 v190, v[216:217], s[100:101] offset:384
	global_store_dwordx2 v190, v[218:219], s[100:101] offset:1024
	global_store_dwordx2 v190, v[208:209], s[100:101] offset:1152
	global_store_dwordx2 v190, v[210:211], s[100:101] offset:1280
	global_store_dwordx2 v190, v[244:245], s[100:101] offset:1408
	s_mov_b64 exec, -1
	s_mov_b32 s83, s81
	s_mov_b32 s84, s82
	s_mov_b64 s[40:41], s[0:1]
	s_mov_b64 s[38:39], s[8:9]
	s_mov_b64 vcc, s[6:7]
	s_cbranch_vccz .LBB10_12
	s_waitcnt vmcnt(0)
	s_cmpk_gt_u32 s44, 0xff
	s_cbranch_scc1 .LBB10_31
	s_barrier
